# EpiResid epilogues of wout L0/L1 and dense-down: residual tile loads prefetched 4-8 rounds ahead into dead fragment regs with counted vmcnt (was load->vmcnt(0) per round)
# baseline (speedup 1.0000x reference)
; __device__ __forceinline__ unsigned pk4_fp8(float a, float b, float c, float d) { int w = 0; w = __builtin_amdgcn_cvt_pk_fp8_f32(a, b, w, false); w = __builtin_amdgcn_cvt_pk_fp8_f32(c, d, w, true); return (unsigned)w; }
; __device__ __forceinline__ u32x4 pack8(f32x4 v0, f32x4 v1) { u32x4 w; w.x = cvt_pk_bf16(v0[0], v0[1]); w.y = cvt_pk_bf16(v0[2], v0[3]); w.z = cvt_pk_bf16(v1[0], v1[1]); w.w = cvt_pk_bf16(v1[2], v1[3]); return w; }
; template <class T> __device__ __forceinline__ void est(T* p, T v) { if constexpr (MK_EPI_NT != 0) __builtin_nontemporal_store(v, p); else *p = v; }
; __device__ __forceinline__ void unpack8(u32x4 w, f32x4& v0, f32x4& v1) { v0 = (f32x4){bf_lo(w.x), bf_hi(w.x), bf_lo(w.y), bf_hi(w.y)}; v1 = (f32x4){bf_lo(w.z), bf_hi(w.z), bf_lo(w.w), bf_hi(w.w)}; }
;     __device__ __forceinline__ void operator()(AccT acc, const Unit& u, int wr, int wc, int fr, int fq) const {
;         const int row0 = u.pm * 256 + wr * 64 + fr, col0 = u.pn * 256 + wc * 32 + 8 * fq;
;         f32x4 gv[2][2];
; #pragma unroll
;         for (int bj = 0; bj < 2; ++bj) { gv[bj][0] = *(const f32x4*)(gain + col0 + bj * 128); gv[bj][1] = *(const f32x4*)(gain + col0 + bj * 128 + 4); }
; #pragma unroll
;         for (int ai = 0; ai < 2; ++ai)
; #pragma unroll
;             for (int m = 0; m < 4; ++m) { const int row = row0 + ai * 128 + m * 16; float sq = 0.f;
; #pragma unroll
;                 for (int bj = 0; bj < 2; ++bj) { const size_t o = (size_t)row * DM + col0 + bj * 128;
;                     f32x4 r0, r1; if constexpr (RIN16) unpack8(*(const u32x4*)((const bf16_t*)Xin + o), r0, r1); else { r0 = *(const f32x4*)((const float*)Xin + o); r1 = *(const f32x4*)((const float*)Xin + o + 4); }
;                     const f32x4 x0 = r0 + acc[ai][bj][m][0] * ascale, x1 = r1 + acc[ai][bj][m][1] * ascale;
;                     est((u32x4*)(Xout + o), (u32x4)pack8(x0, x1));
;                     const f32x4 y0 = x0 * gv[bj][0], y1 = x1 * gv[bj][1];
;                     if constexpr (F8OUT) est((u32x2*)((unsigned char*)XB + o), (u32x2)(u32x2){pk4_fp8(y0[0], y0[1], y0[2], y0[3]), pk4_fp8(y1[0], y1[1], y1[2], y1[3])});
;                     else est((u32x4*)((bf16_t*)XB + o), (u32x4)pack8(y0, y1));
;                     sq += sum8sq(x0, x1); }
;                 row_atomic(ss, row, sq, fq); }
.LBB0_983:
	v_lshl_add_u32 v164, s88, 8, v166
	v_lshl_or_b32 v162, s20, 8, v168
	v_ashrrev_i32_e32 v165, 31, v164
	v_ashrrev_i32_e32 v163, 31, v162
	v_lshlrev_b64 v[174:175], 11, v[164:165]
	v_readlane_b32 s36, v247, 3
	v_lshl_add_u64 v[182:183], v[174:175], 0, v[162:163]
	v_readlane_b32 s37, v247, 4
	v_lshl_add_u64 v[46:47], v[162:163], 2, s[24:25]
	global_load_dwordx4 v[58:61], v[46:47], off offset:16
	global_load_dwordx4 v[62:65], v[46:47], off
	global_load_dwordx4 v[42:45], v[46:47], off offset:528
	s_nop 0
	global_load_dwordx4 v[46:49], v[46:47], off offset:512
	v_lshl_add_u64 v[184:185], v[182:183], 2, s[36:37]
	v_mov_b32_e32 v188, v184
	v_mov_b32_e32 v189, v185
	global_load_dwordx4 v[196:199], v[188:189], off
	global_load_dwordx4 v[200:203], v[188:189], off offset:16
	global_load_dwordx4 v[204:207], v[188:189], off offset:512
	global_load_dwordx4 v[208:211], v[188:189], off offset:528
	s_mov_b64 s[100:101], 0x20000
	v_lshl_add_u64 v[188:189], v[188:189], 0, s[100:101]
	global_load_dwordx4 v[212:215], v[188:189], off
	global_load_dwordx4 v[216:219], v[188:189], off offset:16
	global_load_dwordx4 v[248:251], v[188:189], off offset:512
	global_load_dwordx4 v[252:255], v[188:189], off offset:528
	s_nop 0
	v_readlane_b32 s38, v247, 5
	v_readlane_b32 s39, v247, 6
	v_readlane_b32 s40, v247, 7
	v_readlane_b32 s41, v247, 8
	v_readlane_b32 s42, v247, 9
	v_readlane_b32 s43, v247, 10
	v_readlane_b32 s44, v247, 11
	v_readlane_b32 s45, v247, 12
	v_readlane_b32 s46, v247, 13
	v_readlane_b32 s47, v247, 14
	v_readlane_b32 s48, v247, 15
	v_readlane_b32 s49, v247, 16
	v_readlane_b32 s50, v247, 17
	v_readlane_b32 s51, v247, 18
	s_waitcnt vmcnt(0)
	s_nop 1
	v_mov_b32_e32 v174, v200
	v_mov_b32_e32 v175, v201
	v_mov_b32_e32 v176, v202
	v_mov_b32_e32 v177, v203
	v_mov_b32_e32 v178, v196
	v_mov_b32_e32 v179, v197
	v_mov_b32_e32 v180, v198
	v_mov_b32_e32 v181, v199
	s_mov_b64 s[100:101], 0x20000
	v_lshl_add_u64 v[188:189], v[188:189], 0, s[100:101]
	global_load_dwordx4 v[196:199], v[188:189], off
	global_load_dwordx4 v[200:203], v[188:189], off offset:16
	v_pk_add_f32 v[142:143], v[174:175], v[142:143]
	v_lshlrev_b64 v[174:175], 1, v[182:183]
	v_pk_add_f32 v[180:181], v[180:181], v[140:141]
	v_pk_add_f32 v[178:179], v[178:179], v[138:139]
	v_pk_add_f32 v[144:145], v[176:177], v[144:145]
	v_lshl_add_u64 v[176:177], s[30:31], 0, v[174:175]
	v_cvt_pk_bf16_f32 v138, v178, v179
	v_cvt_pk_bf16_f32 v139, v180, v181
	v_cvt_pk_bf16_f32 v140, v142, v143
	v_cvt_pk_bf16_f32 v141, v144, v145
	global_store_dwordx4 v[176:177], v[138:141], off
	v_lshl_add_u64 v[186:187], s[26:27], 0, v[174:175]
	v_pk_mul_f32 v[176:177], v[60:61], v[144:145]
	v_pk_mul_f32 v[138:139], v[62:63], v[178:179]
	v_pk_mul_f32 v[140:141], v[64:65], v[180:181]
	v_cvt_pk_bf16_f32 v138, v138, v139
	v_pk_mul_f32 v[182:183], v[58:59], v[142:143]
	v_cvt_pk_bf16_f32 v139, v140, v141
	v_or_b32_e32 v174, 0x100, v174
	v_cvt_pk_bf16_f32 v140, v182, v183
	v_cvt_pk_bf16_f32 v141, v176, v177
	global_store_dwordx4 v[186:187], v[138:141], off
	s_nop 1
	v_mul_f32_e32 v138, v179, v179
	v_mul_f32_e32 v139, v181, v181
	v_fmac_f32_e32 v138, v178, v178
	v_fmac_f32_e32 v139, v180, v180
	v_add_f32_e32 v138, v138, v139
	v_mul_f32_e32 v139, v143, v143
	v_fmac_f32_e32 v139, v142, v142
	v_add_f32_e32 v138, v139, v138
	v_mul_f32_e32 v139, v145, v145
	v_fmac_f32_e32 v139, v144, v144
	v_add_f32_e32 v173, v139, v138
	s_nop 0
	s_nop 0
	s_waitcnt vmcnt(8)
	s_nop 1
	v_mov_b32_e32 v138, v208
	v_mov_b32_e32 v139, v209
	v_mov_b32_e32 v140, v210
	v_mov_b32_e32 v141, v211
	v_mov_b32_e32 v142, v204
	v_mov_b32_e32 v143, v205
	v_mov_b32_e32 v144, v206
	v_mov_b32_e32 v145, v207
	global_load_dwordx4 v[204:207], v[188:189], off offset:512
	global_load_dwordx4 v[208:211], v[188:189], off offset:528
	v_pk_add_f32 v[138:139], v[130:131], v[138:139]
	v_pk_add_f32 v[136:137], v[136:137], v[144:145]
	v_pk_add_f32 v[134:135], v[134:135], v[142:143]
	v_lshl_add_u64 v[142:143], s[30:31], 0, v[174:175]
	v_cvt_pk_bf16_f32 v130, v134, v135
	v_cvt_pk_bf16_f32 v131, v136, v137
	v_pk_add_f32 v[140:141], v[132:133], v[140:141]
	v_cvt_pk_bf16_f32 v132, v138, v139
	v_lshl_add_u64 v[174:175], s[26:27], 0, v[174:175]
	v_cvt_pk_bf16_f32 v133, v140, v141
	global_store_dwordx4 v[142:143], v[130:133], off
	v_pk_mul_f32 v[142:143], v[44:45], v[140:141]
	v_pk_mul_f32 v[144:145], v[42:43], v[138:139]
	v_pk_mul_f32 v[130:131], v[46:47], v[134:135]
	v_pk_mul_f32 v[132:133], v[48:49], v[136:137]
	v_cvt_pk_bf16_f32 v130, v130, v131
	s_nop 0
	v_cvt_pk_bf16_f32 v131, v132, v133
	v_cvt_pk_bf16_f32 v132, v144, v145
	v_cvt_pk_bf16_f32 v133, v142, v143
	global_store_dwordx4 v[174:175], v[130:133], off
	s_nop 1
	v_mul_f32_e32 v130, v135, v135
	v_mul_f32_e32 v131, v137, v137
	v_fmac_f32_e32 v130, v134, v134
	v_fmac_f32_e32 v131, v136, v136
	v_add_f32_e32 v130, v130, v131
	v_mul_f32_e32 v131, v139, v139
	v_fmac_f32_e32 v131, v138, v138
	v_add_f32_e32 v130, v131, v130
	v_mul_f32_e32 v131, v141, v141
	v_fmac_f32_e32 v131, v140, v140
	v_and_b32_e32 v132, 64, v172
	v_add_f32_e32 v130, v131, v130
	v_xor_b32_e32 v131, 16, v172
	v_add_u32_e32 v133, 64, v132
	v_cmp_lt_i32_e32 vcc, v131, v133
	v_add_f32_e32 v130, v173, v130
	s_nop 0
	v_cndmask_b32_e32 v131, v172, v131, vcc
	v_lshlrev_b32_e32 v132, 2, v131
	ds_bpermute_b32 v131, v132, v130
	s_waitcnt lgkmcnt(0)
	v_add_f32_e32 v130, v130, v131
	v_xor_b32_e32 v131, 32, v172
	v_cmp_lt_i32_e32 vcc, v131, v133
	s_nop 1
	v_cndmask_b32_e32 v131, v172, v131, vcc
	v_lshlrev_b32_e32 v133, 2, v131
	ds_bpermute_b32 v131, v133, v130
	s_and_saveexec_b64 s[88:89], s[0:1]
	s_cbranch_execz .LBB0_985
	s_waitcnt lgkmcnt(0)
	v_add_f32_e32 v130, v130, v131
	v_mul_f32_e32 v130, 0x4b800000, v130
	v_trunc_f32_e32 v130, v130
	v_mul_f32_e32 v131, 0x2f800000, v130
	v_floor_f32_e32 v131, v131
	v_fmac_f32_e32 v130, 0xcf800000, v131
	v_cvt_u32_f32_e32 v130, v130
	v_cvt_u32_f32_e32 v131, v131
	v_lshl_add_u64 v[134:135], v[164:165], 3, s[6:7]
	global_atomic_add_x2 v[134:135], v[130:131], off
; __device__ __forceinline__ unsigned pk4_fp8(float a, float b, float c, float d) { int w = 0; w = __builtin_amdgcn_cvt_pk_fp8_f32(a, b, w, false); w = __builtin_amdgcn_cvt_pk_fp8_f32(c, d, w, true); return (unsigned)w; }
; __device__ __forceinline__ u32x4 pack8(f32x4 v0, f32x4 v1) { u32x4 w; w.x = cvt_pk_bf16(v0[0], v0[1]); w.y = cvt_pk_bf16(v0[2], v0[3]); w.z = cvt_pk_bf16(v1[0], v1[1]); w.w = cvt_pk_bf16(v1[2], v1[3]); return w; }
; template <class T> __device__ __forceinline__ void est(T* p, T v) { if constexpr (MK_EPI_NT != 0) __builtin_nontemporal_store(v, p); else *p = v; }
; __device__ __forceinline__ void unpack8(u32x4 w, f32x4& v0, f32x4& v1) { v0 = (f32x4){bf_lo(w.x), bf_hi(w.x), bf_lo(w.y), bf_hi(w.y)}; v1 = (f32x4){bf_lo(w.z), bf_hi(w.z), bf_lo(w.w), bf_hi(w.w)}; }
; __device__ __forceinline__ float sum8sq(f32x4 a, f32x4 b) { return (a[0] * a[0] + a[1] * a[1]) + (a[2] * a[2] + a[3] * a[3]) + (b[0] * b[0] + b[1] * b[1]) + (b[2] * b[2] + b[3] * b[3]); }
; __device__ __forceinline__ void row_atomic(ss_t* ss, int row, float sq, int fq) { sq += __shfl_xor(sq, 16); sq += __shfl_xor(sq, 32); if (fq == 0) atomicAdd(ss + row, ss_fix(sq)); }
;     __device__ __forceinline__ void operator()(AccT acc, const Unit& u, int wr, int wc, int fr, int fq) const {
;     ...
;             for (int m = 0; m < 4; ++m) { const int row = row0 + ai * 128 + m * 16; float sq = 0.f;
; #pragma unroll
;                 for (int bj = 0; bj < 2; ++bj) { const size_t o = (size_t)row * DM + col0 + bj * 128;
;                     f32x4 r0, r1; if constexpr (RIN16) unpack8(*(const u32x4*)((const bf16_t*)Xin + o), r0, r1); else { r0 = *(const f32x4*)((const float*)Xin + o); r1 = *(const f32x4*)((const float*)Xin + o + 4); }
;                     const f32x4 x0 = r0 + acc[ai][bj][m][0] * ascale, x1 = r1 + acc[ai][bj][m][1] * ascale;
;                     est((u32x4*)(Xout + o), (u32x4)pack8(x0, x1));
;                     const f32x4 y0 = x0 * gv[bj][0], y1 = x1 * gv[bj][1];
;                     if constexpr (F8OUT) est((u32x2*)((unsigned char*)XB + o), (u32x2)(u32x2){pk4_fp8(y0[0], y0[1], y0[2], y0[3]), pk4_fp8(y1[0], y1[1], y1[2], y1[3])});
;                     else est((u32x4*)((bf16_t*)XB + o), (u32x4)pack8(y0, y1));
;                     sq += sum8sq(x0, x1); }
;                 row_atomic(ss, row, sq, fq); }
.LBB0_985:
	s_or_b64 exec, exec, s[88:89]
	v_or_b32_e32 v130, 16, v164
	s_waitcnt lgkmcnt(0)
	v_ashrrev_i32_e32 v131, 31, v130
	v_lshlrev_b64 v[134:135], 11, v[130:131]
	v_readlane_b32 s36, v247, 3
	v_lshl_add_u64 v[142:143], v[134:135], 0, v[162:163]
	v_readlane_b32 s37, v247, 4
	v_readlane_b32 s38, v247, 5
	v_readlane_b32 s39, v247, 6
	v_lshl_add_u64 v[144:145], v[142:143], 2, s[36:37]
	s_nop 0
	s_nop 0
	v_readlane_b32 s40, v247, 7
	v_readlane_b32 s41, v247, 8
	v_readlane_b32 s42, v247, 9
	v_readlane_b32 s43, v247, 10
	v_readlane_b32 s44, v247, 11
	v_readlane_b32 s45, v247, 12
	v_readlane_b32 s46, v247, 13
	v_readlane_b32 s47, v247, 14
	v_readlane_b32 s48, v247, 15
	v_readlane_b32 s49, v247, 16
	v_readlane_b32 s50, v247, 17
	v_readlane_b32 s51, v247, 18
	s_waitcnt vmcnt(10)
	s_nop 1
	v_mov_b32_e32 v134, v216
	v_mov_b32_e32 v135, v217
	v_mov_b32_e32 v136, v218
	v_mov_b32_e32 v137, v219
	v_mov_b32_e32 v138, v212
	v_mov_b32_e32 v139, v213
	v_mov_b32_e32 v140, v214
	v_mov_b32_e32 v141, v215
	s_mov_b64 s[100:101], 0x20000
	v_lshl_add_u64 v[188:189], v[188:189], 0, s[100:101]
	global_load_dwordx4 v[212:215], v[188:189], off
	global_load_dwordx4 v[216:219], v[188:189], off offset:16
	v_pk_add_f32 v[134:135], v[122:123], v[134:135]
	v_lshlrev_b64 v[122:123], 1, v[142:143]
	s_nop 0
	v_pk_add_f32 v[128:129], v[128:129], v[140:141]
	v_pk_add_f32 v[138:139], v[126:127], v[138:139]
	v_pk_add_f32 v[136:137], v[124:125], v[136:137]
	v_lshl_add_u64 v[140:141], s[30:31], 0, v[122:123]
	v_cvt_pk_bf16_f32 v124, v138, v139
	v_cvt_pk_bf16_f32 v125, v128, v129
	v_cvt_pk_bf16_f32 v126, v134, v135
	v_cvt_pk_bf16_f32 v127, v136, v137
	global_store_dwordx4 v[140:141], v[124:127], off
	v_lshl_add_u64 v[174:175], s[26:27], 0, v[122:123]
	v_pk_mul_f32 v[140:141], v[60:61], v[136:137]
	v_pk_mul_f32 v[124:125], v[62:63], v[138:139]
	v_pk_mul_f32 v[126:127], v[64:65], v[128:129]
	v_cvt_pk_bf16_f32 v124, v124, v125
	v_pk_mul_f32 v[142:143], v[58:59], v[134:135]
	v_cvt_pk_bf16_f32 v125, v126, v127
	v_or_b32_e32 v122, 0x100, v122
	v_cvt_pk_bf16_f32 v126, v142, v143
	v_cvt_pk_bf16_f32 v127, v140, v141
	global_store_dwordx4 v[174:175], v[124:127], off
	s_nop 1
	v_mul_f32_e32 v124, v139, v139
	v_mul_f32_e32 v125, v129, v129
	v_fmac_f32_e32 v124, v138, v138
	v_fmac_f32_e32 v125, v128, v128
	v_add_f32_e32 v124, v124, v125
	v_mul_f32_e32 v125, v135, v135
	v_fmac_f32_e32 v125, v134, v134
	v_add_f32_e32 v124, v125, v124
	v_mul_f32_e32 v125, v137, v137
	v_fmac_f32_e32 v125, v136, v136
	v_add_f32_e32 v138, v125, v124
	s_nop 0
	s_nop 0
	v_lshl_add_u64 v[128:129], s[30:31], 0, v[122:123]
	v_lshl_add_u64 v[122:123], s[26:27], 0, v[122:123]
	s_waitcnt vmcnt(12)
	s_nop 1
	v_mov_b32_e32 v124, v252
	v_mov_b32_e32 v125, v253
	v_mov_b32_e32 v126, v254
	v_mov_b32_e32 v127, v255
	v_mov_b32_e32 v134, v248
	v_mov_b32_e32 v135, v249
	v_mov_b32_e32 v136, v250
	v_mov_b32_e32 v137, v251
	global_load_dwordx4 v[248:251], v[188:189], off offset:512
	global_load_dwordx4 v[252:255], v[188:189], off offset:528
	v_pk_add_f32 v[124:125], v[114:115], v[124:125]
	s_nop 0
	v_pk_add_f32 v[120:121], v[120:121], v[136:137]
	v_pk_add_f32 v[118:119], v[118:119], v[134:135]
	v_pk_add_f32 v[126:127], v[116:117], v[126:127]
	v_cvt_pk_bf16_f32 v114, v118, v119
	v_cvt_pk_bf16_f32 v115, v120, v121
	v_cvt_pk_bf16_f32 v116, v124, v125
	v_pk_mul_f32 v[134:135], v[42:43], v[124:125]
	v_cvt_pk_bf16_f32 v117, v126, v127
	global_store_dwordx4 v[128:129], v[114:117], off
	v_pk_mul_f32 v[128:129], v[44:45], v[126:127]
	s_nop 0
	v_pk_mul_f32 v[114:115], v[46:47], v[118:119]
	v_pk_mul_f32 v[116:117], v[48:49], v[120:121]
	v_cvt_pk_bf16_f32 v114, v114, v115
	s_nop 0
	v_cvt_pk_bf16_f32 v115, v116, v117
	v_cvt_pk_bf16_f32 v116, v134, v135
	v_cvt_pk_bf16_f32 v117, v128, v129
	global_store_dwordx4 v[122:123], v[114:117], off
	s_nop 1
	v_mul_f32_e32 v114, v119, v119
	v_mul_f32_e32 v115, v121, v121
	v_fmac_f32_e32 v114, v118, v118
	v_fmac_f32_e32 v115, v120, v120
	v_add_f32_e32 v114, v114, v115
	v_mul_f32_e32 v115, v125, v125
	v_fmac_f32_e32 v115, v124, v124
	v_add_f32_e32 v114, v115, v114
	v_mul_f32_e32 v115, v127, v127
	v_fmac_f32_e32 v115, v126, v126
	v_add_f32_e32 v114, v115, v114
	v_add_f32_e32 v114, v138, v114
	ds_bpermute_b32 v115, v132, v114
	s_waitcnt lgkmcnt(0)
	v_add_f32_e32 v114, v114, v115
	ds_bpermute_b32 v115, v133, v114
	s_and_saveexec_b64 s[88:89], s[0:1]
	s_cbranch_execz .LBB0_987
	s_waitcnt lgkmcnt(0)
	v_add_f32_e32 v114, v114, v115
	v_mul_f32_e32 v114, 0x4b800000, v114
	v_trunc_f32_e32 v114, v114
	v_mul_f32_e32 v115, 0x2f800000, v114
	v_floor_f32_e32 v115, v115
	v_fmac_f32_e32 v114, 0xcf800000, v115
	v_cvt_u32_f32_e32 v114, v114
	v_cvt_u32_f32_e32 v115, v115
	v_lshl_add_u64 v[116:117], v[130:131], 3, s[6:7]
	global_atomic_add_x2 v[116:117], v[114:115], off
; __device__ __forceinline__ unsigned pk4_fp8(float a, float b, float c, float d) { int w = 0; w = __builtin_amdgcn_cvt_pk_fp8_f32(a, b, w, false); w = __builtin_amdgcn_cvt_pk_fp8_f32(c, d, w, true); return (unsigned)w; }
; __device__ __forceinline__ u32x4 pack8(f32x4 v0, f32x4 v1) { u32x4 w; w.x = cvt_pk_bf16(v0[0], v0[1]); w.y = cvt_pk_bf16(v0[2], v0[3]); w.z = cvt_pk_bf16(v1[0], v1[1]); w.w = cvt_pk_bf16(v1[2], v1[3]); return w; }
; template <class T> __device__ __forceinline__ void est(T* p, T v) { if constexpr (MK_EPI_NT != 0) __builtin_nontemporal_store(v, p); else *p = v; }
; __device__ __forceinline__ void unpack8(u32x4 w, f32x4& v0, f32x4& v1) { v0 = (f32x4){bf_lo(w.x), bf_hi(w.x), bf_lo(w.y), bf_hi(w.y)}; v1 = (f32x4){bf_lo(w.z), bf_hi(w.z), bf_lo(w.w), bf_hi(w.w)}; }
; __device__ __forceinline__ float sum8sq(f32x4 a, f32x4 b) { return (a[0] * a[0] + a[1] * a[1]) + (a[2] * a[2] + a[3] * a[3]) + (b[0] * b[0] + b[1] * b[1]) + (b[2] * b[2] + b[3] * b[3]); }
; __device__ __forceinline__ void row_atomic(ss_t* ss, int row, float sq, int fq) { sq += __shfl_xor(sq, 16); sq += __shfl_xor(sq, 32); if (fq == 0) atomicAdd(ss + row, ss_fix(sq)); }
;     __device__ __forceinline__ void operator()(AccT acc, const Unit& u, int wr, int wc, int fr, int fq) const {
;     ...
;             for (int m = 0; m < 4; ++m) { const int row = row0 + ai * 128 + m * 16; float sq = 0.f;
; #pragma unroll
;                 for (int bj = 0; bj < 2; ++bj) { const size_t o = (size_t)row * DM + col0 + bj * 128;
;                     f32x4 r0, r1; if constexpr (RIN16) unpack8(*(const u32x4*)((const bf16_t*)Xin + o), r0, r1); else { r0 = *(const f32x4*)((const float*)Xin + o); r1 = *(const f32x4*)((const float*)Xin + o + 4); }
;                     const f32x4 x0 = r0 + acc[ai][bj][m][0] * ascale, x1 = r1 + acc[ai][bj][m][1] * ascale;
;                     est((u32x4*)(Xout + o), (u32x4)pack8(x0, x1));
;                     const f32x4 y0 = x0 * gv[bj][0], y1 = x1 * gv[bj][1];
;                     if constexpr (F8OUT) est((u32x2*)((unsigned char*)XB + o), (u32x2)(u32x2){pk4_fp8(y0[0], y0[1], y0[2], y0[3]), pk4_fp8(y1[0], y1[1], y1[2], y1[3])});
;                     else est((u32x4*)((bf16_t*)XB + o), (u32x4)pack8(y0, y1));
;                     sq += sum8sq(x0, x1); }
;                 row_atomic(ss, row, sq, fq); }
.LBB0_987:
	s_or_b64 exec, exec, s[88:89]
	v_or_b32_e32 v114, 32, v164
	s_waitcnt lgkmcnt(0)
	v_ashrrev_i32_e32 v115, 31, v114
	v_lshlrev_b64 v[116:117], 11, v[114:115]
	v_readlane_b32 s36, v247, 3
	v_lshl_add_u64 v[124:125], v[116:117], 0, v[162:163]
	v_readlane_b32 s37, v247, 4
	v_readlane_b32 s38, v247, 5
	v_readlane_b32 s39, v247, 6
	v_lshl_add_u64 v[126:127], v[124:125], 2, s[36:37]
	s_nop 0
	s_nop 0
	v_readlane_b32 s40, v247, 7
	v_readlane_b32 s41, v247, 8
	v_readlane_b32 s42, v247, 9
	v_readlane_b32 s43, v247, 10
	v_readlane_b32 s44, v247, 11
	v_readlane_b32 s45, v247, 12
	v_readlane_b32 s46, v247, 13
	v_readlane_b32 s47, v247, 14
	v_readlane_b32 s48, v247, 15
	v_readlane_b32 s49, v247, 16
	v_readlane_b32 s50, v247, 17
	v_readlane_b32 s51, v247, 18
	s_waitcnt vmcnt(14)
	s_nop 1
	v_mov_b32_e32 v116, v200
	v_mov_b32_e32 v117, v201
	v_mov_b32_e32 v118, v202
	v_mov_b32_e32 v119, v203
	v_mov_b32_e32 v120, v196
	v_mov_b32_e32 v121, v197
	v_mov_b32_e32 v122, v198
	v_mov_b32_e32 v123, v199
	s_mov_b64 s[100:101], 0xa0000
	v_lshl_add_u64 v[188:189], v[188:189], 0, s[100:101]
	global_load_dwordx4 v[196:199], v[188:189], off
	global_load_dwordx4 v[200:203], v[188:189], off offset:16
	v_pk_add_f32 v[116:117], v[106:107], v[116:117]
	v_lshlrev_b64 v[106:107], 1, v[124:125]
	s_nop 0
	v_pk_add_f32 v[112:113], v[112:113], v[122:123]
	v_pk_add_f32 v[120:121], v[110:111], v[120:121]
	v_pk_add_f32 v[118:119], v[108:109], v[118:119]
	v_lshl_add_u64 v[122:123], s[30:31], 0, v[106:107]
	v_cvt_pk_bf16_f32 v108, v120, v121
	v_cvt_pk_bf16_f32 v109, v112, v113
	v_cvt_pk_bf16_f32 v110, v116, v117
	v_cvt_pk_bf16_f32 v111, v118, v119
	global_store_dwordx4 v[122:123], v[108:111], off
	v_lshl_add_u64 v[128:129], s[26:27], 0, v[106:107]
	v_pk_mul_f32 v[122:123], v[60:61], v[118:119]
	v_pk_mul_f32 v[108:109], v[62:63], v[120:121]
	v_pk_mul_f32 v[110:111], v[64:65], v[112:113]
	v_cvt_pk_bf16_f32 v108, v108, v109
	v_pk_mul_f32 v[124:125], v[58:59], v[116:117]
	v_cvt_pk_bf16_f32 v109, v110, v111
	v_or_b32_e32 v106, 0x100, v106
	v_cvt_pk_bf16_f32 v110, v124, v125
	v_cvt_pk_bf16_f32 v111, v122, v123
	global_store_dwordx4 v[128:129], v[108:111], off
	s_nop 1
	v_mul_f32_e32 v108, v121, v121
	v_mul_f32_e32 v109, v113, v113
	v_fmac_f32_e32 v108, v120, v120
	v_fmac_f32_e32 v109, v112, v112
	v_add_f32_e32 v108, v108, v109
	v_mul_f32_e32 v109, v117, v117
	v_fmac_f32_e32 v109, v116, v116
	v_add_f32_e32 v108, v109, v108
	v_mul_f32_e32 v109, v119, v119
	v_fmac_f32_e32 v109, v118, v118
	v_add_f32_e32 v120, v109, v108
	s_nop 0
	s_nop 0
	v_lshl_add_u64 v[112:113], s[30:31], 0, v[106:107]
	v_lshl_add_u64 v[106:107], s[26:27], 0, v[106:107]
	s_waitcnt vmcnt(14)
	s_nop 1
	v_mov_b32_e32 v108, v208
	v_mov_b32_e32 v109, v209
	v_mov_b32_e32 v110, v210
	v_mov_b32_e32 v111, v211
	v_mov_b32_e32 v116, v204
	v_mov_b32_e32 v117, v205
	v_mov_b32_e32 v118, v206
	v_mov_b32_e32 v119, v207
	global_load_dwordx4 v[204:207], v[188:189], off offset:512
	global_load_dwordx4 v[208:211], v[188:189], off offset:528
	v_pk_add_f32 v[108:109], v[98:99], v[108:109]
	s_nop 0
	v_pk_add_f32 v[104:105], v[104:105], v[118:119]
	v_pk_add_f32 v[102:103], v[102:103], v[116:117]
	v_pk_add_f32 v[110:111], v[100:101], v[110:111]
	v_cvt_pk_bf16_f32 v98, v102, v103
	v_cvt_pk_bf16_f32 v99, v104, v105
	v_cvt_pk_bf16_f32 v100, v108, v109
	v_pk_mul_f32 v[116:117], v[42:43], v[108:109]
	v_cvt_pk_bf16_f32 v101, v110, v111
	global_store_dwordx4 v[112:113], v[98:101], off
	v_pk_mul_f32 v[112:113], v[44:45], v[110:111]
	s_nop 0
	v_pk_mul_f32 v[98:99], v[46:47], v[102:103]
	v_pk_mul_f32 v[100:101], v[48:49], v[104:105]
	v_cvt_pk_bf16_f32 v98, v98, v99
	s_nop 0
	v_cvt_pk_bf16_f32 v99, v100, v101
	v_cvt_pk_bf16_f32 v100, v116, v117
	v_cvt_pk_bf16_f32 v101, v112, v113
	global_store_dwordx4 v[106:107], v[98:101], off
	s_nop 1
	v_mul_f32_e32 v98, v103, v103
	v_mul_f32_e32 v99, v105, v105
	v_fmac_f32_e32 v98, v102, v102
	v_fmac_f32_e32 v99, v104, v104
	v_add_f32_e32 v98, v98, v99
	v_mul_f32_e32 v99, v109, v109
	v_fmac_f32_e32 v99, v108, v108
	v_add_f32_e32 v98, v99, v98
	v_mul_f32_e32 v99, v111, v111
	v_fmac_f32_e32 v99, v110, v110
	v_add_f32_e32 v98, v99, v98
	v_add_f32_e32 v98, v120, v98
	ds_bpermute_b32 v99, v132, v98
	s_waitcnt lgkmcnt(0)
	v_add_f32_e32 v98, v98, v99
	ds_bpermute_b32 v99, v133, v98
	s_and_saveexec_b64 s[88:89], s[0:1]
	s_cbranch_execz .LBB0_989
	s_waitcnt lgkmcnt(0)
	v_add_f32_e32 v98, v98, v99
	v_mul_f32_e32 v98, 0x4b800000, v98
	v_trunc_f32_e32 v98, v98
	v_mul_f32_e32 v99, 0x2f800000, v98
	v_floor_f32_e32 v99, v99
	v_fmac_f32_e32 v98, 0xcf800000, v99
	v_cvt_u32_f32_e32 v98, v98
	v_cvt_u32_f32_e32 v99, v99
	v_lshl_add_u64 v[100:101], v[114:115], 3, s[6:7]
	global_atomic_add_x2 v[100:101], v[98:99], off
; __device__ __forceinline__ unsigned pk4_fp8(float a, float b, float c, float d) { int w = 0; w = __builtin_amdgcn_cvt_pk_fp8_f32(a, b, w, false); w = __builtin_amdgcn_cvt_pk_fp8_f32(c, d, w, true); return (unsigned)w; }
; __device__ __forceinline__ u32x4 pack8(f32x4 v0, f32x4 v1) { u32x4 w; w.x = cvt_pk_bf16(v0[0], v0[1]); w.y = cvt_pk_bf16(v0[2], v0[3]); w.z = cvt_pk_bf16(v1[0], v1[1]); w.w = cvt_pk_bf16(v1[2], v1[3]); return w; }
; template <class T> __device__ __forceinline__ void est(T* p, T v) { if constexpr (MK_EPI_NT != 0) __builtin_nontemporal_store(v, p); else *p = v; }
; __device__ __forceinline__ void unpack8(u32x4 w, f32x4& v0, f32x4& v1) { v0 = (f32x4){bf_lo(w.x), bf_hi(w.x), bf_lo(w.y), bf_hi(w.y)}; v1 = (f32x4){bf_lo(w.z), bf_hi(w.z), bf_lo(w.w), bf_hi(w.w)}; }
; __device__ __forceinline__ float sum8sq(f32x4 a, f32x4 b) { return (a[0] * a[0] + a[1] * a[1]) + (a[2] * a[2] + a[3] * a[3]) + (b[0] * b[0] + b[1] * b[1]) + (b[2] * b[2] + b[3] * b[3]); }
; __device__ __forceinline__ void row_atomic(ss_t* ss, int row, float sq, int fq) { sq += __shfl_xor(sq, 16); sq += __shfl_xor(sq, 32); if (fq == 0) atomicAdd(ss + row, ss_fix(sq)); }
;     __device__ __forceinline__ void operator()(AccT acc, const Unit& u, int wr, int wc, int fr, int fq) const {
;     ...
;             for (int m = 0; m < 4; ++m) { const int row = row0 + ai * 128 + m * 16; float sq = 0.f;
; #pragma unroll
;                 for (int bj = 0; bj < 2; ++bj) { const size_t o = (size_t)row * DM + col0 + bj * 128;
;                     f32x4 r0, r1; if constexpr (RIN16) unpack8(*(const u32x4*)((const bf16_t*)Xin + o), r0, r1); else { r0 = *(const f32x4*)((const float*)Xin + o); r1 = *(const f32x4*)((const float*)Xin + o + 4); }
;                     const f32x4 x0 = r0 + acc[ai][bj][m][0] * ascale, x1 = r1 + acc[ai][bj][m][1] * ascale;
;                     est((u32x4*)(Xout + o), (u32x4)pack8(x0, x1));
;                     const f32x4 y0 = x0 * gv[bj][0], y1 = x1 * gv[bj][1];
;                     if constexpr (F8OUT) est((u32x2*)((unsigned char*)XB + o), (u32x2)(u32x2){pk4_fp8(y0[0], y0[1], y0[2], y0[3]), pk4_fp8(y1[0], y1[1], y1[2], y1[3])});
;                     else est((u32x4*)((bf16_t*)XB + o), (u32x4)pack8(y0, y1));
;                     sq += sum8sq(x0, x1); }
;                 row_atomic(ss, row, sq, fq); }
.LBB0_989:
	s_or_b64 exec, exec, s[88:89]
	v_or_b32_e32 v98, 48, v164
	s_waitcnt lgkmcnt(0)
	v_ashrrev_i32_e32 v99, 31, v98
	v_lshlrev_b64 v[100:101], 11, v[98:99]
	v_readlane_b32 s36, v247, 3
	v_lshl_add_u64 v[108:109], v[100:101], 0, v[162:163]
	v_readlane_b32 s37, v247, 4
	v_readlane_b32 s38, v247, 5
	v_readlane_b32 s39, v247, 6
	v_lshl_add_u64 v[110:111], v[108:109], 2, s[36:37]
	s_nop 0
	s_nop 0
	v_readlane_b32 s40, v247, 7
	v_readlane_b32 s41, v247, 8
	v_readlane_b32 s42, v247, 9
	v_readlane_b32 s43, v247, 10
	v_readlane_b32 s44, v247, 11
	v_readlane_b32 s45, v247, 12
	v_readlane_b32 s46, v247, 13
	v_readlane_b32 s47, v247, 14
	v_readlane_b32 s48, v247, 15
	v_readlane_b32 s49, v247, 16
	v_readlane_b32 s50, v247, 17
	v_readlane_b32 s51, v247, 18
	s_waitcnt vmcnt(14)
	s_nop 1
	v_mov_b32_e32 v100, v216
	v_mov_b32_e32 v101, v217
	v_mov_b32_e32 v102, v218
	v_mov_b32_e32 v103, v219
	v_mov_b32_e32 v104, v212
	v_mov_b32_e32 v105, v213
	v_mov_b32_e32 v106, v214
	v_mov_b32_e32 v107, v215
	s_mov_b64 s[100:101], 0x20000
	v_lshl_add_u64 v[188:189], v[188:189], 0, s[100:101]
	global_load_dwordx4 v[212:215], v[188:189], off
	global_load_dwordx4 v[216:219], v[188:189], off offset:16
	v_pk_add_f32 v[100:101], v[100:101], v[90:91]
	v_lshlrev_b64 v[90:91], 1, v[108:109]
	s_nop 0
	v_pk_add_f32 v[96:97], v[106:107], v[96:97]
	v_pk_add_f32 v[104:105], v[104:105], v[94:95]
	v_pk_add_f32 v[102:103], v[102:103], v[92:93]
	v_lshl_add_u64 v[106:107], s[30:31], 0, v[90:91]
	v_cvt_pk_bf16_f32 v92, v104, v105
	v_cvt_pk_bf16_f32 v93, v96, v97
	v_cvt_pk_bf16_f32 v94, v100, v101
	v_cvt_pk_bf16_f32 v95, v102, v103
	global_store_dwordx4 v[106:107], v[92:95], off
	v_lshl_add_u64 v[112:113], s[26:27], 0, v[90:91]
	v_pk_mul_f32 v[106:107], v[60:61], v[102:103]
	v_pk_mul_f32 v[92:93], v[62:63], v[104:105]
	v_pk_mul_f32 v[94:95], v[64:65], v[96:97]
	v_cvt_pk_bf16_f32 v92, v92, v93
	v_pk_mul_f32 v[108:109], v[58:59], v[100:101]
	v_cvt_pk_bf16_f32 v93, v94, v95
	v_or_b32_e32 v90, 0x100, v90
	v_cvt_pk_bf16_f32 v94, v108, v109
	v_cvt_pk_bf16_f32 v95, v106, v107
	global_store_dwordx4 v[112:113], v[92:95], off
	s_nop 1
	v_mul_f32_e32 v92, v105, v105
	v_mul_f32_e32 v93, v97, v97
	v_fmac_f32_e32 v92, v104, v104
	v_fmac_f32_e32 v93, v96, v96
	v_add_f32_e32 v92, v92, v93
	v_mul_f32_e32 v93, v101, v101
	v_fmac_f32_e32 v93, v100, v100
	v_add_f32_e32 v92, v93, v92
	v_mul_f32_e32 v93, v103, v103
	v_fmac_f32_e32 v93, v102, v102
	v_add_f32_e32 v104, v93, v92
	s_nop 0
	s_nop 0
	v_lshl_add_u64 v[96:97], s[30:31], 0, v[90:91]
	v_lshl_add_u64 v[90:91], s[26:27], 0, v[90:91]
	s_waitcnt vmcnt(14)
	s_nop 1
	v_mov_b32_e32 v92, v252
	v_mov_b32_e32 v93, v253
	v_mov_b32_e32 v94, v254
	v_mov_b32_e32 v95, v255
	v_mov_b32_e32 v100, v248
	v_mov_b32_e32 v101, v249
	v_mov_b32_e32 v102, v250
	v_mov_b32_e32 v103, v251
	global_load_dwordx4 v[248:251], v[188:189], off offset:512
	global_load_dwordx4 v[252:255], v[188:189], off offset:528
	v_pk_add_f32 v[92:93], v[82:83], v[92:93]
	s_nop 0
	v_pk_add_f32 v[88:89], v[88:89], v[102:103]
	v_pk_add_f32 v[86:87], v[86:87], v[100:101]
	v_pk_add_f32 v[94:95], v[84:85], v[94:95]
	v_cvt_pk_bf16_f32 v82, v86, v87
	v_cvt_pk_bf16_f32 v83, v88, v89
	v_cvt_pk_bf16_f32 v84, v92, v93
	v_pk_mul_f32 v[100:101], v[42:43], v[92:93]
	v_cvt_pk_bf16_f32 v85, v94, v95
	global_store_dwordx4 v[96:97], v[82:85], off
	v_pk_mul_f32 v[96:97], v[44:45], v[94:95]
	s_nop 0
	v_pk_mul_f32 v[82:83], v[46:47], v[86:87]
	v_pk_mul_f32 v[84:85], v[48:49], v[88:89]
	v_cvt_pk_bf16_f32 v82, v82, v83
	s_nop 0
	v_cvt_pk_bf16_f32 v83, v84, v85
	v_cvt_pk_bf16_f32 v84, v100, v101
	v_cvt_pk_bf16_f32 v85, v96, v97
	global_store_dwordx4 v[90:91], v[82:85], off
	s_nop 1
	v_mul_f32_e32 v82, v87, v87
	v_mul_f32_e32 v83, v89, v89
	v_fmac_f32_e32 v82, v86, v86
	v_fmac_f32_e32 v83, v88, v88
	v_add_f32_e32 v82, v82, v83
	v_mul_f32_e32 v83, v93, v93
	v_fmac_f32_e32 v83, v92, v92
	v_add_f32_e32 v82, v83, v82
	v_mul_f32_e32 v83, v95, v95
	v_fmac_f32_e32 v83, v94, v94
	v_add_f32_e32 v82, v83, v82
	v_add_f32_e32 v82, v104, v82
	ds_bpermute_b32 v83, v132, v82
	s_waitcnt lgkmcnt(0)
	v_add_f32_e32 v82, v82, v83
	ds_bpermute_b32 v83, v133, v82
	s_and_saveexec_b64 s[88:89], s[0:1]
	s_cbranch_execz .LBB0_991
	s_waitcnt lgkmcnt(0)
	v_add_f32_e32 v82, v82, v83
	v_mul_f32_e32 v82, 0x4b800000, v82
	v_trunc_f32_e32 v82, v82
	v_mul_f32_e32 v83, 0x2f800000, v82
	v_floor_f32_e32 v83, v83
	v_fmac_f32_e32 v82, 0xcf800000, v83
	v_cvt_u32_f32_e32 v82, v82
	v_cvt_u32_f32_e32 v83, v83
	v_lshl_add_u64 v[84:85], v[98:99], 3, s[6:7]
	global_atomic_add_x2 v[84:85], v[82:83], off
; __device__ __forceinline__ unsigned pk4_fp8(float a, float b, float c, float d) { int w = 0; w = __builtin_amdgcn_cvt_pk_fp8_f32(a, b, w, false); w = __builtin_amdgcn_cvt_pk_fp8_f32(c, d, w, true); return (unsigned)w; }
; __device__ __forceinline__ u32x4 pack8(f32x4 v0, f32x4 v1) { u32x4 w; w.x = cvt_pk_bf16(v0[0], v0[1]); w.y = cvt_pk_bf16(v0[2], v0[3]); w.z = cvt_pk_bf16(v1[0], v1[1]); w.w = cvt_pk_bf16(v1[2], v1[3]); return w; }
; template <class T> __device__ __forceinline__ void est(T* p, T v) { if constexpr (MK_EPI_NT != 0) __builtin_nontemporal_store(v, p); else *p = v; }
; __device__ __forceinline__ void unpack8(u32x4 w, f32x4& v0, f32x4& v1) { v0 = (f32x4){bf_lo(w.x), bf_hi(w.x), bf_lo(w.y), bf_hi(w.y)}; v1 = (f32x4){bf_lo(w.z), bf_hi(w.z), bf_lo(w.w), bf_hi(w.w)}; }
; __device__ __forceinline__ float sum8sq(f32x4 a, f32x4 b) { return (a[0] * a[0] + a[1] * a[1]) + (a[2] * a[2] + a[3] * a[3]) + (b[0] * b[0] + b[1] * b[1]) + (b[2] * b[2] + b[3] * b[3]); }
; __device__ __forceinline__ void row_atomic(ss_t* ss, int row, float sq, int fq) { sq += __shfl_xor(sq, 16); sq += __shfl_xor(sq, 32); if (fq == 0) atomicAdd(ss + row, ss_fix(sq)); }
;     __device__ __forceinline__ void operator()(AccT acc, const Unit& u, int wr, int wc, int fr, int fq) const {
;     ...
;             for (int m = 0; m < 4; ++m) { const int row = row0 + ai * 128 + m * 16; float sq = 0.f;
; #pragma unroll
;                 for (int bj = 0; bj < 2; ++bj) { const size_t o = (size_t)row * DM + col0 + bj * 128;
;                     f32x4 r0, r1; if constexpr (RIN16) unpack8(*(const u32x4*)((const bf16_t*)Xin + o), r0, r1); else { r0 = *(const f32x4*)((const float*)Xin + o); r1 = *(const f32x4*)((const float*)Xin + o + 4); }
;                     const f32x4 x0 = r0 + acc[ai][bj][m][0] * ascale, x1 = r1 + acc[ai][bj][m][1] * ascale;
;                     est((u32x4*)(Xout + o), (u32x4)pack8(x0, x1));
;                     const f32x4 y0 = x0 * gv[bj][0], y1 = x1 * gv[bj][1];
;                     if constexpr (F8OUT) est((u32x2*)((unsigned char*)XB + o), (u32x2)(u32x2){pk4_fp8(y0[0], y0[1], y0[2], y0[3]), pk4_fp8(y1[0], y1[1], y1[2], y1[3])});
;                     else est((u32x4*)((bf16_t*)XB + o), (u32x4)pack8(y0, y1));
;                     sq += sum8sq(x0, x1); }
;                 row_atomic(ss, row, sq, fq); }
.LBB0_991:
	s_or_b64 exec, exec, s[88:89]
	v_add_u32_e32 v82, 0x80, v164
	s_waitcnt lgkmcnt(0)
	v_ashrrev_i32_e32 v83, 31, v82
	v_lshlrev_b64 v[84:85], 11, v[82:83]
	v_readlane_b32 s36, v247, 3
	v_lshl_add_u64 v[92:93], v[84:85], 0, v[162:163]
	v_readlane_b32 s37, v247, 4
	v_readlane_b32 s38, v247, 5
	v_readlane_b32 s39, v247, 6
	v_lshl_add_u64 v[94:95], v[92:93], 2, s[36:37]
	s_nop 0
	s_nop 0
	v_readlane_b32 s40, v247, 7
	v_readlane_b32 s41, v247, 8
	v_readlane_b32 s42, v247, 9
	v_readlane_b32 s43, v247, 10
	v_readlane_b32 s44, v247, 11
	v_readlane_b32 s45, v247, 12
	v_readlane_b32 s46, v247, 13
	v_readlane_b32 s47, v247, 14
	v_readlane_b32 s48, v247, 15
	v_readlane_b32 s49, v247, 16
	v_readlane_b32 s50, v247, 17
	v_readlane_b32 s51, v247, 18
	s_waitcnt vmcnt(14)
	s_nop 1
	v_mov_b32_e32 v84, v200
	v_mov_b32_e32 v85, v201
	v_mov_b32_e32 v86, v202
	v_mov_b32_e32 v87, v203
	v_mov_b32_e32 v88, v196
	v_mov_b32_e32 v89, v197
	v_mov_b32_e32 v90, v198
	v_mov_b32_e32 v91, v199
	s_mov_b64 s[100:101], 0x20000
	v_lshl_add_u64 v[188:189], v[188:189], 0, s[100:101]
	global_load_dwordx4 v[196:199], v[188:189], off
	global_load_dwordx4 v[200:203], v[188:189], off offset:16
	v_pk_add_f32 v[84:85], v[74:75], v[84:85]
	v_lshlrev_b64 v[74:75], 1, v[92:93]
	s_nop 0
	v_pk_add_f32 v[80:81], v[80:81], v[90:91]
	v_pk_add_f32 v[88:89], v[78:79], v[88:89]
	v_pk_add_f32 v[86:87], v[76:77], v[86:87]
	v_lshl_add_u64 v[90:91], s[30:31], 0, v[74:75]
	v_cvt_pk_bf16_f32 v76, v88, v89
	v_cvt_pk_bf16_f32 v77, v80, v81
	v_cvt_pk_bf16_f32 v78, v84, v85
	v_cvt_pk_bf16_f32 v79, v86, v87
	global_store_dwordx4 v[90:91], v[76:79], off
	v_lshl_add_u64 v[96:97], s[26:27], 0, v[74:75]
	v_pk_mul_f32 v[90:91], v[60:61], v[86:87]
	v_pk_mul_f32 v[76:77], v[62:63], v[88:89]
	v_pk_mul_f32 v[78:79], v[64:65], v[80:81]
	v_cvt_pk_bf16_f32 v76, v76, v77
	v_pk_mul_f32 v[92:93], v[58:59], v[84:85]
	v_cvt_pk_bf16_f32 v77, v78, v79
	v_or_b32_e32 v74, 0x100, v74
	v_cvt_pk_bf16_f32 v78, v92, v93
	v_cvt_pk_bf16_f32 v79, v90, v91
	global_store_dwordx4 v[96:97], v[76:79], off
	s_nop 1
	v_mul_f32_e32 v76, v89, v89
	v_mul_f32_e32 v77, v81, v81
	v_fmac_f32_e32 v76, v88, v88
	v_fmac_f32_e32 v77, v80, v80
	v_add_f32_e32 v76, v76, v77
	v_mul_f32_e32 v77, v85, v85
	v_fmac_f32_e32 v77, v84, v84
	v_add_f32_e32 v76, v77, v76
	v_mul_f32_e32 v77, v87, v87
	v_fmac_f32_e32 v77, v86, v86
	v_add_f32_e32 v88, v77, v76
	s_nop 0
	s_nop 0
	v_lshl_add_u64 v[80:81], s[30:31], 0, v[74:75]
	v_lshl_add_u64 v[74:75], s[26:27], 0, v[74:75]
	s_waitcnt vmcnt(14)
	s_nop 1
	v_mov_b32_e32 v76, v208
	v_mov_b32_e32 v77, v209
	v_mov_b32_e32 v78, v210
	v_mov_b32_e32 v79, v211
	v_mov_b32_e32 v84, v204
	v_mov_b32_e32 v85, v205
	v_mov_b32_e32 v86, v206
	v_mov_b32_e32 v87, v207
	global_load_dwordx4 v[204:207], v[188:189], off offset:512
	global_load_dwordx4 v[208:211], v[188:189], off offset:528
	v_pk_add_f32 v[76:77], v[66:67], v[76:77]
	s_nop 0
	v_pk_add_f32 v[72:73], v[72:73], v[86:87]
	v_pk_add_f32 v[70:71], v[70:71], v[84:85]
	v_pk_add_f32 v[78:79], v[68:69], v[78:79]
	v_cvt_pk_bf16_f32 v66, v70, v71
	v_cvt_pk_bf16_f32 v67, v72, v73
	v_cvt_pk_bf16_f32 v68, v76, v77
	v_pk_mul_f32 v[84:85], v[42:43], v[76:77]
	v_cvt_pk_bf16_f32 v69, v78, v79
	global_store_dwordx4 v[80:81], v[66:69], off
	v_pk_mul_f32 v[80:81], v[44:45], v[78:79]
	s_nop 0
	v_pk_mul_f32 v[66:67], v[46:47], v[70:71]
	v_pk_mul_f32 v[68:69], v[48:49], v[72:73]
	v_cvt_pk_bf16_f32 v66, v66, v67
	s_nop 0
	v_cvt_pk_bf16_f32 v67, v68, v69
	v_cvt_pk_bf16_f32 v68, v84, v85
	v_cvt_pk_bf16_f32 v69, v80, v81
	global_store_dwordx4 v[74:75], v[66:69], off
	s_nop 1
	v_mul_f32_e32 v66, v71, v71
	v_mul_f32_e32 v67, v73, v73
	v_fmac_f32_e32 v66, v70, v70
	v_fmac_f32_e32 v67, v72, v72
	v_add_f32_e32 v66, v66, v67
	v_mul_f32_e32 v67, v77, v77
	v_fmac_f32_e32 v67, v76, v76
	v_add_f32_e32 v66, v67, v66
	v_mul_f32_e32 v67, v79, v79
	v_fmac_f32_e32 v67, v78, v78
	v_add_f32_e32 v66, v67, v66
	v_add_f32_e32 v66, v88, v66
	ds_bpermute_b32 v67, v132, v66
	s_waitcnt lgkmcnt(0)
	v_add_f32_e32 v66, v66, v67
	ds_bpermute_b32 v67, v133, v66
	s_and_saveexec_b64 s[88:89], s[0:1]
	s_cbranch_execz .LBB0_993
	s_waitcnt lgkmcnt(0)
	v_add_f32_e32 v66, v66, v67
	v_mul_f32_e32 v66, 0x4b800000, v66
	v_trunc_f32_e32 v66, v66
	v_mul_f32_e32 v67, 0x2f800000, v66
	v_floor_f32_e32 v67, v67
	v_fmac_f32_e32 v66, 0xcf800000, v67
	v_cvt_u32_f32_e32 v66, v66
	v_cvt_u32_f32_e32 v67, v67
	v_lshl_add_u64 v[68:69], v[82:83], 3, s[6:7]
	global_atomic_add_x2 v[68:69], v[66:67], off
; __device__ __forceinline__ unsigned pk4_fp8(float a, float b, float c, float d) { int w = 0; w = __builtin_amdgcn_cvt_pk_fp8_f32(a, b, w, false); w = __builtin_amdgcn_cvt_pk_fp8_f32(c, d, w, true); return (unsigned)w; }
; __device__ __forceinline__ u32x4 pack8(f32x4 v0, f32x4 v1) { u32x4 w; w.x = cvt_pk_bf16(v0[0], v0[1]); w.y = cvt_pk_bf16(v0[2], v0[3]); w.z = cvt_pk_bf16(v1[0], v1[1]); w.w = cvt_pk_bf16(v1[2], v1[3]); return w; }
; template <class T> __device__ __forceinline__ void est(T* p, T v) { if constexpr (MK_EPI_NT != 0) __builtin_nontemporal_store(v, p); else *p = v; }
; __device__ __forceinline__ void unpack8(u32x4 w, f32x4& v0, f32x4& v1) { v0 = (f32x4){bf_lo(w.x), bf_hi(w.x), bf_lo(w.y), bf_hi(w.y)}; v1 = (f32x4){bf_lo(w.z), bf_hi(w.z), bf_lo(w.w), bf_hi(w.w)}; }
; __device__ __forceinline__ float sum8sq(f32x4 a, f32x4 b) { return (a[0] * a[0] + a[1] * a[1]) + (a[2] * a[2] + a[3] * a[3]) + (b[0] * b[0] + b[1] * b[1]) + (b[2] * b[2] + b[3] * b[3]); }
; __device__ __forceinline__ void row_atomic(ss_t* ss, int row, float sq, int fq) { sq += __shfl_xor(sq, 16); sq += __shfl_xor(sq, 32); if (fq == 0) atomicAdd(ss + row, ss_fix(sq)); }
;     __device__ __forceinline__ void operator()(AccT acc, const Unit& u, int wr, int wc, int fr, int fq) const {
;     ...
;             for (int m = 0; m < 4; ++m) { const int row = row0 + ai * 128 + m * 16; float sq = 0.f;
; #pragma unroll
;                 for (int bj = 0; bj < 2; ++bj) { const size_t o = (size_t)row * DM + col0 + bj * 128;
;                     f32x4 r0, r1; if constexpr (RIN16) unpack8(*(const u32x4*)((const bf16_t*)Xin + o), r0, r1); else { r0 = *(const f32x4*)((const float*)Xin + o); r1 = *(const f32x4*)((const float*)Xin + o + 4); }
;                     const f32x4 x0 = r0 + acc[ai][bj][m][0] * ascale, x1 = r1 + acc[ai][bj][m][1] * ascale;
;                     est((u32x4*)(Xout + o), (u32x4)pack8(x0, x1));
;                     const f32x4 y0 = x0 * gv[bj][0], y1 = x1 * gv[bj][1];
;                     if constexpr (F8OUT) est((u32x2*)((unsigned char*)XB + o), (u32x2)(u32x2){pk4_fp8(y0[0], y0[1], y0[2], y0[3]), pk4_fp8(y1[0], y1[1], y1[2], y1[3])});
;                     else est((u32x4*)((bf16_t*)XB + o), (u32x4)pack8(y0, y1));
;                     sq += sum8sq(x0, x1); }
;                 row_atomic(ss, row, sq, fq); }
.LBB0_993:
	s_or_b64 exec, exec, s[88:89]
	v_add_u32_e32 v66, 0x90, v164
	s_waitcnt lgkmcnt(0)
	v_ashrrev_i32_e32 v67, 31, v66
	v_lshlrev_b64 v[68:69], 11, v[66:67]
	v_readlane_b32 s36, v247, 3
	v_lshl_add_u64 v[76:77], v[68:69], 0, v[162:163]
	v_readlane_b32 s37, v247, 4
	v_readlane_b32 s38, v247, 5
	v_readlane_b32 s39, v247, 6
	v_lshl_add_u64 v[78:79], v[76:77], 2, s[36:37]
	s_nop 0
	s_nop 0
	v_readlane_b32 s40, v247, 7
	v_readlane_b32 s41, v247, 8
	v_readlane_b32 s42, v247, 9
	v_readlane_b32 s43, v247, 10
	v_readlane_b32 s44, v247, 11
	v_readlane_b32 s45, v247, 12
	v_readlane_b32 s46, v247, 13
	v_readlane_b32 s47, v247, 14
	v_readlane_b32 s48, v247, 15
	v_readlane_b32 s49, v247, 16
	v_readlane_b32 s50, v247, 17
	v_readlane_b32 s51, v247, 18
	s_waitcnt vmcnt(14)
	s_nop 1
	v_mov_b32_e32 v68, v216
	v_mov_b32_e32 v69, v217
	v_mov_b32_e32 v70, v218
	v_mov_b32_e32 v71, v219
	v_mov_b32_e32 v72, v212
	v_mov_b32_e32 v73, v213
	v_mov_b32_e32 v74, v214
	v_mov_b32_e32 v75, v215
	s_mov_b64 s[100:101], 0x20000
	v_lshl_add_u64 v[188:189], v[188:189], 0, s[100:101]
	global_load_dwordx4 v[212:215], v[188:189], off
	global_load_dwordx4 v[216:219], v[188:189], off offset:16
	v_pk_add_f32 v[68:69], v[50:51], v[68:69]
	v_lshlrev_b64 v[50:51], 1, v[76:77]
	s_nop 0
	v_pk_add_f32 v[56:57], v[56:57], v[74:75]
	v_pk_add_f32 v[72:73], v[54:55], v[72:73]
	v_pk_add_f32 v[70:71], v[52:53], v[70:71]
	v_lshl_add_u64 v[74:75], s[30:31], 0, v[50:51]
	v_cvt_pk_bf16_f32 v52, v72, v73
	v_cvt_pk_bf16_f32 v53, v56, v57
	v_cvt_pk_bf16_f32 v54, v68, v69
	v_cvt_pk_bf16_f32 v55, v70, v71
	global_store_dwordx4 v[74:75], v[52:55], off
	v_lshl_add_u64 v[80:81], s[26:27], 0, v[50:51]
	v_pk_mul_f32 v[74:75], v[60:61], v[70:71]
	v_pk_mul_f32 v[52:53], v[62:63], v[72:73]
	v_pk_mul_f32 v[54:55], v[64:65], v[56:57]
	v_cvt_pk_bf16_f32 v52, v52, v53
	v_pk_mul_f32 v[76:77], v[58:59], v[68:69]
	v_cvt_pk_bf16_f32 v53, v54, v55
	v_or_b32_e32 v50, 0x100, v50
	v_cvt_pk_bf16_f32 v54, v76, v77
	v_cvt_pk_bf16_f32 v55, v74, v75
	global_store_dwordx4 v[80:81], v[52:55], off
	s_nop 1
	v_mul_f32_e32 v52, v73, v73
	v_mul_f32_e32 v53, v57, v57
	v_fmac_f32_e32 v52, v72, v72
	v_fmac_f32_e32 v53, v56, v56
	v_add_f32_e32 v52, v52, v53
	v_mul_f32_e32 v53, v69, v69
	v_fmac_f32_e32 v53, v68, v68
	v_add_f32_e32 v52, v53, v52
	v_mul_f32_e32 v53, v71, v71
	v_fmac_f32_e32 v53, v70, v70
	v_add_f32_e32 v72, v53, v52
	s_nop 0
	s_nop 0
	v_lshl_add_u64 v[56:57], s[30:31], 0, v[50:51]
	v_lshl_add_u64 v[50:51], s[26:27], 0, v[50:51]
	s_waitcnt vmcnt(14)
	s_nop 1
	v_mov_b32_e32 v52, v252
	v_mov_b32_e32 v53, v253
	v_mov_b32_e32 v54, v254
	v_mov_b32_e32 v55, v255
	v_mov_b32_e32 v68, v248
	v_mov_b32_e32 v69, v249
	v_mov_b32_e32 v70, v250
	v_mov_b32_e32 v71, v251
	global_load_dwordx4 v[248:251], v[188:189], off offset:512
	global_load_dwordx4 v[252:255], v[188:189], off offset:528
	v_pk_add_f32 v[52:53], v[34:35], v[52:53]
	s_nop 0
	v_pk_add_f32 v[40:41], v[40:41], v[70:71]
	v_pk_add_f32 v[38:39], v[38:39], v[68:69]
	v_pk_add_f32 v[54:55], v[36:37], v[54:55]
	v_cvt_pk_bf16_f32 v34, v38, v39
	v_cvt_pk_bf16_f32 v35, v40, v41
	v_cvt_pk_bf16_f32 v36, v52, v53
	v_pk_mul_f32 v[68:69], v[42:43], v[52:53]
	v_cvt_pk_bf16_f32 v37, v54, v55
	global_store_dwordx4 v[56:57], v[34:37], off
	v_pk_mul_f32 v[56:57], v[44:45], v[54:55]
	s_nop 0
	v_pk_mul_f32 v[34:35], v[46:47], v[38:39]
	v_pk_mul_f32 v[36:37], v[48:49], v[40:41]
	v_cvt_pk_bf16_f32 v34, v34, v35
	s_nop 0
	v_cvt_pk_bf16_f32 v35, v36, v37
	v_cvt_pk_bf16_f32 v36, v68, v69
	v_cvt_pk_bf16_f32 v37, v56, v57
	global_store_dwordx4 v[50:51], v[34:37], off
	s_nop 1
	v_mul_f32_e32 v34, v39, v39
	v_mul_f32_e32 v35, v41, v41
	v_fmac_f32_e32 v34, v38, v38
	v_fmac_f32_e32 v35, v40, v40
	v_add_f32_e32 v34, v34, v35
	v_mul_f32_e32 v35, v53, v53
	v_fmac_f32_e32 v35, v52, v52
	v_add_f32_e32 v34, v35, v34
	v_mul_f32_e32 v35, v55, v55
	v_fmac_f32_e32 v35, v54, v54
	v_add_f32_e32 v34, v35, v34
	v_add_f32_e32 v34, v72, v34
	ds_bpermute_b32 v35, v132, v34
	s_waitcnt lgkmcnt(0)
	v_add_f32_e32 v34, v34, v35
	ds_bpermute_b32 v35, v133, v34
	s_and_saveexec_b64 s[88:89], s[0:1]
	s_cbranch_execz .LBB0_995
	s_waitcnt lgkmcnt(0)
	v_add_f32_e32 v34, v34, v35
	v_mul_f32_e32 v34, 0x4b800000, v34
	v_trunc_f32_e32 v34, v34
	v_mul_f32_e32 v35, 0x2f800000, v34
	v_floor_f32_e32 v35, v35
	v_fmac_f32_e32 v34, 0xcf800000, v35
	v_cvt_u32_f32_e32 v34, v34
	v_cvt_u32_f32_e32 v35, v35
	v_lshl_add_u64 v[36:37], v[66:67], 3, s[6:7]
	global_atomic_add_x2 v[36:37], v[34:35], off
; __device__ __forceinline__ unsigned pk4_fp8(float a, float b, float c, float d) { int w = 0; w = __builtin_amdgcn_cvt_pk_fp8_f32(a, b, w, false); w = __builtin_amdgcn_cvt_pk_fp8_f32(c, d, w, true); return (unsigned)w; }
; __device__ __forceinline__ u32x4 pack8(f32x4 v0, f32x4 v1) { u32x4 w; w.x = cvt_pk_bf16(v0[0], v0[1]); w.y = cvt_pk_bf16(v0[2], v0[3]); w.z = cvt_pk_bf16(v1[0], v1[1]); w.w = cvt_pk_bf16(v1[2], v1[3]); return w; }
; template <class T> __device__ __forceinline__ void est(T* p, T v) { if constexpr (MK_EPI_NT != 0) __builtin_nontemporal_store(v, p); else *p = v; }
; __device__ __forceinline__ void unpack8(u32x4 w, f32x4& v0, f32x4& v1) { v0 = (f32x4){bf_lo(w.x), bf_hi(w.x), bf_lo(w.y), bf_hi(w.y)}; v1 = (f32x4){bf_lo(w.z), bf_hi(w.z), bf_lo(w.w), bf_hi(w.w)}; }
; __device__ __forceinline__ float sum8sq(f32x4 a, f32x4 b) { return (a[0] * a[0] + a[1] * a[1]) + (a[2] * a[2] + a[3] * a[3]) + (b[0] * b[0] + b[1] * b[1]) + (b[2] * b[2] + b[3] * b[3]); }
; __device__ __forceinline__ void row_atomic(ss_t* ss, int row, float sq, int fq) { sq += __shfl_xor(sq, 16); sq += __shfl_xor(sq, 32); if (fq == 0) atomicAdd(ss + row, ss_fix(sq)); }
;     __device__ __forceinline__ void operator()(AccT acc, const Unit& u, int wr, int wc, int fr, int fq) const {
;     ...
;             for (int m = 0; m < 4; ++m) { const int row = row0 + ai * 128 + m * 16; float sq = 0.f;
; #pragma unroll
;                 for (int bj = 0; bj < 2; ++bj) { const size_t o = (size_t)row * DM + col0 + bj * 128;
;                     f32x4 r0, r1; if constexpr (RIN16) unpack8(*(const u32x4*)((const bf16_t*)Xin + o), r0, r1); else { r0 = *(const f32x4*)((const float*)Xin + o); r1 = *(const f32x4*)((const float*)Xin + o + 4); }
;                     const f32x4 x0 = r0 + acc[ai][bj][m][0] * ascale, x1 = r1 + acc[ai][bj][m][1] * ascale;
;                     est((u32x4*)(Xout + o), (u32x4)pack8(x0, x1));
;                     const f32x4 y0 = x0 * gv[bj][0], y1 = x1 * gv[bj][1];
;                     if constexpr (F8OUT) est((u32x2*)((unsigned char*)XB + o), (u32x2)(u32x2){pk4_fp8(y0[0], y0[1], y0[2], y0[3]), pk4_fp8(y1[0], y1[1], y1[2], y1[3])});
;                     else est((u32x4*)((bf16_t*)XB + o), (u32x4)pack8(y0, y1));
;                     sq += sum8sq(x0, x1); }
;                 row_atomic(ss, row, sq, fq); }
.LBB0_995:
	s_or_b64 exec, exec, s[88:89]
	v_add_u32_e32 v34, 0xa0, v164
	s_waitcnt lgkmcnt(0)
	v_ashrrev_i32_e32 v35, 31, v34
	v_lshlrev_b64 v[36:37], 11, v[34:35]
	v_readlane_b32 s36, v247, 3
	v_lshl_add_u64 v[40:41], v[36:37], 0, v[162:163]
	v_readlane_b32 s37, v247, 4
	v_readlane_b32 s38, v247, 5
	v_readlane_b32 s39, v247, 6
	v_lshl_add_u64 v[54:55], v[40:41], 2, s[36:37]
	s_nop 0
	s_nop 0
	v_readlane_b32 s40, v247, 7
	v_readlane_b32 s41, v247, 8
	v_readlane_b32 s42, v247, 9
	v_readlane_b32 s43, v247, 10
	v_readlane_b32 s44, v247, 11
	v_readlane_b32 s45, v247, 12
	v_readlane_b32 s46, v247, 13
	v_readlane_b32 s47, v247, 14
	v_readlane_b32 s48, v247, 15
	v_readlane_b32 s49, v247, 16
	v_readlane_b32 s50, v247, 17
	v_readlane_b32 s51, v247, 18
	s_waitcnt vmcnt(14)
	s_nop 1
	v_mov_b32_e32 v36, v200
	v_mov_b32_e32 v37, v201
	v_mov_b32_e32 v38, v202
	v_mov_b32_e32 v39, v203
	v_mov_b32_e32 v50, v196
	v_mov_b32_e32 v51, v197
	v_mov_b32_e32 v52, v198
	v_mov_b32_e32 v53, v199
	v_pk_add_f32 v[36:37], v[36:37], v[26:27]
	v_lshlrev_b64 v[26:27], 1, v[40:41]
	s_nop 0
	v_pk_add_f32 v[32:33], v[52:53], v[32:33]
	v_pk_add_f32 v[50:51], v[50:51], v[30:31]
	v_pk_add_f32 v[38:39], v[38:39], v[28:29]
	v_lshl_add_u64 v[40:41], s[30:31], 0, v[26:27]
	v_cvt_pk_bf16_f32 v28, v50, v51
	v_cvt_pk_bf16_f32 v29, v32, v33
	v_cvt_pk_bf16_f32 v30, v36, v37
	v_cvt_pk_bf16_f32 v31, v38, v39
	global_store_dwordx4 v[40:41], v[28:31], off
	v_lshl_add_u64 v[56:57], s[26:27], 0, v[26:27]
	v_pk_mul_f32 v[40:41], v[60:61], v[38:39]
	v_pk_mul_f32 v[28:29], v[62:63], v[50:51]
	v_pk_mul_f32 v[30:31], v[64:65], v[32:33]
	v_cvt_pk_bf16_f32 v28, v28, v29
	v_pk_mul_f32 v[52:53], v[58:59], v[36:37]
	v_cvt_pk_bf16_f32 v29, v30, v31
	v_or_b32_e32 v26, 0x100, v26
	v_cvt_pk_bf16_f32 v30, v52, v53
	v_cvt_pk_bf16_f32 v31, v40, v41
	global_store_dwordx4 v[56:57], v[28:31], off
	s_nop 1
	v_mul_f32_e32 v28, v51, v51
	v_mul_f32_e32 v29, v33, v33
	v_fmac_f32_e32 v28, v50, v50
	v_fmac_f32_e32 v29, v32, v32
	v_add_f32_e32 v28, v28, v29
	v_mul_f32_e32 v29, v37, v37
	v_fmac_f32_e32 v29, v36, v36
	v_add_f32_e32 v28, v29, v28
	v_mul_f32_e32 v29, v39, v39
	v_fmac_f32_e32 v29, v38, v38
	v_add_f32_e32 v40, v29, v28
	s_nop 0
	s_nop 0
	v_lshl_add_u64 v[32:33], s[30:31], 0, v[26:27]
	v_lshl_add_u64 v[26:27], s[26:27], 0, v[26:27]
	s_waitcnt vmcnt(12)
	s_nop 1
	v_mov_b32_e32 v28, v208
	v_mov_b32_e32 v29, v209
	v_mov_b32_e32 v30, v210
	v_mov_b32_e32 v31, v211
	v_mov_b32_e32 v36, v204
	v_mov_b32_e32 v37, v205
	v_mov_b32_e32 v38, v206
	v_mov_b32_e32 v39, v207
	v_pk_add_f32 v[28:29], v[18:19], v[28:29]
	s_nop 0
	v_pk_add_f32 v[24:25], v[24:25], v[38:39]
	v_pk_add_f32 v[22:23], v[22:23], v[36:37]
	v_pk_add_f32 v[30:31], v[20:21], v[30:31]
	v_cvt_pk_bf16_f32 v18, v22, v23
	v_cvt_pk_bf16_f32 v19, v24, v25
	v_cvt_pk_bf16_f32 v20, v28, v29
	v_pk_mul_f32 v[36:37], v[42:43], v[28:29]
	v_cvt_pk_bf16_f32 v21, v30, v31
	global_store_dwordx4 v[32:33], v[18:21], off
	v_pk_mul_f32 v[32:33], v[44:45], v[30:31]
	s_nop 0
	v_pk_mul_f32 v[18:19], v[46:47], v[22:23]
	v_pk_mul_f32 v[20:21], v[48:49], v[24:25]
	v_cvt_pk_bf16_f32 v18, v18, v19
	s_nop 0
	v_cvt_pk_bf16_f32 v19, v20, v21
	v_cvt_pk_bf16_f32 v20, v36, v37
	v_cvt_pk_bf16_f32 v21, v32, v33
	global_store_dwordx4 v[26:27], v[18:21], off
	s_nop 1
	v_mul_f32_e32 v18, v23, v23
	v_mul_f32_e32 v19, v25, v25
	v_fmac_f32_e32 v18, v22, v22
	v_fmac_f32_e32 v19, v24, v24
	v_add_f32_e32 v18, v18, v19
	v_mul_f32_e32 v19, v29, v29
	v_fmac_f32_e32 v19, v28, v28
	v_add_f32_e32 v18, v19, v18
	v_mul_f32_e32 v19, v31, v31
	v_fmac_f32_e32 v19, v30, v30
	v_add_f32_e32 v18, v19, v18
	v_add_f32_e32 v18, v40, v18
	ds_bpermute_b32 v19, v132, v18
	s_waitcnt lgkmcnt(0)
	v_add_f32_e32 v18, v18, v19
	ds_bpermute_b32 v19, v133, v18
	s_and_saveexec_b64 s[88:89], s[0:1]
	s_cbranch_execz .LBB0_997
	s_waitcnt lgkmcnt(0)
	v_add_f32_e32 v18, v18, v19
	v_mul_f32_e32 v18, 0x4b800000, v18
	v_trunc_f32_e32 v18, v18
	v_mul_f32_e32 v19, 0x2f800000, v18
	v_floor_f32_e32 v19, v19
	v_fmac_f32_e32 v18, 0xcf800000, v19
	v_cvt_u32_f32_e32 v18, v18
	v_cvt_u32_f32_e32 v19, v19
	v_lshl_add_u64 v[20:21], v[34:35], 3, s[6:7]
	global_atomic_add_x2 v[20:21], v[18:19], off
; __device__ __forceinline__ unsigned pk4_fp8(float a, float b, float c, float d) { int w = 0; w = __builtin_amdgcn_cvt_pk_fp8_f32(a, b, w, false); w = __builtin_amdgcn_cvt_pk_fp8_f32(c, d, w, true); return (unsigned)w; }
; __device__ __forceinline__ u32x4 pack8(f32x4 v0, f32x4 v1) { u32x4 w; w.x = cvt_pk_bf16(v0[0], v0[1]); w.y = cvt_pk_bf16(v0[2], v0[3]); w.z = cvt_pk_bf16(v1[0], v1[1]); w.w = cvt_pk_bf16(v1[2], v1[3]); return w; }
; template <class T> __device__ __forceinline__ void est(T* p, T v) { if constexpr (MK_EPI_NT != 0) __builtin_nontemporal_store(v, p); else *p = v; }
; __device__ __forceinline__ void unpack8(u32x4 w, f32x4& v0, f32x4& v1) { v0 = (f32x4){bf_lo(w.x), bf_hi(w.x), bf_lo(w.y), bf_hi(w.y)}; v1 = (f32x4){bf_lo(w.z), bf_hi(w.z), bf_lo(w.w), bf_hi(w.w)}; }
; __device__ __forceinline__ float sum8sq(f32x4 a, f32x4 b) { return (a[0] * a[0] + a[1] * a[1]) + (a[2] * a[2] + a[3] * a[3]) + (b[0] * b[0] + b[1] * b[1]) + (b[2] * b[2] + b[3] * b[3]); }
; __device__ __forceinline__ void row_atomic(ss_t* ss, int row, float sq, int fq) { sq += __shfl_xor(sq, 16); sq += __shfl_xor(sq, 32); if (fq == 0) atomicAdd(ss + row, ss_fix(sq)); }
;     __device__ __forceinline__ void operator()(AccT acc, const Unit& u, int wr, int wc, int fr, int fq) const {
;     ...
;             for (int m = 0; m < 4; ++m) { const int row = row0 + ai * 128 + m * 16; float sq = 0.f;
; #pragma unroll
;                 for (int bj = 0; bj < 2; ++bj) { const size_t o = (size_t)row * DM + col0 + bj * 128;
;                     f32x4 r0, r1; if constexpr (RIN16) unpack8(*(const u32x4*)((const bf16_t*)Xin + o), r0, r1); else { r0 = *(const f32x4*)((const float*)Xin + o); r1 = *(const f32x4*)((const float*)Xin + o + 4); }
;                     const f32x4 x0 = r0 + acc[ai][bj][m][0] * ascale, x1 = r1 + acc[ai][bj][m][1] * ascale;
;                     est((u32x4*)(Xout + o), (u32x4)pack8(x0, x1));
;                     const f32x4 y0 = x0 * gv[bj][0], y1 = x1 * gv[bj][1];
;                     if constexpr (F8OUT) est((u32x2*)((unsigned char*)XB + o), (u32x2)(u32x2){pk4_fp8(y0[0], y0[1], y0[2], y0[3]), pk4_fp8(y1[0], y1[1], y1[2], y1[3])});
;                     else est((u32x4*)((bf16_t*)XB + o), (u32x4)pack8(y0, y1));
;                     sq += sum8sq(x0, x1); }
;                 row_atomic(ss, row, sq, fq); }
.LBB0_997:
	s_or_b64 exec, exec, s[88:89]
	v_add_u32_e32 v18, 0xb0, v164
	s_waitcnt lgkmcnt(0)
	v_ashrrev_i32_e32 v19, 31, v18
	v_lshlrev_b64 v[20:21], 11, v[18:19]
	v_readlane_b32 s36, v247, 3
	v_lshl_add_u64 v[28:29], v[20:21], 0, v[162:163]
	v_readlane_b32 s37, v247, 4
	v_readlane_b32 s38, v247, 5
	v_readlane_b32 s39, v247, 6
	v_lshl_add_u64 v[30:31], v[28:29], 2, s[36:37]
	s_nop 0
	s_nop 0
	v_readlane_b32 s40, v247, 7
	v_readlane_b32 s41, v247, 8
	v_readlane_b32 s42, v247, 9
	v_readlane_b32 s43, v247, 10
	v_readlane_b32 s44, v247, 11
	v_readlane_b32 s45, v247, 12
	v_readlane_b32 s46, v247, 13
	v_readlane_b32 s47, v247, 14
	v_readlane_b32 s48, v247, 15
	v_readlane_b32 s49, v247, 16
	v_readlane_b32 s50, v247, 17
	v_readlane_b32 s51, v247, 18
	s_waitcnt vmcnt(10)
	s_nop 1
	v_mov_b32_e32 v20, v216
	v_mov_b32_e32 v21, v217
	v_mov_b32_e32 v22, v218
	v_mov_b32_e32 v23, v219
	v_mov_b32_e32 v24, v212
	v_mov_b32_e32 v25, v213
	v_mov_b32_e32 v26, v214
	v_mov_b32_e32 v27, v215
	v_pk_add_f32 v[20:21], v[10:11], v[20:21]
	v_lshlrev_b64 v[10:11], 1, v[28:29]
	s_nop 0
	v_pk_add_f32 v[16:17], v[16:17], v[26:27]
	v_pk_add_f32 v[24:25], v[14:15], v[24:25]
	v_pk_add_f32 v[22:23], v[12:13], v[22:23]
	v_lshl_add_u64 v[26:27], s[30:31], 0, v[10:11]
	v_cvt_pk_bf16_f32 v12, v24, v25
	v_cvt_pk_bf16_f32 v13, v16, v17
	v_cvt_pk_bf16_f32 v14, v20, v21
	v_cvt_pk_bf16_f32 v15, v22, v23
	global_store_dwordx4 v[26:27], v[12:15], off
	v_lshl_add_u64 v[32:33], s[26:27], 0, v[10:11]
	v_pk_mul_f32 v[26:27], v[60:61], v[22:23]
	v_pk_mul_f32 v[12:13], v[62:63], v[24:25]
	v_pk_mul_f32 v[14:15], v[64:65], v[16:17]
	v_cvt_pk_bf16_f32 v12, v12, v13
	v_pk_mul_f32 v[28:29], v[58:59], v[20:21]
	v_cvt_pk_bf16_f32 v13, v14, v15
	v_or_b32_e32 v10, 0x100, v10
	v_cvt_pk_bf16_f32 v14, v28, v29
	v_cvt_pk_bf16_f32 v15, v26, v27
	global_store_dwordx4 v[32:33], v[12:15], off
	s_nop 1
	v_mul_f32_e32 v12, v25, v25
	v_mul_f32_e32 v13, v17, v17
	v_fmac_f32_e32 v12, v24, v24
	v_fmac_f32_e32 v13, v16, v16
	v_add_f32_e32 v12, v12, v13
	v_mul_f32_e32 v13, v21, v21
	v_fmac_f32_e32 v13, v20, v20
	v_add_f32_e32 v12, v13, v12
	v_mul_f32_e32 v13, v23, v23
	v_fmac_f32_e32 v13, v22, v22
	v_add_f32_e32 v24, v13, v12
	s_nop 0
	s_nop 0
	v_lshl_add_u64 v[16:17], s[30:31], 0, v[10:11]
	v_lshl_add_u64 v[10:11], s[26:27], 0, v[10:11]
	s_waitcnt vmcnt(8)
	s_nop 1
	v_mov_b32_e32 v12, v252
	v_mov_b32_e32 v13, v253
	v_mov_b32_e32 v14, v254
	v_mov_b32_e32 v15, v255
	v_mov_b32_e32 v20, v248
	v_mov_b32_e32 v21, v249
	v_mov_b32_e32 v22, v250
	v_mov_b32_e32 v23, v251
	v_pk_add_f32 v[12:13], v[2:3], v[12:13]
	s_nop 0
	v_pk_add_f32 v[8:9], v[8:9], v[22:23]
	v_pk_add_f32 v[6:7], v[6:7], v[20:21]
	v_pk_add_f32 v[14:15], v[4:5], v[14:15]
	v_cvt_pk_bf16_f32 v2, v6, v7
	v_cvt_pk_bf16_f32 v3, v8, v9
	v_cvt_pk_bf16_f32 v4, v12, v13
	v_pk_mul_f32 v[20:21], v[42:43], v[12:13]
	v_cvt_pk_bf16_f32 v5, v14, v15
	global_store_dwordx4 v[16:17], v[2:5], off
	v_pk_mul_f32 v[16:17], v[44:45], v[14:15]
	s_nop 0
	v_pk_mul_f32 v[2:3], v[46:47], v[6:7]
	v_pk_mul_f32 v[4:5], v[48:49], v[8:9]
	v_cvt_pk_bf16_f32 v2, v2, v3
	s_nop 0
	v_cvt_pk_bf16_f32 v3, v4, v5
	v_cvt_pk_bf16_f32 v4, v20, v21
	v_cvt_pk_bf16_f32 v5, v16, v17
	global_store_dwordx4 v[10:11], v[2:5], off
	s_nop 1
	v_mul_f32_e32 v2, v7, v7
	v_mul_f32_e32 v3, v9, v9
	v_fmac_f32_e32 v2, v6, v6
	v_fmac_f32_e32 v3, v8, v8
	v_add_f32_e32 v2, v2, v3
	v_mul_f32_e32 v3, v13, v13
	v_fmac_f32_e32 v3, v12, v12
	v_add_f32_e32 v2, v3, v2
	v_mul_f32_e32 v3, v15, v15
	v_fmac_f32_e32 v3, v14, v14
	v_add_f32_e32 v2, v3, v2
	v_add_f32_e32 v2, v24, v2
	ds_bpermute_b32 v3, v132, v2
	s_waitcnt lgkmcnt(0)
	v_add_f32_e32 v2, v2, v3
	ds_bpermute_b32 v3, v133, v2
	s_and_saveexec_b64 s[88:89], s[0:1]
	s_cbranch_execz .LBB0_999
	s_waitcnt lgkmcnt(0)
	v_add_f32_e32 v2, v2, v3
	v_mul_f32_e32 v2, 0x4b800000, v2
	v_trunc_f32_e32 v2, v2
	v_mul_f32_e32 v3, 0x2f800000, v2
	v_floor_f32_e32 v3, v3
	v_fmac_f32_e32 v2, 0xcf800000, v3
	v_cvt_u32_f32_e32 v2, v2
	v_cvt_u32_f32_e32 v3, v3
	v_lshl_add_u64 v[4:5], v[18:19], 3, s[6:7]
	global_atomic_add_x2 v[4:5], v[2:3], off

; __device__ __forceinline__ unsigned pk4_fp8(float a, float b, float c, float d) { int w = 0; w = __builtin_amdgcn_cvt_pk_fp8_f32(a, b, w, false); w = __builtin_amdgcn_cvt_pk_fp8_f32(c, d, w, true); return (unsigned)w; }
; __device__ __forceinline__ u32x4 pack8(f32x4 v0, f32x4 v1) { u32x4 w; w.x = cvt_pk_bf16(v0[0], v0[1]); w.y = cvt_pk_bf16(v0[2], v0[3]); w.z = cvt_pk_bf16(v1[0], v1[1]); w.w = cvt_pk_bf16(v1[2], v1[3]); return w; }
; template <class T> __device__ __forceinline__ void est(T* p, T v) { if constexpr (MK_EPI_NT != 0) __builtin_nontemporal_store(v, p); else *p = v; }
; __device__ __forceinline__ void unpack8(u32x4 w, f32x4& v0, f32x4& v1) { v0 = (f32x4){bf_lo(w.x), bf_hi(w.x), bf_lo(w.y), bf_hi(w.y)}; v1 = (f32x4){bf_lo(w.z), bf_hi(w.z), bf_lo(w.w), bf_hi(w.w)}; }
;     __device__ __forceinline__ void operator()(AccT acc, const Unit& u, int wr, int wc, int fr, int fq) const {
;         const int row0 = u.pm * 256 + wr * 64 + fr, col0 = u.pn * 256 + wc * 32 + 8 * fq;
;         f32x4 gv[2][2];
; #pragma unroll
;         for (int bj = 0; bj < 2; ++bj) { gv[bj][0] = *(const f32x4*)(gain + col0 + bj * 128); gv[bj][1] = *(const f32x4*)(gain + col0 + bj * 128 + 4); }
; #pragma unroll
;         for (int ai = 0; ai < 2; ++ai)
; #pragma unroll
;             for (int m = 0; m < 4; ++m) { const int row = row0 + ai * 128 + m * 16; float sq = 0.f;
; #pragma unroll
;                 for (int bj = 0; bj < 2; ++bj) { const size_t o = (size_t)row * DM + col0 + bj * 128;
;                     f32x4 r0, r1; if constexpr (RIN16) unpack8(*(const u32x4*)((const bf16_t*)Xin + o), r0, r1); else { r0 = *(const f32x4*)((const float*)Xin + o); r1 = *(const f32x4*)((const float*)Xin + o + 4); }
;                     const f32x4 x0 = r0 + acc[ai][bj][m][0] * ascale, x1 = r1 + acc[ai][bj][m][1] * ascale;
;                     est((u32x4*)(Xout + o), (u32x4)pack8(x0, x1));
;                     const f32x4 y0 = x0 * gv[bj][0], y1 = x1 * gv[bj][1];
;                     if constexpr (F8OUT) est((u32x2*)((unsigned char*)XB + o), (u32x2)(u32x2){pk4_fp8(y0[0], y0[1], y0[2], y0[3]), pk4_fp8(y1[0], y1[1], y1[2], y1[3])});
;                     else est((u32x4*)((bf16_t*)XB + o), (u32x4)pack8(y0, y1));
;                     sq += sum8sq(x0, x1); }
;                 row_atomic(ss, row, sq, fq); }
.LBB0_1153:
	v_lshl_add_u32 v36, s20, 8, v190
	v_lshl_or_b32 v34, s21, 8, v192
	v_ashrrev_i32_e32 v37, 31, v36
	v_ashrrev_i32_e32 v35, 31, v34
	v_lshlrev_b64 v[38:39], 11, v[36:37]
	v_readlane_b32 s36, v247, 36
	v_lshl_add_u64 v[38:39], v[38:39], 0, v[34:35]
	v_readlane_b32 s44, v247, 44
	v_readlane_b32 s45, v247, 45
	v_lshlrev_b64 v[38:39], 1, v[38:39]
	s_nop 15
	s_nop 15
	v_lshl_add_u64 v[40:41], s[30:31], 0, v[38:39]
	v_lshl_add_u64 v[6:7], v[34:35], 2, s[44:45]
	global_load_dwordx4 v[10:13], v[6:7], off offset:16
	global_load_dwordx4 v[14:17], v[6:7], off
	s_waitcnt lgkmcnt(0)
	global_load_dwordx4 v[2:5], v[6:7], off offset:528
	s_nop 0
	global_load_dwordx4 v[6:9], v[6:7], off offset:512
	v_readlane_b32 s20, v247, 55
	v_mov_b32_e32 v248, v40
	v_mov_b32_e32 v249, v41
	global_load_dwordx4 v[198:201], v[248:249], off
	global_load_dwordx4 v[202:205], v[248:249], off offset:256
	s_mov_b64 s[100:101], 0x10000
	v_lshl_add_u64 v[248:249], v[248:249], 0, s[100:101]
	global_load_dwordx4 v[206:209], v[248:249], off
	global_load_dwordx4 v[210:213], v[248:249], off offset:256
	s_mov_b64 s[100:101], 0x10000
	v_lshl_add_u64 v[248:249], v[248:249], 0, s[100:101]
	global_load_dwordx4 v[214:217], v[248:249], off
	global_load_dwordx4 v[218:221], v[248:249], off offset:256
	s_mov_b64 s[100:101], 0x10000
	v_lshl_add_u64 v[248:249], v[248:249], 0, s[100:101]
	global_load_dwordx4 v[222:225], v[248:249], off
	global_load_dwordx4 v[226:229], v[248:249], off offset:256
	v_readlane_b32 s21, v247, 56
	v_readlane_b32 s37, v247, 37
	v_readlane_b32 s38, v247, 38
	v_lshl_add_u64 v[76:77], s[20:21], 0, v[38:39]
	v_or_b32_e32 v38, 0x100, v38
	v_readlane_b32 s39, v247, 39
	v_readlane_b32 s40, v247, 40
	v_readlane_b32 s41, v247, 41
	v_readlane_b32 s42, v247, 42
	v_readlane_b32 s43, v247, 43
	v_readlane_b32 s46, v247, 46
	v_readlane_b32 s47, v247, 47
	v_readlane_b32 s48, v247, 48
	v_readlane_b32 s49, v247, 49
	v_readlane_b32 s50, v247, 50
	v_readlane_b32 s51, v247, 51
	s_waitcnt vmcnt(0)
	s_nop 1
	v_mov_b32_e32 v50, v198
	v_mov_b32_e32 v51, v199
	v_mov_b32_e32 v52, v200
	v_mov_b32_e32 v53, v201
	s_mov_b64 s[100:101], 0x50000
	v_lshl_add_u64 v[248:249], v[248:249], 0, s[100:101]
	global_load_dwordx4 v[198:201], v[248:249], off
	v_lshlrev_b32_e32 v58, 16, v50
	v_and_b32_e32 v59, 0xffff0000, v50
	v_lshlrev_b32_e32 v50, 16, v51
	v_and_b32_e32 v51, 0xffff0000, v51
	v_lshlrev_b32_e32 v60, 16, v52
	v_and_b32_e32 v61, 0xffff0000, v52
	v_lshlrev_b32_e32 v52, 16, v53
	v_and_b32_e32 v53, 0xffff0000, v53
	v_pk_add_f32 v[66:67], v[182:183], v[50:51]
	v_pk_add_f32 v[58:59], v[184:185], v[58:59]
	v_pk_add_f32 v[68:69], v[186:187], v[52:53]
	v_cvt_pk_bf16_f32 v50, v58, v59
	v_cvt_pk_bf16_f32 v51, v66, v67
	v_pk_add_f32 v[60:61], v[188:189], v[60:61]
	v_pk_mul_f32 v[74:75], v[12:13], v[68:69]
	v_cvt_pk_bf16_f32 v52, v60, v61
	v_cvt_pk_bf16_f32 v53, v68, v69
	global_store_dwordx4 v[40:41], v[50:53], off
	v_pk_mul_f32 v[40:41], v[16:17], v[66:67]
	s_nop 0
	v_pk_mul_f32 v[50:51], v[14:15], v[58:59]
	v_pk_mul_f32 v[52:53], v[10:11], v[60:61]
	v_cvt_pk_bf16_f32 v50, v50, v51
	v_cvt_pk_bf16_f32 v51, v40, v41
	v_mul_f32_e32 v40, v59, v59
	v_mul_f32_e32 v41, v67, v67
	v_fmac_f32_e32 v40, v58, v58
	v_fmac_f32_e32 v41, v66, v66
	v_add_f32_e32 v40, v40, v41
	v_mul_f32_e32 v41, v61, v61
	v_fmac_f32_e32 v41, v60, v60
	v_add_f32_e32 v40, v41, v40
	v_mul_f32_e32 v41, v69, v69
	v_fmac_f32_e32 v41, v68, v68
	v_cvt_pk_bf16_f32 v52, v52, v53
	v_cvt_pk_bf16_f32 v53, v74, v75
	v_add_f32_e32 v122, v41, v40
	v_lshl_add_u64 v[40:41], s[30:31], 0, v[38:39]
	global_store_dwordx4 v[76:77], v[50:53], off
	s_nop 0
	v_lshl_add_u64 v[76:77], s[20:21], 0, v[38:39]
	s_waitcnt vmcnt(9)
	s_nop 1
	v_mov_b32_e32 v50, v202
	v_mov_b32_e32 v51, v203
	v_mov_b32_e32 v52, v204
	v_mov_b32_e32 v53, v205
	global_load_dwordx4 v[202:205], v[248:249], off offset:256
	v_lshlrev_b32_e32 v58, 16, v50
	v_and_b32_e32 v59, 0xffff0000, v50
	v_lshlrev_b32_e32 v50, 16, v51
	v_and_b32_e32 v51, 0xffff0000, v51
	v_lshlrev_b32_e32 v60, 16, v52
	v_and_b32_e32 v61, 0xffff0000, v52
	v_lshlrev_b32_e32 v52, 16, v53
	v_and_b32_e32 v53, 0xffff0000, v53
	v_pk_add_f32 v[66:67], v[158:159], v[50:51]
	v_pk_add_f32 v[58:59], v[160:161], v[58:59]
	v_pk_add_f32 v[68:69], v[178:179], v[52:53]
	v_cvt_pk_bf16_f32 v50, v58, v59
	v_cvt_pk_bf16_f32 v51, v66, v67
	v_pk_add_f32 v[60:61], v[180:181], v[60:61]
	s_nop 0
	v_cvt_pk_bf16_f32 v52, v60, v61
	v_cvt_pk_bf16_f32 v53, v68, v69
	global_store_dwordx4 v[40:41], v[50:53], off
	v_pk_mul_f32 v[40:41], v[8:9], v[66:67]
	v_pk_mul_f32 v[74:75], v[2:3], v[60:61]
	v_pk_mul_f32 v[50:51], v[6:7], v[58:59]
	v_pk_mul_f32 v[52:53], v[4:5], v[68:69]
	v_cvt_pk_bf16_f32 v38, v50, v51
	v_cvt_pk_bf16_f32 v39, v40, v41
	v_cvt_pk_bf16_f32 v40, v74, v75
	s_nop 0
	v_cvt_pk_bf16_f32 v41, v52, v53
	global_store_dwordx4 v[76:77], v[38:41], off
	s_nop 1
	v_mul_f32_e32 v38, v59, v59
	v_mul_f32_e32 v39, v67, v67
	v_fmac_f32_e32 v38, v58, v58
	v_fmac_f32_e32 v39, v66, v66
	v_add_f32_e32 v38, v38, v39
	v_mul_f32_e32 v39, v61, v61
	v_fmac_f32_e32 v39, v60, v60
	v_add_f32_e32 v38, v39, v38
	v_mul_f32_e32 v39, v69, v69
	v_fmac_f32_e32 v39, v68, v68
	v_and_b32_e32 v40, 64, v197
	v_add_f32_e32 v38, v39, v38
	v_xor_b32_e32 v39, 16, v197
	v_add_u32_e32 v40, 64, v40
	v_cmp_lt_i32_e32 vcc, v39, v40
	v_add_f32_e32 v38, v122, v38
	s_nop 0
	v_cndmask_b32_e32 v39, v197, v39, vcc
	v_lshlrev_b32_e32 v50, 2, v39
	ds_bpermute_b32 v39, v50, v38
	s_waitcnt lgkmcnt(0)
	v_add_f32_e32 v38, v38, v39
	v_xor_b32_e32 v39, 32, v197
	v_cmp_lt_i32_e32 vcc, v39, v40
	s_nop 1
	v_cndmask_b32_e32 v39, v197, v39, vcc
	v_lshlrev_b32_e32 v51, 2, v39
	ds_bpermute_b32 v39, v51, v38
	s_and_saveexec_b64 s[82:83], s[0:1]
	s_cbranch_execz .LBB0_1155
	s_waitcnt lgkmcnt(0)
	v_add_f32_e32 v38, v38, v39
	v_mul_f32_e32 v38, 0x4b800000, v38
	v_trunc_f32_e32 v38, v38
	v_mul_f32_e32 v39, 0x2f800000, v38
	v_floor_f32_e32 v39, v39
	v_fmac_f32_e32 v38, 0xcf800000, v39
	v_cvt_u32_f32_e32 v38, v38
	v_cvt_u32_f32_e32 v39, v39
	v_lshl_add_u64 v[40:41], v[36:37], 3, s[6:7]
	global_atomic_add_x2 v[40:41], v[38:39], off
; __device__ __forceinline__ unsigned pk4_fp8(float a, float b, float c, float d) { int w = 0; w = __builtin_amdgcn_cvt_pk_fp8_f32(a, b, w, false); w = __builtin_amdgcn_cvt_pk_fp8_f32(c, d, w, true); return (unsigned)w; }
; __device__ __forceinline__ u32x4 pack8(f32x4 v0, f32x4 v1) { u32x4 w; w.x = cvt_pk_bf16(v0[0], v0[1]); w.y = cvt_pk_bf16(v0[2], v0[3]); w.z = cvt_pk_bf16(v1[0], v1[1]); w.w = cvt_pk_bf16(v1[2], v1[3]); return w; }
; template <class T> __device__ __forceinline__ void est(T* p, T v) { if constexpr (MK_EPI_NT != 0) __builtin_nontemporal_store(v, p); else *p = v; }
; __device__ __forceinline__ void unpack8(u32x4 w, f32x4& v0, f32x4& v1) { v0 = (f32x4){bf_lo(w.x), bf_hi(w.x), bf_lo(w.y), bf_hi(w.y)}; v1 = (f32x4){bf_lo(w.z), bf_hi(w.z), bf_lo(w.w), bf_hi(w.w)}; }
; __device__ __forceinline__ float sum8sq(f32x4 a, f32x4 b) { return (a[0] * a[0] + a[1] * a[1]) + (a[2] * a[2] + a[3] * a[3]) + (b[0] * b[0] + b[1] * b[1]) + (b[2] * b[2] + b[3] * b[3]); }
; __device__ __forceinline__ void row_atomic(ss_t* ss, int row, float sq, int fq) { sq += __shfl_xor(sq, 16); sq += __shfl_xor(sq, 32); if (fq == 0) atomicAdd(ss + row, ss_fix(sq)); }
;     __device__ __forceinline__ void operator()(AccT acc, const Unit& u, int wr, int wc, int fr, int fq) const {
;     ...
;             for (int m = 0; m < 4; ++m) { const int row = row0 + ai * 128 + m * 16; float sq = 0.f;
; #pragma unroll
;                 for (int bj = 0; bj < 2; ++bj) { const size_t o = (size_t)row * DM + col0 + bj * 128;
;                     f32x4 r0, r1; if constexpr (RIN16) unpack8(*(const u32x4*)((const bf16_t*)Xin + o), r0, r1); else { r0 = *(const f32x4*)((const float*)Xin + o); r1 = *(const f32x4*)((const float*)Xin + o + 4); }
;                     const f32x4 x0 = r0 + acc[ai][bj][m][0] * ascale, x1 = r1 + acc[ai][bj][m][1] * ascale;
;                     est((u32x4*)(Xout + o), (u32x4)pack8(x0, x1));
;                     const f32x4 y0 = x0 * gv[bj][0], y1 = x1 * gv[bj][1];
;                     if constexpr (F8OUT) est((u32x2*)((unsigned char*)XB + o), (u32x2)(u32x2){pk4_fp8(y0[0], y0[1], y0[2], y0[3]), pk4_fp8(y1[0], y1[1], y1[2], y1[3])});
;                     else est((u32x4*)((bf16_t*)XB + o), (u32x4)pack8(y0, y1));
;                     sq += sum8sq(x0, x1); }
;                 row_atomic(ss, row, sq, fq); }
.LBB0_1155:
	s_or_b64 exec, exec, s[82:83]
	v_or_b32_e32 v38, 16, v36
	s_waitcnt lgkmcnt(0)
	v_ashrrev_i32_e32 v39, 31, v38
	v_lshlrev_b64 v[40:41], 11, v[38:39]
	v_lshl_add_u64 v[40:41], v[40:41], 0, v[34:35]
	v_lshlrev_b64 v[40:41], 1, v[40:41]
	v_lshl_add_u64 v[52:53], s[30:31], 0, v[40:41]
	s_nop 0
	v_readlane_b32 s20, v247, 55
	v_readlane_b32 s21, v247, 56
	s_waitcnt vmcnt(11)
	s_nop 1
	v_mov_b32_e32 v58, v206
	v_mov_b32_e32 v59, v207
	v_mov_b32_e32 v60, v208
	v_mov_b32_e32 v61, v209
	s_mov_b64 s[100:101], 0x10000
	v_lshl_add_u64 v[248:249], v[248:249], 0, s[100:101]
	global_load_dwordx4 v[206:209], v[248:249], off
	v_lshlrev_b32_e32 v66, 16, v58
	v_and_b32_e32 v67, 0xffff0000, v58
	v_lshlrev_b32_e32 v58, 16, v59
	v_and_b32_e32 v59, 0xffff0000, v59
	v_lshlrev_b32_e32 v68, 16, v60
	v_and_b32_e32 v69, 0xffff0000, v60
	v_lshlrev_b32_e32 v60, 16, v61
	v_and_b32_e32 v61, 0xffff0000, v61
	v_pk_add_f32 v[74:75], v[152:153], v[58:59]
	v_pk_add_f32 v[66:67], v[150:151], v[66:67]
	v_pk_add_f32 v[76:77], v[154:155], v[60:61]
	v_cvt_pk_bf16_f32 v58, v66, v67
	v_cvt_pk_bf16_f32 v59, v74, v75
	v_pk_add_f32 v[68:69], v[156:157], v[68:69]
	v_mul_f32_e32 v37, v67, v67
	v_cvt_pk_bf16_f32 v60, v68, v69
	v_cvt_pk_bf16_f32 v61, v76, v77
	global_store_dwordx4 v[52:53], v[58:61], off
	v_pk_mul_f32 v[52:53], v[16:17], v[74:75]
	v_fmac_f32_e32 v37, v66, v66
	v_pk_mul_f32 v[58:59], v[14:15], v[66:67]
	v_pk_mul_f32 v[60:61], v[10:11], v[68:69]
	v_cvt_pk_bf16_f32 v58, v58, v59
	v_cvt_pk_bf16_f32 v59, v52, v53
	v_mul_f32_e32 v52, v75, v75
	v_fmac_f32_e32 v52, v74, v74
	v_add_f32_e32 v37, v37, v52
	v_mul_f32_e32 v52, v69, v69
	v_fmac_f32_e32 v52, v68, v68
	v_add_f32_e32 v37, v52, v37
	v_mul_f32_e32 v52, v77, v77
	v_lshl_add_u64 v[124:125], s[20:21], 0, v[40:41]
	v_fmac_f32_e32 v52, v76, v76
	v_or_b32_e32 v40, 0x100, v40
	v_pk_mul_f32 v[122:123], v[12:13], v[76:77]
	v_cvt_pk_bf16_f32 v60, v60, v61
	v_add_f32_e32 v37, v52, v37
	v_cvt_pk_bf16_f32 v61, v122, v123
	v_lshl_add_u64 v[52:53], s[30:31], 0, v[40:41]
	global_store_dwordx4 v[124:125], v[58:61], off
	s_nop 0
	v_lshl_add_u64 v[40:41], s[20:21], 0, v[40:41]
	s_waitcnt vmcnt(13)
	s_nop 1
	v_mov_b32_e32 v58, v210
	v_mov_b32_e32 v59, v211
	v_mov_b32_e32 v60, v212
	v_mov_b32_e32 v61, v213
	global_load_dwordx4 v[210:213], v[248:249], off offset:256
	v_lshlrev_b32_e32 v66, 16, v58
	v_and_b32_e32 v67, 0xffff0000, v58
	v_lshlrev_b32_e32 v58, 16, v59
	v_and_b32_e32 v59, 0xffff0000, v59
	v_lshlrev_b32_e32 v68, 16, v60
	v_and_b32_e32 v69, 0xffff0000, v60
	v_lshlrev_b32_e32 v60, 16, v61
	v_and_b32_e32 v61, 0xffff0000, v61
	v_pk_add_f32 v[74:75], v[148:149], v[58:59]
	v_pk_add_f32 v[66:67], v[146:147], v[66:67]
	v_pk_add_f32 v[76:77], v[144:145], v[60:61]
	v_pk_add_f32 v[68:69], v[142:143], v[68:69]
	v_cvt_pk_bf16_f32 v58, v66, v67
	v_cvt_pk_bf16_f32 v59, v74, v75
	v_pk_mul_f32 v[122:123], v[4:5], v[76:77]
	v_cvt_pk_bf16_f32 v60, v68, v69
	v_cvt_pk_bf16_f32 v61, v76, v77
	global_store_dwordx4 v[52:53], v[58:61], off
	v_pk_mul_f32 v[52:53], v[8:9], v[74:75]
	s_nop 0
	v_pk_mul_f32 v[58:59], v[6:7], v[66:67]
	v_pk_mul_f32 v[60:61], v[2:3], v[68:69]
	v_cvt_pk_bf16_f32 v58, v58, v59
	v_cvt_pk_bf16_f32 v59, v52, v53
	s_nop 0
	v_cvt_pk_bf16_f32 v60, v60, v61
	v_cvt_pk_bf16_f32 v61, v122, v123
	global_store_dwordx4 v[40:41], v[58:61], off
	v_mul_f32_e32 v40, v67, v67
	v_mul_f32_e32 v41, v75, v75
	v_fmac_f32_e32 v40, v66, v66
	v_fmac_f32_e32 v41, v74, v74
	v_add_f32_e32 v40, v40, v41
	v_mul_f32_e32 v41, v69, v69
	v_fmac_f32_e32 v41, v68, v68
	v_add_f32_e32 v40, v41, v40
	v_mul_f32_e32 v41, v77, v77
	v_fmac_f32_e32 v41, v76, v76
	v_add_f32_e32 v40, v41, v40
	v_add_f32_e32 v37, v37, v40
	ds_bpermute_b32 v40, v50, v37
	s_waitcnt lgkmcnt(0)
	v_add_f32_e32 v37, v37, v40
	ds_bpermute_b32 v40, v51, v37
	s_and_saveexec_b64 s[82:83], s[0:1]
	s_cbranch_execz .LBB0_1157
	s_waitcnt lgkmcnt(0)
	v_add_f32_e32 v37, v37, v40
	v_mul_f32_e32 v37, 0x4b800000, v37
	v_trunc_f32_e32 v37, v37
	v_mul_f32_e32 v40, 0x2f800000, v37
	v_floor_f32_e32 v41, v40
	v_fmac_f32_e32 v37, 0xcf800000, v41
	v_cvt_u32_f32_e32 v40, v37
	v_cvt_u32_f32_e32 v41, v41
	v_lshl_add_u64 v[38:39], v[38:39], 3, s[6:7]
	global_atomic_add_x2 v[38:39], v[40:41], off
.LBB0_1157:
	s_or_b64 exec, exec, s[82:83]
	v_or_b32_e32 v38, 32, v36
	v_ashrrev_i32_e32 v39, 31, v38
	s_waitcnt lgkmcnt(0)
	v_lshlrev_b64 v[40:41], 11, v[38:39]
	v_lshl_add_u64 v[40:41], v[40:41], 0, v[34:35]
	v_lshlrev_b64 v[40:41], 1, v[40:41]
	v_lshl_add_u64 v[52:53], s[30:31], 0, v[40:41]
	s_nop 0
	v_readlane_b32 s20, v247, 55
	v_readlane_b32 s21, v247, 56
	s_waitcnt vmcnt(15)
	s_nop 1
	v_mov_b32_e32 v58, v214
	v_mov_b32_e32 v59, v215
	v_mov_b32_e32 v60, v216
	v_mov_b32_e32 v61, v217
	s_mov_b64 s[100:101], 0x10000
	v_lshl_add_u64 v[248:249], v[248:249], 0, s[100:101]
	global_load_dwordx4 v[214:217], v[248:249], off
	v_lshlrev_b32_e32 v66, 16, v58
	v_and_b32_e32 v67, 0xffff0000, v58
	v_lshlrev_b32_e32 v58, 16, v59
	v_and_b32_e32 v59, 0xffff0000, v59
	v_lshlrev_b32_e32 v68, 16, v60
	v_and_b32_e32 v69, 0xffff0000, v60
	v_lshlrev_b32_e32 v60, 16, v61
	v_and_b32_e32 v61, 0xffff0000, v61
	v_pk_add_f32 v[74:75], v[134:135], v[58:59]
	v_pk_add_f32 v[66:67], v[136:137], v[66:67]
	v_pk_add_f32 v[76:77], v[138:139], v[60:61]
	v_cvt_pk_bf16_f32 v58, v66, v67
	v_cvt_pk_bf16_f32 v59, v74, v75
	v_pk_add_f32 v[68:69], v[140:141], v[68:69]
	v_mul_f32_e32 v37, v67, v67
	v_cvt_pk_bf16_f32 v60, v68, v69
	v_cvt_pk_bf16_f32 v61, v76, v77
	global_store_dwordx4 v[52:53], v[58:61], off
	v_pk_mul_f32 v[52:53], v[16:17], v[74:75]
	v_fmac_f32_e32 v37, v66, v66
	v_pk_mul_f32 v[58:59], v[14:15], v[66:67]
	v_pk_mul_f32 v[60:61], v[10:11], v[68:69]
	v_cvt_pk_bf16_f32 v58, v58, v59
	v_cvt_pk_bf16_f32 v59, v52, v53
	v_mul_f32_e32 v52, v75, v75
	v_fmac_f32_e32 v52, v74, v74
	v_add_f32_e32 v37, v37, v52
	v_mul_f32_e32 v52, v69, v69
	v_fmac_f32_e32 v52, v68, v68
	v_add_f32_e32 v37, v52, v37
	v_mul_f32_e32 v52, v77, v77
	v_lshl_add_u64 v[124:125], s[20:21], 0, v[40:41]
	v_fmac_f32_e32 v52, v76, v76
	v_or_b32_e32 v40, 0x100, v40
	v_pk_mul_f32 v[122:123], v[12:13], v[76:77]
	v_cvt_pk_bf16_f32 v60, v60, v61
	v_add_f32_e32 v37, v52, v37
	v_cvt_pk_bf16_f32 v61, v122, v123
	v_lshl_add_u64 v[52:53], s[30:31], 0, v[40:41]
	global_store_dwordx4 v[124:125], v[58:61], off
	s_nop 0
	v_lshl_add_u64 v[40:41], s[20:21], 0, v[40:41]
	s_waitcnt vmcnt(17)
; __device__ __forceinline__ unsigned pk4_fp8(float a, float b, float c, float d) { int w = 0; w = __builtin_amdgcn_cvt_pk_fp8_f32(a, b, w, false); w = __builtin_amdgcn_cvt_pk_fp8_f32(c, d, w, true); return (unsigned)w; }
; __device__ __forceinline__ u32x4 pack8(f32x4 v0, f32x4 v1) { u32x4 w; w.x = cvt_pk_bf16(v0[0], v0[1]); w.y = cvt_pk_bf16(v0[2], v0[3]); w.z = cvt_pk_bf16(v1[0], v1[1]); w.w = cvt_pk_bf16(v1[2], v1[3]); return w; }
; template <class T> __device__ __forceinline__ void est(T* p, T v) { if constexpr (MK_EPI_NT != 0) __builtin_nontemporal_store(v, p); else *p = v; }
; __device__ __forceinline__ void unpack8(u32x4 w, f32x4& v0, f32x4& v1) { v0 = (f32x4){bf_lo(w.x), bf_hi(w.x), bf_lo(w.y), bf_hi(w.y)}; v1 = (f32x4){bf_lo(w.z), bf_hi(w.z), bf_lo(w.w), bf_hi(w.w)}; }
; __device__ __forceinline__ float sum8sq(f32x4 a, f32x4 b) { return (a[0] * a[0] + a[1] * a[1]) + (a[2] * a[2] + a[3] * a[3]) + (b[0] * b[0] + b[1] * b[1]) + (b[2] * b[2] + b[3] * b[3]); }
; __device__ __forceinline__ void row_atomic(ss_t* ss, int row, float sq, int fq) { sq += __shfl_xor(sq, 16); sq += __shfl_xor(sq, 32); if (fq == 0) atomicAdd(ss + row, ss_fix(sq)); }
;     __device__ __forceinline__ void operator()(AccT acc, const Unit& u, int wr, int wc, int fr, int fq) const {
;     ...
;             for (int m = 0; m < 4; ++m) { const int row = row0 + ai * 128 + m * 16; float sq = 0.f;
; #pragma unroll
;                 for (int bj = 0; bj < 2; ++bj) { const size_t o = (size_t)row * DM + col0 + bj * 128;
;                     f32x4 r0, r1; if constexpr (RIN16) unpack8(*(const u32x4*)((const bf16_t*)Xin + o), r0, r1); else { r0 = *(const f32x4*)((const float*)Xin + o); r1 = *(const f32x4*)((const float*)Xin + o + 4); }
;                     const f32x4 x0 = r0 + acc[ai][bj][m][0] * ascale, x1 = r1 + acc[ai][bj][m][1] * ascale;
;                     est((u32x4*)(Xout + o), (u32x4)pack8(x0, x1));
;                     const f32x4 y0 = x0 * gv[bj][0], y1 = x1 * gv[bj][1];
;                     if constexpr (F8OUT) est((u32x2*)((unsigned char*)XB + o), (u32x2)(u32x2){pk4_fp8(y0[0], y0[1], y0[2], y0[3]), pk4_fp8(y1[0], y1[1], y1[2], y1[3])});
;                     else est((u32x4*)((bf16_t*)XB + o), (u32x4)pack8(y0, y1));
;                     sq += sum8sq(x0, x1); }
;                 row_atomic(ss, row, sq, fq); }
	s_nop 1
	v_mov_b32_e32 v58, v218
	v_mov_b32_e32 v59, v219
	v_mov_b32_e32 v60, v220
	v_mov_b32_e32 v61, v221
	global_load_dwordx4 v[218:221], v[248:249], off offset:256
	v_lshlrev_b32_e32 v66, 16, v58
	v_and_b32_e32 v67, 0xffff0000, v58
	v_lshlrev_b32_e32 v58, 16, v59
	v_and_b32_e32 v59, 0xffff0000, v59
	v_lshlrev_b32_e32 v68, 16, v60
	v_and_b32_e32 v69, 0xffff0000, v60
	v_lshlrev_b32_e32 v60, 16, v61
	v_and_b32_e32 v61, 0xffff0000, v61
	v_pk_add_f32 v[74:75], v[132:133], v[58:59]
	v_pk_add_f32 v[66:67], v[130:131], v[66:67]
	v_pk_add_f32 v[76:77], v[128:129], v[60:61]
	v_pk_add_f32 v[68:69], v[126:127], v[68:69]
	v_cvt_pk_bf16_f32 v58, v66, v67
	v_cvt_pk_bf16_f32 v59, v74, v75
	v_pk_mul_f32 v[122:123], v[4:5], v[76:77]
	v_cvt_pk_bf16_f32 v60, v68, v69
	v_cvt_pk_bf16_f32 v61, v76, v77
	global_store_dwordx4 v[52:53], v[58:61], off
	v_pk_mul_f32 v[52:53], v[8:9], v[74:75]
	s_nop 0
	v_pk_mul_f32 v[58:59], v[6:7], v[66:67]
	v_pk_mul_f32 v[60:61], v[2:3], v[68:69]
	v_cvt_pk_bf16_f32 v58, v58, v59
	v_cvt_pk_bf16_f32 v59, v52, v53
	s_nop 0
	v_cvt_pk_bf16_f32 v60, v60, v61
	v_cvt_pk_bf16_f32 v61, v122, v123
	global_store_dwordx4 v[40:41], v[58:61], off
	v_mul_f32_e32 v40, v67, v67
	v_mul_f32_e32 v41, v75, v75
	v_fmac_f32_e32 v40, v66, v66
	v_fmac_f32_e32 v41, v74, v74
	v_add_f32_e32 v40, v40, v41
	v_mul_f32_e32 v41, v69, v69
	v_fmac_f32_e32 v41, v68, v68
	v_add_f32_e32 v40, v41, v40
	v_mul_f32_e32 v41, v77, v77
	v_fmac_f32_e32 v41, v76, v76
	v_add_f32_e32 v40, v41, v40
	v_add_f32_e32 v37, v37, v40
	ds_bpermute_b32 v40, v50, v37
	s_waitcnt lgkmcnt(0)
	v_add_f32_e32 v37, v37, v40
	ds_bpermute_b32 v40, v51, v37
	s_and_saveexec_b64 s[82:83], s[0:1]
	s_cbranch_execz .LBB0_1159
	s_waitcnt lgkmcnt(0)
	v_add_f32_e32 v37, v37, v40
	v_mul_f32_e32 v37, 0x4b800000, v37
	v_trunc_f32_e32 v37, v37
	v_mul_f32_e32 v40, 0x2f800000, v37
	v_floor_f32_e32 v41, v40
	v_fmac_f32_e32 v37, 0xcf800000, v41
	v_cvt_u32_f32_e32 v40, v37
	v_cvt_u32_f32_e32 v41, v41
	v_lshl_add_u64 v[38:39], v[38:39], 3, s[6:7]
	global_atomic_add_x2 v[38:39], v[40:41], off
.LBB0_1159:
	s_or_b64 exec, exec, s[82:83]
	v_or_b32_e32 v38, 48, v36
	v_ashrrev_i32_e32 v39, 31, v38
	s_waitcnt lgkmcnt(0)
	v_lshlrev_b64 v[40:41], 11, v[38:39]
	v_lshl_add_u64 v[40:41], v[40:41], 0, v[34:35]
	v_lshlrev_b64 v[40:41], 1, v[40:41]
	v_lshl_add_u64 v[52:53], s[30:31], 0, v[40:41]
	s_nop 0
	v_readlane_b32 s20, v247, 55
	v_readlane_b32 s21, v247, 56
	s_waitcnt vmcnt(19)
	s_nop 1
	v_mov_b32_e32 v58, v222
	v_mov_b32_e32 v59, v223
	v_mov_b32_e32 v60, v224
	v_mov_b32_e32 v61, v225
	s_mov_b64 s[100:101], 0x10000
	v_lshl_add_u64 v[248:249], v[248:249], 0, s[100:101]
	global_load_dwordx4 v[222:225], v[248:249], off
	v_lshlrev_b32_e32 v66, 16, v58
	v_and_b32_e32 v67, 0xffff0000, v58
	v_lshlrev_b32_e32 v58, 16, v59
	v_and_b32_e32 v59, 0xffff0000, v59
	v_lshlrev_b32_e32 v68, 16, v60
	v_and_b32_e32 v69, 0xffff0000, v60
	v_lshlrev_b32_e32 v60, 16, v61
	v_and_b32_e32 v61, 0xffff0000, v61
	v_pk_add_f32 v[74:75], v[118:119], v[58:59]
	v_pk_add_f32 v[66:67], v[120:121], v[66:67]
	v_pk_add_f32 v[76:77], v[116:117], v[60:61]
	v_cvt_pk_bf16_f32 v58, v66, v67
	v_cvt_pk_bf16_f32 v59, v74, v75
	v_pk_add_f32 v[68:69], v[114:115], v[68:69]
	v_mul_f32_e32 v37, v67, v67
	v_cvt_pk_bf16_f32 v60, v68, v69
	v_cvt_pk_bf16_f32 v61, v76, v77
	global_store_dwordx4 v[52:53], v[58:61], off
	v_pk_mul_f32 v[52:53], v[16:17], v[74:75]
	v_fmac_f32_e32 v37, v66, v66
	v_pk_mul_f32 v[58:59], v[14:15], v[66:67]
	v_pk_mul_f32 v[60:61], v[10:11], v[68:69]
	v_cvt_pk_bf16_f32 v58, v58, v59
	v_cvt_pk_bf16_f32 v59, v52, v53
	v_mul_f32_e32 v52, v75, v75
	v_fmac_f32_e32 v52, v74, v74
	v_add_f32_e32 v37, v37, v52
	v_mul_f32_e32 v52, v69, v69
	v_fmac_f32_e32 v52, v68, v68
	v_add_f32_e32 v37, v52, v37
	v_mul_f32_e32 v52, v77, v77
	v_lshl_add_u64 v[116:117], s[20:21], 0, v[40:41]
	v_fmac_f32_e32 v52, v76, v76
	v_or_b32_e32 v40, 0x100, v40
	v_pk_mul_f32 v[114:115], v[12:13], v[76:77]
	v_cvt_pk_bf16_f32 v60, v60, v61
	v_add_f32_e32 v37, v52, v37
	v_cvt_pk_bf16_f32 v61, v114, v115
	v_lshl_add_u64 v[52:53], s[30:31], 0, v[40:41]
	global_store_dwordx4 v[116:117], v[58:61], off
	s_nop 0
	v_lshl_add_u64 v[40:41], s[20:21], 0, v[40:41]
	s_waitcnt vmcnt(21)
	s_nop 1
	v_mov_b32_e32 v58, v226
	v_mov_b32_e32 v59, v227
	v_mov_b32_e32 v60, v228
	v_mov_b32_e32 v61, v229
	global_load_dwordx4 v[226:229], v[248:249], off offset:256
	v_lshlrev_b32_e32 v66, 16, v58
	v_and_b32_e32 v67, 0xffff0000, v58
	v_lshlrev_b32_e32 v58, 16, v59
	v_and_b32_e32 v59, 0xffff0000, v59
	v_lshlrev_b32_e32 v68, 16, v60
	v_and_b32_e32 v69, 0xffff0000, v60
	v_lshlrev_b32_e32 v60, 16, v61
	v_and_b32_e32 v61, 0xffff0000, v61
	v_pk_add_f32 v[74:75], v[112:113], v[58:59]
	v_pk_add_f32 v[66:67], v[110:111], v[66:67]
	v_pk_add_f32 v[76:77], v[108:109], v[60:61]
	v_pk_add_f32 v[68:69], v[106:107], v[68:69]
	v_cvt_pk_bf16_f32 v58, v66, v67
	v_cvt_pk_bf16_f32 v59, v74, v75
	v_pk_mul_f32 v[106:107], v[4:5], v[76:77]
	v_cvt_pk_bf16_f32 v60, v68, v69
	v_cvt_pk_bf16_f32 v61, v76, v77
	global_store_dwordx4 v[52:53], v[58:61], off
	v_pk_mul_f32 v[52:53], v[8:9], v[74:75]
	s_nop 0
	v_pk_mul_f32 v[58:59], v[6:7], v[66:67]
	v_pk_mul_f32 v[60:61], v[2:3], v[68:69]
	v_cvt_pk_bf16_f32 v58, v58, v59
	v_cvt_pk_bf16_f32 v59, v52, v53
	s_nop 0
	v_cvt_pk_bf16_f32 v60, v60, v61
	v_cvt_pk_bf16_f32 v61, v106, v107
	global_store_dwordx4 v[40:41], v[58:61], off
	v_mul_f32_e32 v40, v67, v67
	v_mul_f32_e32 v41, v75, v75
	v_fmac_f32_e32 v40, v66, v66
	v_fmac_f32_e32 v41, v74, v74
	v_add_f32_e32 v40, v40, v41
	v_mul_f32_e32 v41, v69, v69
	v_fmac_f32_e32 v41, v68, v68
	v_add_f32_e32 v40, v41, v40
	v_mul_f32_e32 v41, v77, v77
	v_fmac_f32_e32 v41, v76, v76
	v_add_f32_e32 v40, v41, v40
	v_add_f32_e32 v37, v37, v40
	ds_bpermute_b32 v40, v50, v37
	s_waitcnt lgkmcnt(0)
	v_add_f32_e32 v37, v37, v40
	ds_bpermute_b32 v40, v51, v37
	s_and_saveexec_b64 s[82:83], s[0:1]
	s_cbranch_execz .LBB0_1161
	s_waitcnt lgkmcnt(0)
	v_add_f32_e32 v37, v37, v40
	v_mul_f32_e32 v37, 0x4b800000, v37
	v_trunc_f32_e32 v37, v37
	v_mul_f32_e32 v40, 0x2f800000, v37
	v_floor_f32_e32 v41, v40
	v_fmac_f32_e32 v37, 0xcf800000, v41
	v_cvt_u32_f32_e32 v40, v37
	v_cvt_u32_f32_e32 v41, v41
	v_lshl_add_u64 v[38:39], v[38:39], 3, s[6:7]
	global_atomic_add_x2 v[38:39], v[40:41], off
; __device__ __forceinline__ unsigned pk4_fp8(float a, float b, float c, float d) { int w = 0; w = __builtin_amdgcn_cvt_pk_fp8_f32(a, b, w, false); w = __builtin_amdgcn_cvt_pk_fp8_f32(c, d, w, true); return (unsigned)w; }
; __device__ __forceinline__ u32x4 pack8(f32x4 v0, f32x4 v1) { u32x4 w; w.x = cvt_pk_bf16(v0[0], v0[1]); w.y = cvt_pk_bf16(v0[2], v0[3]); w.z = cvt_pk_bf16(v1[0], v1[1]); w.w = cvt_pk_bf16(v1[2], v1[3]); return w; }
; template <class T> __device__ __forceinline__ void est(T* p, T v) { if constexpr (MK_EPI_NT != 0) __builtin_nontemporal_store(v, p); else *p = v; }
; __device__ __forceinline__ void unpack8(u32x4 w, f32x4& v0, f32x4& v1) { v0 = (f32x4){bf_lo(w.x), bf_hi(w.x), bf_lo(w.y), bf_hi(w.y)}; v1 = (f32x4){bf_lo(w.z), bf_hi(w.z), bf_lo(w.w), bf_hi(w.w)}; }
; __device__ __forceinline__ float sum8sq(f32x4 a, f32x4 b) { return (a[0] * a[0] + a[1] * a[1]) + (a[2] * a[2] + a[3] * a[3]) + (b[0] * b[0] + b[1] * b[1]) + (b[2] * b[2] + b[3] * b[3]); }
; __device__ __forceinline__ void row_atomic(ss_t* ss, int row, float sq, int fq) { sq += __shfl_xor(sq, 16); sq += __shfl_xor(sq, 32); if (fq == 0) atomicAdd(ss + row, ss_fix(sq)); }
;     __device__ __forceinline__ void operator()(AccT acc, const Unit& u, int wr, int wc, int fr, int fq) const {
;     ...
;             for (int m = 0; m < 4; ++m) { const int row = row0 + ai * 128 + m * 16; float sq = 0.f;
; #pragma unroll
;                 for (int bj = 0; bj < 2; ++bj) { const size_t o = (size_t)row * DM + col0 + bj * 128;
;                     f32x4 r0, r1; if constexpr (RIN16) unpack8(*(const u32x4*)((const bf16_t*)Xin + o), r0, r1); else { r0 = *(const f32x4*)((const float*)Xin + o); r1 = *(const f32x4*)((const float*)Xin + o + 4); }
;                     const f32x4 x0 = r0 + acc[ai][bj][m][0] * ascale, x1 = r1 + acc[ai][bj][m][1] * ascale;
;                     est((u32x4*)(Xout + o), (u32x4)pack8(x0, x1));
;                     const f32x4 y0 = x0 * gv[bj][0], y1 = x1 * gv[bj][1];
;                     if constexpr (F8OUT) est((u32x2*)((unsigned char*)XB + o), (u32x2)(u32x2){pk4_fp8(y0[0], y0[1], y0[2], y0[3]), pk4_fp8(y1[0], y1[1], y1[2], y1[3])});
;                     else est((u32x4*)((bf16_t*)XB + o), (u32x4)pack8(y0, y1));
;                     sq += sum8sq(x0, x1); }
;                 row_atomic(ss, row, sq, fq); }
.LBB0_1161:
	s_or_b64 exec, exec, s[82:83]
	v_add_u32_e32 v38, 0x80, v36
	v_ashrrev_i32_e32 v39, 31, v38
	s_waitcnt lgkmcnt(0)
	v_lshlrev_b64 v[40:41], 11, v[38:39]
	v_lshl_add_u64 v[40:41], v[40:41], 0, v[34:35]
	v_lshlrev_b64 v[40:41], 1, v[40:41]
	v_lshl_add_u64 v[52:53], s[30:31], 0, v[40:41]
	s_nop 0
	v_readlane_b32 s20, v247, 55
	v_readlane_b32 s21, v247, 56
	s_waitcnt vmcnt(23)
	s_nop 1
	v_mov_b32_e32 v58, v198
	v_mov_b32_e32 v59, v199
	v_mov_b32_e32 v60, v200
	v_mov_b32_e32 v61, v201
	v_lshlrev_b32_e32 v66, 16, v58
	v_and_b32_e32 v67, 0xffff0000, v58
	v_lshlrev_b32_e32 v58, 16, v59
	v_and_b32_e32 v59, 0xffff0000, v59
	v_lshlrev_b32_e32 v68, 16, v60
	v_and_b32_e32 v69, 0xffff0000, v60
	v_lshlrev_b32_e32 v60, 16, v61
	v_and_b32_e32 v61, 0xffff0000, v61
	v_pk_add_f32 v[74:75], v[98:99], v[58:59]
	v_pk_add_f32 v[66:67], v[100:101], v[66:67]
	v_pk_add_f32 v[76:77], v[102:103], v[60:61]
	v_cvt_pk_bf16_f32 v58, v66, v67
	v_cvt_pk_bf16_f32 v59, v74, v75
	v_pk_add_f32 v[68:69], v[104:105], v[68:69]
	v_mul_f32_e32 v37, v67, v67
	v_cvt_pk_bf16_f32 v60, v68, v69
	v_cvt_pk_bf16_f32 v61, v76, v77
	global_store_dwordx4 v[52:53], v[58:61], off
	v_pk_mul_f32 v[52:53], v[16:17], v[74:75]
	v_fmac_f32_e32 v37, v66, v66
	v_pk_mul_f32 v[58:59], v[14:15], v[66:67]
	v_pk_mul_f32 v[60:61], v[10:11], v[68:69]
	v_cvt_pk_bf16_f32 v58, v58, v59
	v_cvt_pk_bf16_f32 v59, v52, v53
	v_mul_f32_e32 v52, v75, v75
	v_fmac_f32_e32 v52, v74, v74
	v_add_f32_e32 v37, v37, v52
	v_mul_f32_e32 v52, v69, v69
	v_fmac_f32_e32 v52, v68, v68
	v_add_f32_e32 v37, v52, v37
	v_mul_f32_e32 v52, v77, v77
	v_lshl_add_u64 v[100:101], s[20:21], 0, v[40:41]
	v_fmac_f32_e32 v52, v76, v76
	v_or_b32_e32 v40, 0x100, v40
	v_pk_mul_f32 v[98:99], v[12:13], v[76:77]
	v_cvt_pk_bf16_f32 v60, v60, v61
	v_add_f32_e32 v37, v52, v37
	v_cvt_pk_bf16_f32 v61, v98, v99
	v_lshl_add_u64 v[52:53], s[30:31], 0, v[40:41]
	global_store_dwordx4 v[100:101], v[58:61], off
	s_nop 0
	v_lshl_add_u64 v[40:41], s[20:21], 0, v[40:41]
	s_waitcnt vmcnt(22)
	s_nop 1
	v_mov_b32_e32 v58, v202
	v_mov_b32_e32 v59, v203
	v_mov_b32_e32 v60, v204
	v_mov_b32_e32 v61, v205
	v_lshlrev_b32_e32 v66, 16, v58
	v_and_b32_e32 v67, 0xffff0000, v58
	v_lshlrev_b32_e32 v58, 16, v59
	v_and_b32_e32 v59, 0xffff0000, v59
	v_lshlrev_b32_e32 v68, 16, v60
	v_and_b32_e32 v69, 0xffff0000, v60
	v_lshlrev_b32_e32 v60, 16, v61
	v_and_b32_e32 v61, 0xffff0000, v61
	v_pk_add_f32 v[74:75], v[96:97], v[58:59]
	v_pk_add_f32 v[66:67], v[94:95], v[66:67]
	v_pk_add_f32 v[76:77], v[92:93], v[60:61]
	v_pk_add_f32 v[68:69], v[90:91], v[68:69]
	v_cvt_pk_bf16_f32 v58, v66, v67
	v_cvt_pk_bf16_f32 v59, v74, v75
	v_pk_mul_f32 v[90:91], v[4:5], v[76:77]
	v_cvt_pk_bf16_f32 v60, v68, v69
	v_cvt_pk_bf16_f32 v61, v76, v77
	global_store_dwordx4 v[52:53], v[58:61], off
	v_pk_mul_f32 v[52:53], v[8:9], v[74:75]
	s_nop 0
	v_pk_mul_f32 v[58:59], v[6:7], v[66:67]
	v_pk_mul_f32 v[60:61], v[2:3], v[68:69]
	v_cvt_pk_bf16_f32 v58, v58, v59
	v_cvt_pk_bf16_f32 v59, v52, v53
	s_nop 0
	v_cvt_pk_bf16_f32 v60, v60, v61
	v_cvt_pk_bf16_f32 v61, v90, v91
	global_store_dwordx4 v[40:41], v[58:61], off
	v_mul_f32_e32 v40, v67, v67
	v_mul_f32_e32 v41, v75, v75
	v_fmac_f32_e32 v40, v66, v66
	v_fmac_f32_e32 v41, v74, v74
	v_add_f32_e32 v40, v40, v41
	v_mul_f32_e32 v41, v69, v69
	v_fmac_f32_e32 v41, v68, v68
	v_add_f32_e32 v40, v41, v40
	v_mul_f32_e32 v41, v77, v77
	v_fmac_f32_e32 v41, v76, v76
	v_add_f32_e32 v40, v41, v40
	v_add_f32_e32 v37, v37, v40
	ds_bpermute_b32 v40, v50, v37
	s_waitcnt lgkmcnt(0)
	v_add_f32_e32 v37, v37, v40
	ds_bpermute_b32 v40, v51, v37
	s_and_saveexec_b64 s[82:83], s[0:1]
	s_cbranch_execz .LBB0_1163
	s_waitcnt lgkmcnt(0)
	v_add_f32_e32 v37, v37, v40
	v_mul_f32_e32 v37, 0x4b800000, v37
	v_trunc_f32_e32 v37, v37
	v_mul_f32_e32 v40, 0x2f800000, v37
	v_floor_f32_e32 v41, v40
	v_fmac_f32_e32 v37, 0xcf800000, v41
	v_cvt_u32_f32_e32 v40, v37
	v_cvt_u32_f32_e32 v41, v41
	v_lshl_add_u64 v[38:39], v[38:39], 3, s[6:7]
	global_atomic_add_x2 v[38:39], v[40:41], off
.LBB0_1163:
	s_or_b64 exec, exec, s[82:83]
	v_add_u32_e32 v38, 0x90, v36
	v_ashrrev_i32_e32 v39, 31, v38
	s_waitcnt lgkmcnt(0)
	v_lshlrev_b64 v[40:41], 11, v[38:39]
	v_lshl_add_u64 v[40:41], v[40:41], 0, v[34:35]
	v_lshlrev_b64 v[40:41], 1, v[40:41]
	v_lshl_add_u64 v[52:53], s[30:31], 0, v[40:41]
	s_nop 0
	v_readlane_b32 s20, v247, 55
	v_readlane_b32 s21, v247, 56
	s_waitcnt vmcnt(21)
	s_nop 1
	v_mov_b32_e32 v58, v206
	v_mov_b32_e32 v59, v207
	v_mov_b32_e32 v60, v208
	v_mov_b32_e32 v61, v209
	v_lshlrev_b32_e32 v66, 16, v58
	v_and_b32_e32 v67, 0xffff0000, v58
	v_lshlrev_b32_e32 v58, 16, v59
	v_and_b32_e32 v59, 0xffff0000, v59
	v_lshlrev_b32_e32 v68, 16, v60
	v_and_b32_e32 v69, 0xffff0000, v60
	v_lshlrev_b32_e32 v60, 16, v61
	v_and_b32_e32 v61, 0xffff0000, v61
	v_pk_add_f32 v[74:75], v[88:89], v[58:59]
	v_pk_add_f32 v[66:67], v[86:87], v[66:67]
	v_pk_add_f32 v[76:77], v[84:85], v[60:61]
	v_cvt_pk_bf16_f32 v58, v66, v67
	v_cvt_pk_bf16_f32 v59, v74, v75
	v_pk_add_f32 v[68:69], v[82:83], v[68:69]
	v_mul_f32_e32 v37, v67, v67
	v_cvt_pk_bf16_f32 v60, v68, v69
	v_cvt_pk_bf16_f32 v61, v76, v77
	global_store_dwordx4 v[52:53], v[58:61], off
	v_pk_mul_f32 v[52:53], v[16:17], v[74:75]
	v_fmac_f32_e32 v37, v66, v66
	v_pk_mul_f32 v[58:59], v[14:15], v[66:67]
	v_pk_mul_f32 v[60:61], v[10:11], v[68:69]
	v_cvt_pk_bf16_f32 v58, v58, v59
	v_cvt_pk_bf16_f32 v59, v52, v53
	v_mul_f32_e32 v52, v75, v75
	v_fmac_f32_e32 v52, v74, v74
	v_add_f32_e32 v37, v37, v52
	v_mul_f32_e32 v52, v69, v69
	v_fmac_f32_e32 v52, v68, v68
	v_add_f32_e32 v37, v52, v37
	v_mul_f32_e32 v52, v77, v77
	v_lshl_add_u64 v[84:85], s[20:21], 0, v[40:41]
	v_fmac_f32_e32 v52, v76, v76
	v_or_b32_e32 v40, 0x100, v40
	v_pk_mul_f32 v[82:83], v[12:13], v[76:77]
	v_cvt_pk_bf16_f32 v60, v60, v61
	v_add_f32_e32 v37, v52, v37
	v_cvt_pk_bf16_f32 v61, v82, v83
	v_lshl_add_u64 v[52:53], s[30:31], 0, v[40:41]
	global_store_dwordx4 v[84:85], v[58:61], off
	s_nop 0
	v_lshl_add_u64 v[40:41], s[20:21], 0, v[40:41]
	s_waitcnt vmcnt(20)
; __device__ __forceinline__ unsigned pk4_fp8(float a, float b, float c, float d) { int w = 0; w = __builtin_amdgcn_cvt_pk_fp8_f32(a, b, w, false); w = __builtin_amdgcn_cvt_pk_fp8_f32(c, d, w, true); return (unsigned)w; }
; __device__ __forceinline__ u32x4 pack8(f32x4 v0, f32x4 v1) { u32x4 w; w.x = cvt_pk_bf16(v0[0], v0[1]); w.y = cvt_pk_bf16(v0[2], v0[3]); w.z = cvt_pk_bf16(v1[0], v1[1]); w.w = cvt_pk_bf16(v1[2], v1[3]); return w; }
; template <class T> __device__ __forceinline__ void est(T* p, T v) { if constexpr (MK_EPI_NT != 0) __builtin_nontemporal_store(v, p); else *p = v; }
; __device__ __forceinline__ void unpack8(u32x4 w, f32x4& v0, f32x4& v1) { v0 = (f32x4){bf_lo(w.x), bf_hi(w.x), bf_lo(w.y), bf_hi(w.y)}; v1 = (f32x4){bf_lo(w.z), bf_hi(w.z), bf_lo(w.w), bf_hi(w.w)}; }
; __device__ __forceinline__ float sum8sq(f32x4 a, f32x4 b) { return (a[0] * a[0] + a[1] * a[1]) + (a[2] * a[2] + a[3] * a[3]) + (b[0] * b[0] + b[1] * b[1]) + (b[2] * b[2] + b[3] * b[3]); }
; __device__ __forceinline__ void row_atomic(ss_t* ss, int row, float sq, int fq) { sq += __shfl_xor(sq, 16); sq += __shfl_xor(sq, 32); if (fq == 0) atomicAdd(ss + row, ss_fix(sq)); }
;     __device__ __forceinline__ void operator()(AccT acc, const Unit& u, int wr, int wc, int fr, int fq) const {
;     ...
;             for (int m = 0; m < 4; ++m) { const int row = row0 + ai * 128 + m * 16; float sq = 0.f;
; #pragma unroll
;                 for (int bj = 0; bj < 2; ++bj) { const size_t o = (size_t)row * DM + col0 + bj * 128;
;                     f32x4 r0, r1; if constexpr (RIN16) unpack8(*(const u32x4*)((const bf16_t*)Xin + o), r0, r1); else { r0 = *(const f32x4*)((const float*)Xin + o); r1 = *(const f32x4*)((const float*)Xin + o + 4); }
;                     const f32x4 x0 = r0 + acc[ai][bj][m][0] * ascale, x1 = r1 + acc[ai][bj][m][1] * ascale;
;                     est((u32x4*)(Xout + o), (u32x4)pack8(x0, x1));
;                     const f32x4 y0 = x0 * gv[bj][0], y1 = x1 * gv[bj][1];
;                     if constexpr (F8OUT) est((u32x2*)((unsigned char*)XB + o), (u32x2)(u32x2){pk4_fp8(y0[0], y0[1], y0[2], y0[3]), pk4_fp8(y1[0], y1[1], y1[2], y1[3])});
;                     else est((u32x4*)((bf16_t*)XB + o), (u32x4)pack8(y0, y1));
;                     sq += sum8sq(x0, x1); }
;                 row_atomic(ss, row, sq, fq); }
	s_nop 1
	v_mov_b32_e32 v58, v210
	v_mov_b32_e32 v59, v211
	v_mov_b32_e32 v60, v212
	v_mov_b32_e32 v61, v213
	v_lshlrev_b32_e32 v66, 16, v58
	v_and_b32_e32 v67, 0xffff0000, v58
	v_lshlrev_b32_e32 v58, 16, v59
	v_and_b32_e32 v59, 0xffff0000, v59
	v_lshlrev_b32_e32 v68, 16, v60
	v_and_b32_e32 v69, 0xffff0000, v60
	v_lshlrev_b32_e32 v60, 16, v61
	v_and_b32_e32 v61, 0xffff0000, v61
	v_pk_add_f32 v[74:75], v[80:81], v[58:59]
	v_pk_add_f32 v[66:67], v[78:79], v[66:67]
	v_pk_add_f32 v[72:73], v[72:73], v[60:61]
	v_pk_add_f32 v[68:69], v[70:71], v[68:69]
	v_cvt_pk_bf16_f32 v58, v66, v67
	v_cvt_pk_bf16_f32 v59, v74, v75
	v_pk_mul_f32 v[70:71], v[4:5], v[72:73]
	v_cvt_pk_bf16_f32 v60, v68, v69
	v_cvt_pk_bf16_f32 v61, v72, v73
	global_store_dwordx4 v[52:53], v[58:61], off
	v_pk_mul_f32 v[52:53], v[8:9], v[74:75]
	s_nop 0
	v_pk_mul_f32 v[58:59], v[6:7], v[66:67]
	v_pk_mul_f32 v[60:61], v[2:3], v[68:69]
	v_cvt_pk_bf16_f32 v58, v58, v59
	v_cvt_pk_bf16_f32 v59, v52, v53
	s_nop 0
	v_cvt_pk_bf16_f32 v60, v60, v61
	v_cvt_pk_bf16_f32 v61, v70, v71
	global_store_dwordx4 v[40:41], v[58:61], off
	v_mul_f32_e32 v40, v67, v67
	v_mul_f32_e32 v41, v75, v75
	v_fmac_f32_e32 v40, v66, v66
	v_fmac_f32_e32 v41, v74, v74
	v_add_f32_e32 v40, v40, v41
	v_mul_f32_e32 v41, v69, v69
	v_fmac_f32_e32 v41, v68, v68
	v_add_f32_e32 v40, v41, v40
	v_mul_f32_e32 v41, v73, v73
	v_fmac_f32_e32 v41, v72, v72
	v_add_f32_e32 v40, v41, v40
	v_add_f32_e32 v37, v37, v40
	ds_bpermute_b32 v40, v50, v37
	s_waitcnt lgkmcnt(0)
	v_add_f32_e32 v37, v37, v40
	ds_bpermute_b32 v40, v51, v37
	s_and_saveexec_b64 s[82:83], s[0:1]
	s_cbranch_execz .LBB0_1165
	s_waitcnt lgkmcnt(0)
	v_add_f32_e32 v37, v37, v40
	v_mul_f32_e32 v37, 0x4b800000, v37
	v_trunc_f32_e32 v37, v37
	v_mul_f32_e32 v40, 0x2f800000, v37
	v_floor_f32_e32 v41, v40
	v_fmac_f32_e32 v37, 0xcf800000, v41
	v_cvt_u32_f32_e32 v40, v37
	v_cvt_u32_f32_e32 v41, v41
	v_lshl_add_u64 v[38:39], v[38:39], 3, s[6:7]
	global_atomic_add_x2 v[38:39], v[40:41], off
.LBB0_1165:
	s_or_b64 exec, exec, s[82:83]
	v_add_u32_e32 v38, 0xa0, v36
	v_ashrrev_i32_e32 v39, 31, v38
	s_waitcnt lgkmcnt(0)
	v_lshlrev_b64 v[40:41], 11, v[38:39]
	v_lshl_add_u64 v[40:41], v[40:41], 0, v[34:35]
	v_lshlrev_b64 v[40:41], 1, v[40:41]
	v_lshl_add_u64 v[66:67], s[30:31], 0, v[40:41]
	s_nop 0
	v_readlane_b32 s20, v247, 55
	v_readlane_b32 s21, v247, 56
	s_waitcnt vmcnt(19)
	s_nop 1
	v_mov_b32_e32 v58, v214
	v_mov_b32_e32 v59, v215
	v_mov_b32_e32 v60, v216
	v_mov_b32_e32 v61, v217
	v_lshlrev_b32_e32 v52, 16, v58
	v_and_b32_e32 v53, 0xffff0000, v58
	v_lshlrev_b32_e32 v58, 16, v59
	v_and_b32_e32 v59, 0xffff0000, v59
	v_lshlrev_b32_e32 v68, 16, v60
	v_and_b32_e32 v69, 0xffff0000, v60
	v_lshlrev_b32_e32 v60, 16, v61
	v_and_b32_e32 v61, 0xffff0000, v61
	v_pk_add_f32 v[58:59], v[54:55], v[58:59]
	v_pk_add_f32 v[56:57], v[56:57], v[52:53]
	v_pk_add_f32 v[60:61], v[62:63], v[60:61]
	v_cvt_pk_bf16_f32 v52, v56, v57
	v_cvt_pk_bf16_f32 v53, v58, v59
	v_pk_add_f32 v[62:63], v[64:65], v[68:69]
	v_lshl_add_u64 v[68:69], s[20:21], 0, v[40:41]
	v_cvt_pk_bf16_f32 v54, v62, v63
	v_cvt_pk_bf16_f32 v55, v60, v61
	global_store_dwordx4 v[66:67], v[52:55], off
	v_pk_mul_f32 v[64:65], v[12:13], v[60:61]
	v_pk_mul_f32 v[66:67], v[10:11], v[62:63]
	v_pk_mul_f32 v[52:53], v[14:15], v[56:57]
	v_pk_mul_f32 v[54:55], v[16:17], v[58:59]
	v_cvt_pk_bf16_f32 v52, v52, v53
	v_mul_f32_e32 v37, v57, v57
	v_cvt_pk_bf16_f32 v53, v54, v55
	v_cvt_pk_bf16_f32 v54, v66, v67
	v_cvt_pk_bf16_f32 v55, v64, v65
	global_store_dwordx4 v[68:69], v[52:55], off
	v_fmac_f32_e32 v37, v56, v56
	v_or_b32_e32 v40, 0x100, v40
	v_mul_f32_e32 v52, v59, v59
	v_fmac_f32_e32 v52, v58, v58
	v_add_f32_e32 v37, v37, v52
	v_mul_f32_e32 v52, v63, v63
	v_fmac_f32_e32 v52, v62, v62
	v_add_f32_e32 v37, v52, v37
	v_mul_f32_e32 v52, v61, v61
	v_fmac_f32_e32 v52, v60, v60
	v_lshl_add_u64 v[56:57], s[30:31], 0, v[40:41]
	v_add_f32_e32 v37, v52, v37
	s_nop 0
	s_waitcnt vmcnt(18)
	s_nop 1
	v_mov_b32_e32 v52, v218
	v_mov_b32_e32 v53, v219
	v_mov_b32_e32 v54, v220
	v_mov_b32_e32 v55, v221
	v_lshlrev_b32_e32 v58, 16, v52
	v_and_b32_e32 v59, 0xffff0000, v52
	v_lshlrev_b32_e32 v52, 16, v53
	v_and_b32_e32 v53, 0xffff0000, v53
	v_lshlrev_b32_e32 v60, 16, v54
	v_and_b32_e32 v61, 0xffff0000, v54
	v_lshlrev_b32_e32 v54, 16, v55
	v_and_b32_e32 v55, 0xffff0000, v55
	v_pk_add_f32 v[48:49], v[48:49], v[52:53]
	v_pk_add_f32 v[46:47], v[46:47], v[58:59]
	v_pk_add_f32 v[52:53], v[44:45], v[54:55]
	v_pk_add_f32 v[54:55], v[42:43], v[60:61]
	v_cvt_pk_bf16_f32 v42, v46, v47
	v_cvt_pk_bf16_f32 v43, v48, v49
	v_lshl_add_u64 v[60:61], s[20:21], 0, v[40:41]
	v_cvt_pk_bf16_f32 v44, v54, v55
	v_cvt_pk_bf16_f32 v45, v52, v53
	global_store_dwordx4 v[56:57], v[42:45], off
	v_pk_mul_f32 v[56:57], v[4:5], v[52:53]
	v_pk_mul_f32 v[58:59], v[2:3], v[54:55]
	v_pk_mul_f32 v[42:43], v[8:9], v[48:49]
	v_pk_mul_f32 v[44:45], v[6:7], v[46:47]
	s_nop 0
	v_cvt_pk_bf16_f32 v40, v44, v45
	v_cvt_pk_bf16_f32 v41, v42, v43
	v_cvt_pk_bf16_f32 v42, v58, v59
	v_cvt_pk_bf16_f32 v43, v56, v57
	global_store_dwordx4 v[60:61], v[40:43], off
	s_nop 1
	v_mul_f32_e32 v40, v47, v47
	v_mul_f32_e32 v41, v49, v49
	v_fmac_f32_e32 v40, v46, v46
	v_fmac_f32_e32 v41, v48, v48
	v_add_f32_e32 v40, v40, v41
	v_mul_f32_e32 v41, v55, v55
	v_fmac_f32_e32 v41, v54, v54
	v_add_f32_e32 v40, v41, v40
	v_mul_f32_e32 v41, v53, v53
	v_fmac_f32_e32 v41, v52, v52
	v_add_f32_e32 v40, v41, v40
	v_add_f32_e32 v37, v37, v40
	ds_bpermute_b32 v40, v50, v37
	s_waitcnt lgkmcnt(0)
	v_add_f32_e32 v37, v37, v40
	ds_bpermute_b32 v40, v51, v37
	s_and_saveexec_b64 s[82:83], s[0:1]
	s_cbranch_execz .LBB0_1167
	s_waitcnt lgkmcnt(0)
	v_add_f32_e32 v37, v37, v40
	v_mul_f32_e32 v37, 0x4b800000, v37
	v_trunc_f32_e32 v37, v37
	v_mul_f32_e32 v40, 0x2f800000, v37
	v_floor_f32_e32 v41, v40
	v_fmac_f32_e32 v37, 0xcf800000, v41
	v_cvt_u32_f32_e32 v40, v37
	v_cvt_u32_f32_e32 v41, v41
	v_lshl_add_u64 v[38:39], v[38:39], 3, s[6:7]
	global_atomic_add_x2 v[38:39], v[40:41], off
; __device__ __forceinline__ unsigned pk4_fp8(float a, float b, float c, float d) { int w = 0; w = __builtin_amdgcn_cvt_pk_fp8_f32(a, b, w, false); w = __builtin_amdgcn_cvt_pk_fp8_f32(c, d, w, true); return (unsigned)w; }
; __device__ __forceinline__ u32x4 pack8(f32x4 v0, f32x4 v1) { u32x4 w; w.x = cvt_pk_bf16(v0[0], v0[1]); w.y = cvt_pk_bf16(v0[2], v0[3]); w.z = cvt_pk_bf16(v1[0], v1[1]); w.w = cvt_pk_bf16(v1[2], v1[3]); return w; }
; template <class T> __device__ __forceinline__ void est(T* p, T v) { if constexpr (MK_EPI_NT != 0) __builtin_nontemporal_store(v, p); else *p = v; }
; __device__ __forceinline__ void unpack8(u32x4 w, f32x4& v0, f32x4& v1) { v0 = (f32x4){bf_lo(w.x), bf_hi(w.x), bf_lo(w.y), bf_hi(w.y)}; v1 = (f32x4){bf_lo(w.z), bf_hi(w.z), bf_lo(w.w), bf_hi(w.w)}; }
; __device__ __forceinline__ float sum8sq(f32x4 a, f32x4 b) { return (a[0] * a[0] + a[1] * a[1]) + (a[2] * a[2] + a[3] * a[3]) + (b[0] * b[0] + b[1] * b[1]) + (b[2] * b[2] + b[3] * b[3]); }
; __device__ __forceinline__ void row_atomic(ss_t* ss, int row, float sq, int fq) { sq += __shfl_xor(sq, 16); sq += __shfl_xor(sq, 32); if (fq == 0) atomicAdd(ss + row, ss_fix(sq)); }
;     __device__ __forceinline__ void operator()(AccT acc, const Unit& u, int wr, int wc, int fr, int fq) const {
;     ...
;             for (int m = 0; m < 4; ++m) { const int row = row0 + ai * 128 + m * 16; float sq = 0.f;
; #pragma unroll
;                 for (int bj = 0; bj < 2; ++bj) { const size_t o = (size_t)row * DM + col0 + bj * 128;
;                     f32x4 r0, r1; if constexpr (RIN16) unpack8(*(const u32x4*)((const bf16_t*)Xin + o), r0, r1); else { r0 = *(const f32x4*)((const float*)Xin + o); r1 = *(const f32x4*)((const float*)Xin + o + 4); }
;                     const f32x4 x0 = r0 + acc[ai][bj][m][0] * ascale, x1 = r1 + acc[ai][bj][m][1] * ascale;
;                     est((u32x4*)(Xout + o), (u32x4)pack8(x0, x1));
;                     const f32x4 y0 = x0 * gv[bj][0], y1 = x1 * gv[bj][1];
;                     if constexpr (F8OUT) est((u32x2*)((unsigned char*)XB + o), (u32x2)(u32x2){pk4_fp8(y0[0], y0[1], y0[2], y0[3]), pk4_fp8(y1[0], y1[1], y1[2], y1[3])});
;                     else est((u32x4*)((bf16_t*)XB + o), (u32x4)pack8(y0, y1));
;                     sq += sum8sq(x0, x1); }
;                 row_atomic(ss, row, sq, fq); }
.LBB0_1167:
	s_or_b64 exec, exec, s[82:83]
	v_add_u32_e32 v36, 0xb0, v36
	v_ashrrev_i32_e32 v37, 31, v36
	v_lshlrev_b64 v[38:39], 11, v[36:37]
	v_lshl_add_u64 v[34:35], v[38:39], 0, v[34:35]
	v_lshlrev_b64 v[34:35], 1, v[34:35]
	v_lshl_add_u64 v[42:43], s[30:31], 0, v[34:35]
	s_waitcnt lgkmcnt(0)
	s_nop 0
	v_readlane_b32 s20, v247, 55
	v_readlane_b32 s21, v247, 56
	s_waitcnt vmcnt(17)
	s_nop 1
	v_mov_b32_e32 v38, v222
	v_mov_b32_e32 v39, v223
	v_mov_b32_e32 v40, v224
	v_mov_b32_e32 v41, v225
	v_lshlrev_b32_e32 v44, 16, v38
	v_and_b32_e32 v45, 0xffff0000, v38
	v_lshlrev_b32_e32 v38, 16, v39
	v_and_b32_e32 v39, 0xffff0000, v39
	v_lshlrev_b32_e32 v46, 16, v40
	v_and_b32_e32 v47, 0xffff0000, v40
	v_lshlrev_b32_e32 v40, 16, v41
	v_and_b32_e32 v41, 0xffff0000, v41
	v_pk_add_f32 v[38:39], v[26:27], v[38:39]
	v_pk_add_f32 v[44:45], v[28:29], v[44:45]
	v_pk_add_f32 v[30:31], v[30:31], v[40:41]
	v_pk_add_f32 v[32:33], v[32:33], v[46:47]
	v_cvt_pk_bf16_f32 v26, v44, v45
	v_cvt_pk_bf16_f32 v27, v38, v39
	v_pk_mul_f32 v[16:17], v[16:17], v[38:39]
	v_cvt_pk_bf16_f32 v28, v32, v33
	v_cvt_pk_bf16_f32 v29, v30, v31
	global_store_dwordx4 v[42:43], v[26:29], off
	v_pk_mul_f32 v[14:15], v[14:15], v[44:45]
	s_nop 0
	v_pk_mul_f32 v[26:27], v[12:13], v[30:31]
	v_pk_mul_f32 v[12:13], v[10:11], v[32:33]
	v_lshl_add_u64 v[28:29], s[20:21], 0, v[34:35]
	v_cvt_pk_bf16_f32 v10, v14, v15
	v_cvt_pk_bf16_f32 v11, v16, v17
	v_cvt_pk_bf16_f32 v12, v12, v13
	v_cvt_pk_bf16_f32 v13, v26, v27
	global_store_dwordx4 v[28:29], v[10:13], off
	v_or_b32_e32 v34, 0x100, v34
	v_lshl_add_u64 v[14:15], s[30:31], 0, v[34:35]
	v_mul_f32_e32 v10, v45, v45
	v_mul_f32_e32 v11, v39, v39
	v_fmac_f32_e32 v10, v44, v44
	v_fmac_f32_e32 v11, v38, v38
	v_add_f32_e32 v10, v10, v11
	v_mul_f32_e32 v11, v33, v33
	v_fmac_f32_e32 v11, v32, v32
	v_add_f32_e32 v10, v11, v10
	v_mul_f32_e32 v11, v31, v31
	v_fmac_f32_e32 v11, v30, v30
	v_add_f32_e32 v28, v11, v10
	s_nop 0
	s_waitcnt vmcnt(16)
	s_nop 1
	v_mov_b32_e32 v10, v226
	v_mov_b32_e32 v11, v227
	v_mov_b32_e32 v12, v228
	v_mov_b32_e32 v13, v229
	v_lshlrev_b32_e32 v16, 16, v10
	v_and_b32_e32 v17, 0xffff0000, v10
	v_lshlrev_b32_e32 v10, 16, v11
	v_and_b32_e32 v11, 0xffff0000, v11
	v_lshlrev_b32_e32 v26, 16, v12
	v_and_b32_e32 v27, 0xffff0000, v12
	v_lshlrev_b32_e32 v12, 16, v13
	v_and_b32_e32 v13, 0xffff0000, v13
	v_pk_add_f32 v[24:25], v[24:25], v[10:11]
	v_pk_add_f32 v[16:17], v[22:23], v[16:17]
	v_pk_add_f32 v[20:21], v[20:21], v[12:13]
	v_pk_add_f32 v[18:19], v[18:19], v[26:27]
	v_cvt_pk_bf16_f32 v10, v16, v17
	v_cvt_pk_bf16_f32 v11, v24, v25
	v_pk_mul_f32 v[8:9], v[8:9], v[24:25]
	v_cvt_pk_bf16_f32 v12, v18, v19
	v_cvt_pk_bf16_f32 v13, v20, v21
	global_store_dwordx4 v[14:15], v[10:13], off
	v_pk_mul_f32 v[6:7], v[6:7], v[16:17]
	s_nop 0
	v_pk_mul_f32 v[10:11], v[4:5], v[20:21]
	v_pk_mul_f32 v[4:5], v[2:3], v[18:19]
	v_lshl_add_u64 v[12:13], s[20:21], 0, v[34:35]
	v_cvt_pk_bf16_f32 v2, v6, v7
	v_cvt_pk_bf16_f32 v3, v8, v9
	v_cvt_pk_bf16_f32 v4, v4, v5
	v_cvt_pk_bf16_f32 v5, v10, v11
	global_store_dwordx4 v[12:13], v[2:5], off
	s_nop 1
	v_mul_f32_e32 v2, v17, v17
	v_mul_f32_e32 v3, v25, v25
	v_fmac_f32_e32 v2, v16, v16
	v_fmac_f32_e32 v3, v24, v24
	v_add_f32_e32 v2, v2, v3
	v_mul_f32_e32 v3, v19, v19
	v_fmac_f32_e32 v3, v18, v18
	v_add_f32_e32 v2, v3, v2
	v_mul_f32_e32 v3, v21, v21
	v_fmac_f32_e32 v3, v20, v20
	v_add_f32_e32 v2, v3, v2
	v_add_f32_e32 v2, v28, v2
	ds_bpermute_b32 v3, v50, v2
	s_waitcnt lgkmcnt(0)
	v_add_f32_e32 v2, v2, v3
	ds_bpermute_b32 v3, v51, v2
	s_and_saveexec_b64 s[82:83], s[0:1]
	s_cbranch_execz .LBB0_1169
	s_waitcnt lgkmcnt(0)
	v_add_f32_e32 v2, v2, v3
	v_mul_f32_e32 v2, 0x4b800000, v2
	v_trunc_f32_e32 v2, v2
	v_mul_f32_e32 v3, 0x2f800000, v2
	v_floor_f32_e32 v3, v3
	v_fmac_f32_e32 v2, 0xcf800000, v3
	v_cvt_u32_f32_e32 v2, v2
	v_cvt_u32_f32_e32 v3, v3
	v_lshl_add_u64 v[4:5], v[36:37], 3, s[6:7]
	global_atomic_add_x2 v[4:5], v[2:3], off

; __device__ __forceinline__ unsigned pk4_fp8(float a, float b, float c, float d) { int w = 0; w = __builtin_amdgcn_cvt_pk_fp8_f32(a, b, w, false); w = __builtin_amdgcn_cvt_pk_fp8_f32(c, d, w, true); return (unsigned)w; }
; __device__ __forceinline__ u32x4 pack8(f32x4 v0, f32x4 v1) { u32x4 w; w.x = cvt_pk_bf16(v0[0], v0[1]); w.y = cvt_pk_bf16(v0[2], v0[3]); w.z = cvt_pk_bf16(v1[0], v1[1]); w.w = cvt_pk_bf16(v1[2], v1[3]); return w; }
; template <class T> __device__ __forceinline__ void est(T* p, T v) { if constexpr (MK_EPI_NT != 0) __builtin_nontemporal_store(v, p); else *p = v; }
; __device__ __forceinline__ void unpack8(u32x4 w, f32x4& v0, f32x4& v1) { v0 = (f32x4){bf_lo(w.x), bf_hi(w.x), bf_lo(w.y), bf_hi(w.y)}; v1 = (f32x4){bf_lo(w.z), bf_hi(w.z), bf_lo(w.w), bf_hi(w.w)}; }
;     __device__ __forceinline__ void operator()(AccT acc, const Unit& u, int wr, int wc, int fr, int fq) const {
;         const int row0 = u.pm * 256 + wr * 64 + fr, col0 = u.pn * 256 + wc * 32 + 8 * fq;
;         f32x4 gv[2][2];
; #pragma unroll
;         for (int bj = 0; bj < 2; ++bj) { gv[bj][0] = *(const f32x4*)(gain + col0 + bj * 128); gv[bj][1] = *(const f32x4*)(gain + col0 + bj * 128 + 4); }
; #pragma unroll
;         for (int ai = 0; ai < 2; ++ai)
; #pragma unroll
;             for (int m = 0; m < 4; ++m) { const int row = row0 + ai * 128 + m * 16; float sq = 0.f;
; #pragma unroll
;                 for (int bj = 0; bj < 2; ++bj) { const size_t o = (size_t)row * DM + col0 + bj * 128;
;                     f32x4 r0, r1; if constexpr (RIN16) unpack8(*(const u32x4*)((const bf16_t*)Xin + o), r0, r1); else { r0 = *(const f32x4*)((const float*)Xin + o); r1 = *(const f32x4*)((const float*)Xin + o + 4); }
;                     const f32x4 x0 = r0 + acc[ai][bj][m][0] * ascale, x1 = r1 + acc[ai][bj][m][1] * ascale;
;                     est((u32x4*)(Xout + o), (u32x4)pack8(x0, x1));
;                     const f32x4 y0 = x0 * gv[bj][0], y1 = x1 * gv[bj][1];
;                     if constexpr (F8OUT) est((u32x2*)((unsigned char*)XB + o), (u32x2)(u32x2){pk4_fp8(y0[0], y0[1], y0[2], y0[3]), pk4_fp8(y1[0], y1[1], y1[2], y1[3])});
;                     else est((u32x4*)((bf16_t*)XB + o), (u32x4)pack8(y0, y1));
;                     sq += sum8sq(x0, x1); }
;                 row_atomic(ss, row, sq, fq); }
.LBB0_1961:
	v_lshl_add_u32 v164, s46, 8, v168
	v_lshl_or_b32 v162, s36, 8, v170
	v_ashrrev_i32_e32 v165, 31, v164
	v_ashrrev_i32_e32 v163, 31, v162
	v_lshlrev_b64 v[74:75], 11, v[164:165]
	v_lshl_add_u64 v[166:167], v[74:75], 0, v[162:163]
	v_lshl_add_u64 v[180:181], v[166:167], 1, s[30:31]
	v_mov_b32_e32 v252, v180
	v_mov_b32_e32 v253, v181
	global_load_dwordx4 v[196:199], v[252:253], off
	global_load_dwordx4 v[200:203], v[252:253], off offset:256
	s_mov_b64 s[100:101], 0x10000
	v_lshl_add_u64 v[252:253], v[252:253], 0, s[100:101]
	global_load_dwordx4 v[204:207], v[252:253], off
	global_load_dwordx4 v[208:211], v[252:253], off offset:256
	s_mov_b64 s[100:101], 0x10000
	v_lshl_add_u64 v[252:253], v[252:253], 0, s[100:101]
	global_load_dwordx4 v[212:215], v[252:253], off
	global_load_dwordx4 v[216:219], v[252:253], off offset:256
	s_mov_b64 s[100:101], 0x10000
	v_lshl_add_u64 v[252:253], v[252:253], 0, s[100:101]
	global_load_dwordx4 v[220:223], v[252:253], off
	global_load_dwordx4 v[248:251], v[252:253], off offset:256
	v_lshl_add_u64 v[78:79], v[162:163], 2, s[12:13]
	global_load_dwordx4 v[94:97], v[78:79], off
	global_load_dwordx4 v[90:93], v[78:79], off offset:16
	v_mov_b32_e32 v182, 0
	v_mov_b32_e32 v183, 0
	global_load_dwordx4 v[74:77], v[78:79], off offset:528
	s_nop 0
	global_load_dwordx4 v[78:81], v[78:79], off offset:512
	v_lshl_add_u64 v[184:185], s[62:63], 0, v[166:167]
	v_or_b32_e32 v166, 0x80, v166
	v_lshl_add_u64 v[186:187], v[166:167], 1, s[30:31]
	v_xor_b32_e32 v175, 32, v174
	s_waitcnt vmcnt(0)
	s_nop 1
	v_mov_b32_e32 v176, v196
	v_mov_b32_e32 v177, v197
	v_mov_b32_e32 v178, v198
	v_mov_b32_e32 v179, v199
	s_mov_b64 s[100:101], 0x50000
	v_lshl_add_u64 v[252:253], v[252:253], 0, s[100:101]
	global_load_dwordx4 v[196:199], v[252:253], off
	v_lshlrev_b32_e32 v188, 16, v176
	v_and_b32_e32 v189, 0xffff0000, v176
	v_lshlrev_b32_e32 v190, 16, v178
	v_and_b32_e32 v191, 0xffff0000, v178
	v_lshlrev_b32_e32 v178, 16, v179
	v_and_b32_e32 v179, 0xffff0000, v179
	v_lshlrev_b32_e32 v176, 16, v177
	v_and_b32_e32 v177, 0xffff0000, v177
	v_pk_add_f32 v[188:189], v[138:139], v[188:189]
	v_pk_add_f32 v[144:145], v[144:145], v[178:179]
	v_pk_add_f32 v[178:179], v[142:143], v[190:191]
	v_pk_add_f32 v[176:177], v[140:141], v[176:177]
	v_pk_mul_f32 v[140:141], v[94:95], v[188:189]
	v_pk_mul_f32 v[142:143], v[90:91], v[178:179]
	v_cvt_pk_fp8_f32 v182, v140, v141
	v_cvt_pk_fp8_f32 v183, v142, v143
	v_pk_mul_f32 v[140:141], v[96:97], v[176:177]
	v_pk_mul_f32 v[142:143], v[92:93], v[144:145]
	v_cvt_pk_fp8_f32 v182, v140, v141 op_sel:[0,0,1]
	v_cvt_pk_fp8_f32 v183, v142, v143 op_sel:[0,0,1]
	v_cvt_pk_bf16_f32 v138, v188, v189
	v_cvt_pk_bf16_f32 v139, v176, v177
	v_cvt_pk_bf16_f32 v140, v178, v179
	v_cvt_pk_bf16_f32 v141, v144, v145
	global_store_dwordx4 v[180:181], v[138:141], off
	global_store_dwordx2 v[184:185], v[182:183], off
	s_nop 0
	v_and_b32_e32 v139, 64, v174
	v_xor_b32_e32 v138, 16, v174
	v_add_u32_e32 v139, 64, v139
	v_cmp_lt_i32_e32 vcc, v138, v139
	v_mul_f32_e32 v177, v177, v177
	v_mul_f32_e32 v179, v179, v179
	v_cndmask_b32_e32 v138, v174, v138, vcc
	v_cmp_lt_i32_e32 vcc, v175, v139
	v_mul_f32_e32 v145, v145, v145
	v_fmac_f32_e32 v177, v176, v176
	v_cndmask_b32_e32 v139, v174, v175, vcc
	v_mul_f32_e32 v175, v189, v189
	v_fmac_f32_e32 v175, v188, v188
	v_fmac_f32_e32 v179, v178, v178
	v_fmac_f32_e32 v145, v144, v144
	v_add_f32_e32 v144, v175, v177
	v_add_f32_e32 v144, v179, v144
	v_add_f32_e32 v175, v145, v144
	v_lshlrev_b32_e32 v138, 2, v138
	v_mov_b32_e32 v180, 0
	v_mov_b32_e32 v181, 0
	s_waitcnt vmcnt(9)
	s_nop 1
	v_mov_b32_e32 v140, v200
	v_mov_b32_e32 v141, v201
	v_mov_b32_e32 v142, v202
	v_mov_b32_e32 v143, v203
	global_load_dwordx4 v[200:203], v[252:253], off offset:256
	v_lshlrev_b32_e32 v144, 16, v140
	v_and_b32_e32 v145, 0xffff0000, v140
	v_lshlrev_b32_e32 v140, 16, v141
	v_and_b32_e32 v141, 0xffff0000, v141
	v_lshlrev_b32_e32 v176, 16, v142
	v_and_b32_e32 v177, 0xffff0000, v142
	v_lshlrev_b32_e32 v142, 16, v143
	v_and_b32_e32 v143, 0xffff0000, v143
	v_pk_add_f32 v[140:141], v[136:137], v[140:141]
	v_pk_add_f32 v[144:145], v[134:135], v[144:145]
	v_pk_add_f32 v[142:143], v[132:133], v[142:143]
	v_pk_add_f32 v[130:131], v[130:131], v[176:177]
	v_cvt_pk_bf16_f32 v134, v144, v145
	v_pk_mul_f32 v[132:133], v[78:79], v[144:145]
	v_mul_f32_e32 v137, v145, v145
	v_mul_f32_e32 v145, v141, v141
	v_cvt_pk_bf16_f32 v135, v140, v141
	v_cvt_pk_bf16_f32 v136, v130, v131
	v_pk_mul_f32 v[176:177], v[74:75], v[130:131]
	v_mul_f32_e32 v131, v131, v131
	v_fmac_f32_e32 v137, v144, v144
	v_fmac_f32_e32 v145, v140, v140
	v_mul_f32_e32 v178, v143, v143
	v_fmac_f32_e32 v131, v130, v130
	v_add_f32_e32 v130, v137, v145
	v_fmac_f32_e32 v178, v142, v142
	v_add_f32_e32 v130, v131, v130
	v_add_f32_e32 v130, v178, v130
	v_add_f32_e32 v137, v175, v130
	ds_bpermute_b32 v144, v138, v137
	v_cvt_pk_fp8_f32 v180, v132, v133
	v_cvt_pk_fp8_f32 v181, v176, v177
	v_pk_mul_f32 v[130:131], v[80:81], v[140:141]
	v_pk_mul_f32 v[132:133], v[76:77], v[142:143]
	v_cvt_pk_fp8_f32 v180, v130, v131 op_sel:[0,0,1]
	v_cvt_pk_fp8_f32 v181, v132, v133 op_sel:[0,0,1]
	s_waitcnt lgkmcnt(0)
	v_add_f32_e32 v130, v137, v144
	v_lshlrev_b32_e32 v132, 2, v139
	ds_bpermute_b32 v131, v132, v130
	v_cvt_pk_bf16_f32 v137, v142, v143
	global_store_dwordx4 v[186:187], v[134:137], off
	s_nop 1
	v_lshl_add_u64 v[134:135], s[62:63], 0, v[166:167]
	global_store_dwordx2 v[134:135], v[180:181], off
	s_and_saveexec_b64 s[46:47], s[0:1]
	s_cbranch_execz .LBB0_1963
	s_waitcnt lgkmcnt(0)
	v_add_f32_e32 v130, v130, v131
	v_mul_f32_e32 v130, 0x4b800000, v130
	v_trunc_f32_e32 v130, v130
	v_mul_f32_e32 v131, 0x2f800000, v130
	v_floor_f32_e32 v131, v131
	v_fmac_f32_e32 v130, 0xcf800000, v131
	v_cvt_u32_f32_e32 v130, v130
	v_cvt_u32_f32_e32 v131, v131
	v_lshl_add_u64 v[134:135], v[164:165], 3, s[20:21]
	global_atomic_add_x2 v[134:135], v[130:131], off
; __device__ __forceinline__ unsigned pk4_fp8(float a, float b, float c, float d) { int w = 0; w = __builtin_amdgcn_cvt_pk_fp8_f32(a, b, w, false); w = __builtin_amdgcn_cvt_pk_fp8_f32(c, d, w, true); return (unsigned)w; }
; __device__ __forceinline__ u32x4 pack8(f32x4 v0, f32x4 v1) { u32x4 w; w.x = cvt_pk_bf16(v0[0], v0[1]); w.y = cvt_pk_bf16(v0[2], v0[3]); w.z = cvt_pk_bf16(v1[0], v1[1]); w.w = cvt_pk_bf16(v1[2], v1[3]); return w; }
; template <class T> __device__ __forceinline__ void est(T* p, T v) { if constexpr (MK_EPI_NT != 0) __builtin_nontemporal_store(v, p); else *p = v; }
; __device__ __forceinline__ void unpack8(u32x4 w, f32x4& v0, f32x4& v1) { v0 = (f32x4){bf_lo(w.x), bf_hi(w.x), bf_lo(w.y), bf_hi(w.y)}; v1 = (f32x4){bf_lo(w.z), bf_hi(w.z), bf_lo(w.w), bf_hi(w.w)}; }
; __device__ __forceinline__ float sum8sq(f32x4 a, f32x4 b) { return (a[0] * a[0] + a[1] * a[1]) + (a[2] * a[2] + a[3] * a[3]) + (b[0] * b[0] + b[1] * b[1]) + (b[2] * b[2] + b[3] * b[3]); }
; __device__ __forceinline__ void row_atomic(ss_t* ss, int row, float sq, int fq) { sq += __shfl_xor(sq, 16); sq += __shfl_xor(sq, 32); if (fq == 0) atomicAdd(ss + row, ss_fix(sq)); }
;     __device__ __forceinline__ void operator()(AccT acc, const Unit& u, int wr, int wc, int fr, int fq) const {
;     ...
;             for (int m = 0; m < 4; ++m) { const int row = row0 + ai * 128 + m * 16; float sq = 0.f;
; #pragma unroll
;                 for (int bj = 0; bj < 2; ++bj) { const size_t o = (size_t)row * DM + col0 + bj * 128;
;                     f32x4 r0, r1; if constexpr (RIN16) unpack8(*(const u32x4*)((const bf16_t*)Xin + o), r0, r1); else { r0 = *(const f32x4*)((const float*)Xin + o); r1 = *(const f32x4*)((const float*)Xin + o + 4); }
;                     const f32x4 x0 = r0 + acc[ai][bj][m][0] * ascale, x1 = r1 + acc[ai][bj][m][1] * ascale;
;                     est((u32x4*)(Xout + o), (u32x4)pack8(x0, x1));
;                     const f32x4 y0 = x0 * gv[bj][0], y1 = x1 * gv[bj][1];
;                     if constexpr (F8OUT) est((u32x2*)((unsigned char*)XB + o), (u32x2)(u32x2){pk4_fp8(y0[0], y0[1], y0[2], y0[3]), pk4_fp8(y1[0], y1[1], y1[2], y1[3])});
;                     else est((u32x4*)((bf16_t*)XB + o), (u32x4)pack8(y0, y1));
;                     sq += sum8sq(x0, x1); }
;                 row_atomic(ss, row, sq, fq); }
.LBB0_1963:
	s_or_b64 exec, exec, s[46:47]
	v_or_b32_e32 v130, 16, v164
	s_waitcnt lgkmcnt(0)
	v_ashrrev_i32_e32 v131, 31, v130
	v_lshlrev_b64 v[134:135], 11, v[130:131]
	v_lshl_add_u64 v[140:141], v[134:135], 0, v[162:163]
	v_lshl_add_u64 v[142:143], v[140:141], 1, s[30:31]
	s_nop 0
	v_mov_b32_e32 v144, 0
	v_mov_b32_e32 v145, 0
	v_lshl_add_u64 v[166:167], s[62:63], 0, v[140:141]
	v_or_b32_e32 v140, 0x80, v140
	v_lshl_add_u64 v[176:177], v[140:141], 1, s[30:31]
	s_waitcnt vmcnt(11)
	s_nop 1
	v_mov_b32_e32 v134, v204
	v_mov_b32_e32 v135, v205
	v_mov_b32_e32 v136, v206
	v_mov_b32_e32 v137, v207
	s_mov_b64 s[100:101], 0x10000
	v_lshl_add_u64 v[252:253], v[252:253], 0, s[100:101]
	global_load_dwordx4 v[204:207], v[252:253], off
	v_lshlrev_b32_e32 v178, 16, v134
	v_and_b32_e32 v179, 0xffff0000, v134
	v_lshlrev_b32_e32 v134, 16, v135
	v_and_b32_e32 v135, 0xffff0000, v135
	v_lshlrev_b32_e32 v180, 16, v136
	v_and_b32_e32 v181, 0xffff0000, v136
	v_lshlrev_b32_e32 v136, 16, v137
	v_and_b32_e32 v137, 0xffff0000, v137
	v_pk_add_f32 v[128:129], v[128:129], v[134:135]
	v_pk_add_f32 v[126:127], v[126:127], v[178:179]
	v_pk_add_f32 v[134:135], v[124:125], v[136:137]
	v_pk_add_f32 v[136:137], v[122:123], v[180:181]
	v_pk_mul_f32 v[124:125], v[94:95], v[126:127]
	v_pk_mul_f32 v[178:179], v[90:91], v[136:137]
	v_cvt_pk_fp8_f32 v144, v124, v125
	v_cvt_pk_fp8_f32 v145, v178, v179
	v_pk_mul_f32 v[124:125], v[96:97], v[128:129]
	v_pk_mul_f32 v[178:179], v[92:93], v[134:135]
	v_cvt_pk_fp8_f32 v144, v124, v125 op_sel:[0,0,1]
	v_cvt_pk_fp8_f32 v145, v178, v179 op_sel:[0,0,1]
	v_cvt_pk_bf16_f32 v122, v126, v127
	v_cvt_pk_bf16_f32 v123, v128, v129
	v_cvt_pk_bf16_f32 v124, v136, v137
	v_cvt_pk_bf16_f32 v125, v134, v135
	global_store_dwordx4 v[142:143], v[122:125], off
	global_store_dwordx2 v[166:167], v[144:145], off
	s_nop 0
	v_mul_f32_e32 v127, v127, v127
	v_mul_f32_e32 v129, v129, v129
	v_mul_f32_e32 v133, v137, v137
	v_fmac_f32_e32 v127, v126, v126
	v_fmac_f32_e32 v129, v128, v128
	v_mul_f32_e32 v135, v135, v135
	v_fmac_f32_e32 v133, v136, v136
	v_add_f32_e32 v126, v127, v129
	v_fmac_f32_e32 v135, v134, v134
	v_add_f32_e32 v126, v133, v126
	v_add_f32_e32 v133, v135, v126
	v_mov_b32_e32 v142, 0
	v_mov_b32_e32 v143, 0
	s_waitcnt vmcnt(13)
	s_nop 1
	v_mov_b32_e32 v122, v208
	v_mov_b32_e32 v123, v209
	v_mov_b32_e32 v124, v210
	v_mov_b32_e32 v125, v211
	global_load_dwordx4 v[208:211], v[252:253], off offset:256
	v_lshlrev_b32_e32 v126, 16, v122
	v_and_b32_e32 v127, 0xffff0000, v122
	v_lshlrev_b32_e32 v122, 16, v123
	v_and_b32_e32 v123, 0xffff0000, v123
	v_lshlrev_b32_e32 v128, 16, v124
	v_and_b32_e32 v129, 0xffff0000, v124
	v_lshlrev_b32_e32 v124, 16, v125
	v_and_b32_e32 v125, 0xffff0000, v125
	v_pk_add_f32 v[120:121], v[120:121], v[122:123]
	v_pk_add_f32 v[122:123], v[118:119], v[126:127]
	v_pk_add_f32 v[124:125], v[116:117], v[124:125]
	v_pk_add_f32 v[114:115], v[114:115], v[128:129]
	v_cvt_pk_bf16_f32 v116, v122, v123
	v_pk_mul_f32 v[126:127], v[78:79], v[122:123]
	v_mul_f32_e32 v119, v123, v123
	v_mul_f32_e32 v123, v121, v121
	v_cvt_pk_bf16_f32 v117, v120, v121
	v_cvt_pk_bf16_f32 v118, v114, v115
	v_pk_mul_f32 v[128:129], v[74:75], v[114:115]
	v_mul_f32_e32 v115, v115, v115
	v_fmac_f32_e32 v119, v122, v122
	v_fmac_f32_e32 v123, v120, v120
	v_mul_f32_e32 v134, v125, v125
	v_fmac_f32_e32 v115, v114, v114
	v_add_f32_e32 v114, v119, v123
	v_add_f32_e32 v114, v115, v114
	v_fmac_f32_e32 v134, v124, v124
	v_add_f32_e32 v114, v134, v114
	v_add_f32_e32 v119, v133, v114
	ds_bpermute_b32 v122, v138, v119
	v_cvt_pk_fp8_f32 v142, v126, v127
	v_cvt_pk_fp8_f32 v143, v128, v129
	v_pk_mul_f32 v[114:115], v[80:81], v[120:121]
	v_pk_mul_f32 v[120:121], v[76:77], v[124:125]
	v_cvt_pk_fp8_f32 v142, v114, v115 op_sel:[0,0,1]
	s_waitcnt lgkmcnt(0)
	v_add_f32_e32 v114, v119, v122
	ds_bpermute_b32 v115, v132, v114
	v_cvt_pk_fp8_f32 v143, v120, v121 op_sel:[0,0,1]
	v_cvt_pk_bf16_f32 v119, v124, v125
	global_store_dwordx4 v[176:177], v[116:119], off
	s_nop 1
	v_lshl_add_u64 v[116:117], s[62:63], 0, v[140:141]
	global_store_dwordx2 v[116:117], v[142:143], off
	s_and_saveexec_b64 s[46:47], s[0:1]
	s_cbranch_execz .LBB0_1965
	s_waitcnt lgkmcnt(0)
	v_add_f32_e32 v114, v114, v115
	v_mul_f32_e32 v114, 0x4b800000, v114
	v_trunc_f32_e32 v114, v114
	v_mul_f32_e32 v115, 0x2f800000, v114
	v_floor_f32_e32 v115, v115
	v_fmac_f32_e32 v114, 0xcf800000, v115
	v_cvt_u32_f32_e32 v114, v114
	v_cvt_u32_f32_e32 v115, v115
	v_lshl_add_u64 v[116:117], v[130:131], 3, s[20:21]
	global_atomic_add_x2 v[116:117], v[114:115], off
; __device__ __forceinline__ unsigned pk4_fp8(float a, float b, float c, float d) { int w = 0; w = __builtin_amdgcn_cvt_pk_fp8_f32(a, b, w, false); w = __builtin_amdgcn_cvt_pk_fp8_f32(c, d, w, true); return (unsigned)w; }
; __device__ __forceinline__ u32x4 pack8(f32x4 v0, f32x4 v1) { u32x4 w; w.x = cvt_pk_bf16(v0[0], v0[1]); w.y = cvt_pk_bf16(v0[2], v0[3]); w.z = cvt_pk_bf16(v1[0], v1[1]); w.w = cvt_pk_bf16(v1[2], v1[3]); return w; }
; template <class T> __device__ __forceinline__ void est(T* p, T v) { if constexpr (MK_EPI_NT != 0) __builtin_nontemporal_store(v, p); else *p = v; }
; __device__ __forceinline__ void unpack8(u32x4 w, f32x4& v0, f32x4& v1) { v0 = (f32x4){bf_lo(w.x), bf_hi(w.x), bf_lo(w.y), bf_hi(w.y)}; v1 = (f32x4){bf_lo(w.z), bf_hi(w.z), bf_lo(w.w), bf_hi(w.w)}; }
; __device__ __forceinline__ float sum8sq(f32x4 a, f32x4 b) { return (a[0] * a[0] + a[1] * a[1]) + (a[2] * a[2] + a[3] * a[3]) + (b[0] * b[0] + b[1] * b[1]) + (b[2] * b[2] + b[3] * b[3]); }
; __device__ __forceinline__ void row_atomic(ss_t* ss, int row, float sq, int fq) { sq += __shfl_xor(sq, 16); sq += __shfl_xor(sq, 32); if (fq == 0) atomicAdd(ss + row, ss_fix(sq)); }
;     __device__ __forceinline__ void operator()(AccT acc, const Unit& u, int wr, int wc, int fr, int fq) const {
;     ...
;             for (int m = 0; m < 4; ++m) { const int row = row0 + ai * 128 + m * 16; float sq = 0.f;
; #pragma unroll
;                 for (int bj = 0; bj < 2; ++bj) { const size_t o = (size_t)row * DM + col0 + bj * 128;
;                     f32x4 r0, r1; if constexpr (RIN16) unpack8(*(const u32x4*)((const bf16_t*)Xin + o), r0, r1); else { r0 = *(const f32x4*)((const float*)Xin + o); r1 = *(const f32x4*)((const float*)Xin + o + 4); }
;                     const f32x4 x0 = r0 + acc[ai][bj][m][0] * ascale, x1 = r1 + acc[ai][bj][m][1] * ascale;
;                     est((u32x4*)(Xout + o), (u32x4)pack8(x0, x1));
;                     const f32x4 y0 = x0 * gv[bj][0], y1 = x1 * gv[bj][1];
;                     if constexpr (F8OUT) est((u32x2*)((unsigned char*)XB + o), (u32x2)(u32x2){pk4_fp8(y0[0], y0[1], y0[2], y0[3]), pk4_fp8(y1[0], y1[1], y1[2], y1[3])});
;                     else est((u32x4*)((bf16_t*)XB + o), (u32x4)pack8(y0, y1));
;                     sq += sum8sq(x0, x1); }
;                 row_atomic(ss, row, sq, fq); }
.LBB0_1965:
	s_or_b64 exec, exec, s[46:47]
	v_or_b32_e32 v114, 32, v164
	s_waitcnt lgkmcnt(0)
	v_ashrrev_i32_e32 v115, 31, v114
	v_lshlrev_b64 v[116:117], 11, v[114:115]
	v_lshl_add_u64 v[120:121], v[116:117], 0, v[162:163]
	v_lshl_add_u64 v[122:123], v[120:121], 1, s[30:31]
	s_nop 0
	v_mov_b32_e32 v124, 0
	v_mov_b32_e32 v125, 0
	v_lshl_add_u64 v[126:127], s[62:63], 0, v[120:121]
	v_or_b32_e32 v120, 0x80, v120
	v_lshl_add_u64 v[128:129], v[120:121], 1, s[30:31]
	s_waitcnt vmcnt(15)
	s_nop 1
	v_mov_b32_e32 v116, v212
	v_mov_b32_e32 v117, v213
	v_mov_b32_e32 v118, v214
	v_mov_b32_e32 v119, v215
	s_mov_b64 s[100:101], 0x10000
	v_lshl_add_u64 v[252:253], v[252:253], 0, s[100:101]
	global_load_dwordx4 v[212:215], v[252:253], off
	v_lshlrev_b32_e32 v130, 16, v116
	v_and_b32_e32 v131, 0xffff0000, v116
	v_lshlrev_b32_e32 v116, 16, v117
	v_and_b32_e32 v117, 0xffff0000, v117
	v_lshlrev_b32_e32 v134, 16, v118
	v_and_b32_e32 v135, 0xffff0000, v118
	v_lshlrev_b32_e32 v118, 16, v119
	v_and_b32_e32 v119, 0xffff0000, v119
	v_pk_add_f32 v[112:113], v[112:113], v[116:117]
	v_pk_add_f32 v[110:111], v[110:111], v[130:131]
	v_pk_add_f32 v[116:117], v[108:109], v[118:119]
	v_pk_add_f32 v[118:119], v[106:107], v[134:135]
	v_pk_mul_f32 v[108:109], v[94:95], v[110:111]
	v_pk_mul_f32 v[130:131], v[90:91], v[118:119]
	v_cvt_pk_fp8_f32 v124, v108, v109
	v_cvt_pk_fp8_f32 v125, v130, v131
	v_pk_mul_f32 v[108:109], v[96:97], v[112:113]
	v_pk_mul_f32 v[130:131], v[92:93], v[116:117]
	v_cvt_pk_fp8_f32 v124, v108, v109 op_sel:[0,0,1]
	v_cvt_pk_fp8_f32 v125, v130, v131 op_sel:[0,0,1]
	v_cvt_pk_bf16_f32 v106, v110, v111
	v_cvt_pk_bf16_f32 v107, v112, v113
	v_cvt_pk_bf16_f32 v108, v118, v119
	v_cvt_pk_bf16_f32 v109, v116, v117
	global_store_dwordx4 v[122:123], v[106:109], off
	global_store_dwordx2 v[126:127], v[124:125], off
	s_nop 0
	v_mul_f32_e32 v111, v111, v111
	v_mul_f32_e32 v113, v113, v113
	v_mul_f32_e32 v119, v119, v119
	v_fmac_f32_e32 v111, v110, v110
	v_fmac_f32_e32 v113, v112, v112
	v_mul_f32_e32 v117, v117, v117
	v_fmac_f32_e32 v119, v118, v118
	v_add_f32_e32 v110, v111, v113
	v_fmac_f32_e32 v117, v116, v116
	v_add_f32_e32 v110, v119, v110
	v_add_f32_e32 v116, v117, v110
	v_mov_b32_e32 v122, 0
	v_mov_b32_e32 v123, 0
	s_waitcnt vmcnt(17)
	s_nop 1
	v_mov_b32_e32 v106, v216
	v_mov_b32_e32 v107, v217
	v_mov_b32_e32 v108, v218
	v_mov_b32_e32 v109, v219
	global_load_dwordx4 v[216:219], v[252:253], off offset:256
	v_lshlrev_b32_e32 v110, 16, v106
	v_and_b32_e32 v111, 0xffff0000, v106
	v_lshlrev_b32_e32 v106, 16, v107
	v_and_b32_e32 v107, 0xffff0000, v107
	v_lshlrev_b32_e32 v112, 16, v108
	v_and_b32_e32 v113, 0xffff0000, v108
	v_lshlrev_b32_e32 v108, 16, v109
	v_and_b32_e32 v109, 0xffff0000, v109
	v_pk_add_f32 v[104:105], v[104:105], v[106:107]
	v_pk_add_f32 v[106:107], v[102:103], v[110:111]
	v_pk_add_f32 v[108:109], v[100:101], v[108:109]
	v_pk_add_f32 v[98:99], v[98:99], v[112:113]
	v_cvt_pk_bf16_f32 v100, v106, v107
	v_pk_mul_f32 v[110:111], v[78:79], v[106:107]
	v_mul_f32_e32 v103, v107, v107
	v_mul_f32_e32 v107, v105, v105
	v_cvt_pk_bf16_f32 v101, v104, v105
	v_cvt_pk_bf16_f32 v102, v98, v99
	v_pk_mul_f32 v[112:113], v[74:75], v[98:99]
	v_mul_f32_e32 v99, v99, v99
	v_fmac_f32_e32 v103, v106, v106
	v_fmac_f32_e32 v107, v104, v104
	v_mul_f32_e32 v117, v109, v109
	v_fmac_f32_e32 v99, v98, v98
	v_add_f32_e32 v98, v103, v107
	v_add_f32_e32 v98, v99, v98
	v_fmac_f32_e32 v117, v108, v108
	v_add_f32_e32 v98, v117, v98
	v_add_f32_e32 v103, v116, v98
	ds_bpermute_b32 v106, v138, v103
	v_cvt_pk_fp8_f32 v122, v110, v111
	v_cvt_pk_fp8_f32 v123, v112, v113
	v_pk_mul_f32 v[98:99], v[80:81], v[104:105]
	v_pk_mul_f32 v[104:105], v[76:77], v[108:109]
	v_cvt_pk_fp8_f32 v122, v98, v99 op_sel:[0,0,1]
	s_waitcnt lgkmcnt(0)
	v_add_f32_e32 v98, v103, v106
	ds_bpermute_b32 v99, v132, v98
	v_cvt_pk_fp8_f32 v123, v104, v105 op_sel:[0,0,1]
	v_cvt_pk_bf16_f32 v103, v108, v109
	global_store_dwordx4 v[128:129], v[100:103], off
	s_nop 1
	v_lshl_add_u64 v[100:101], s[62:63], 0, v[120:121]
	global_store_dwordx2 v[100:101], v[122:123], off
	s_and_saveexec_b64 s[46:47], s[0:1]
	s_cbranch_execz .LBB0_1967
	s_waitcnt lgkmcnt(0)
	v_add_f32_e32 v98, v98, v99
	v_mul_f32_e32 v98, 0x4b800000, v98
	v_trunc_f32_e32 v98, v98
	v_mul_f32_e32 v99, 0x2f800000, v98
	v_floor_f32_e32 v99, v99
	v_fmac_f32_e32 v98, 0xcf800000, v99
	v_cvt_u32_f32_e32 v98, v98
	v_cvt_u32_f32_e32 v99, v99
	v_lshl_add_u64 v[100:101], v[114:115], 3, s[20:21]
	global_atomic_add_x2 v[100:101], v[98:99], off
; __device__ __forceinline__ unsigned pk4_fp8(float a, float b, float c, float d) { int w = 0; w = __builtin_amdgcn_cvt_pk_fp8_f32(a, b, w, false); w = __builtin_amdgcn_cvt_pk_fp8_f32(c, d, w, true); return (unsigned)w; }
; __device__ __forceinline__ u32x4 pack8(f32x4 v0, f32x4 v1) { u32x4 w; w.x = cvt_pk_bf16(v0[0], v0[1]); w.y = cvt_pk_bf16(v0[2], v0[3]); w.z = cvt_pk_bf16(v1[0], v1[1]); w.w = cvt_pk_bf16(v1[2], v1[3]); return w; }
; template <class T> __device__ __forceinline__ void est(T* p, T v) { if constexpr (MK_EPI_NT != 0) __builtin_nontemporal_store(v, p); else *p = v; }
; __device__ __forceinline__ void unpack8(u32x4 w, f32x4& v0, f32x4& v1) { v0 = (f32x4){bf_lo(w.x), bf_hi(w.x), bf_lo(w.y), bf_hi(w.y)}; v1 = (f32x4){bf_lo(w.z), bf_hi(w.z), bf_lo(w.w), bf_hi(w.w)}; }
; __device__ __forceinline__ float sum8sq(f32x4 a, f32x4 b) { return (a[0] * a[0] + a[1] * a[1]) + (a[2] * a[2] + a[3] * a[3]) + (b[0] * b[0] + b[1] * b[1]) + (b[2] * b[2] + b[3] * b[3]); }
; __device__ __forceinline__ void row_atomic(ss_t* ss, int row, float sq, int fq) { sq += __shfl_xor(sq, 16); sq += __shfl_xor(sq, 32); if (fq == 0) atomicAdd(ss + row, ss_fix(sq)); }
;     __device__ __forceinline__ void operator()(AccT acc, const Unit& u, int wr, int wc, int fr, int fq) const {
;     ...
;             for (int m = 0; m < 4; ++m) { const int row = row0 + ai * 128 + m * 16; float sq = 0.f;
; #pragma unroll
;                 for (int bj = 0; bj < 2; ++bj) { const size_t o = (size_t)row * DM + col0 + bj * 128;
;                     f32x4 r0, r1; if constexpr (RIN16) unpack8(*(const u32x4*)((const bf16_t*)Xin + o), r0, r1); else { r0 = *(const f32x4*)((const float*)Xin + o); r1 = *(const f32x4*)((const float*)Xin + o + 4); }
;                     const f32x4 x0 = r0 + acc[ai][bj][m][0] * ascale, x1 = r1 + acc[ai][bj][m][1] * ascale;
;                     est((u32x4*)(Xout + o), (u32x4)pack8(x0, x1));
;                     const f32x4 y0 = x0 * gv[bj][0], y1 = x1 * gv[bj][1];
;                     if constexpr (F8OUT) est((u32x2*)((unsigned char*)XB + o), (u32x2)(u32x2){pk4_fp8(y0[0], y0[1], y0[2], y0[3]), pk4_fp8(y1[0], y1[1], y1[2], y1[3])});
;                     else est((u32x4*)((bf16_t*)XB + o), (u32x4)pack8(y0, y1));
;                     sq += sum8sq(x0, x1); }
;                 row_atomic(ss, row, sq, fq); }
.LBB0_1967:
	s_or_b64 exec, exec, s[46:47]
	v_or_b32_e32 v98, 48, v164
	s_waitcnt lgkmcnt(0)
	v_ashrrev_i32_e32 v99, 31, v98
	v_lshlrev_b64 v[100:101], 11, v[98:99]
	v_lshl_add_u64 v[104:105], v[100:101], 0, v[162:163]
	v_lshl_add_u64 v[106:107], v[104:105], 1, s[30:31]
	s_nop 0
	v_mov_b32_e32 v108, 0
	v_mov_b32_e32 v109, 0
	v_lshl_add_u64 v[110:111], s[62:63], 0, v[104:105]
	v_or_b32_e32 v104, 0x80, v104
	v_lshl_add_u64 v[112:113], v[104:105], 1, s[30:31]
	s_waitcnt vmcnt(19)
	s_nop 1
	v_mov_b32_e32 v100, v220
	v_mov_b32_e32 v101, v221
	v_mov_b32_e32 v102, v222
	v_mov_b32_e32 v103, v223
	s_mov_b64 s[100:101], 0x10000
	v_lshl_add_u64 v[252:253], v[252:253], 0, s[100:101]
	global_load_dwordx4 v[220:223], v[252:253], off
	v_lshlrev_b32_e32 v114, 16, v100
	v_and_b32_e32 v115, 0xffff0000, v100
	v_lshlrev_b32_e32 v100, 16, v101
	v_and_b32_e32 v101, 0xffff0000, v101
	v_lshlrev_b32_e32 v116, 16, v102
	v_and_b32_e32 v117, 0xffff0000, v102
	v_lshlrev_b32_e32 v102, 16, v103
	v_and_b32_e32 v103, 0xffff0000, v103
	v_pk_add_f32 v[88:89], v[88:89], v[100:101]
	v_pk_add_f32 v[86:87], v[86:87], v[114:115]
	v_pk_add_f32 v[100:101], v[84:85], v[102:103]
	v_pk_add_f32 v[102:103], v[82:83], v[116:117]
	v_pk_mul_f32 v[84:85], v[94:95], v[86:87]
	v_pk_mul_f32 v[114:115], v[90:91], v[102:103]
	v_cvt_pk_fp8_f32 v108, v84, v85
	v_cvt_pk_fp8_f32 v109, v114, v115
	v_pk_mul_f32 v[84:85], v[96:97], v[88:89]
	v_pk_mul_f32 v[114:115], v[92:93], v[100:101]
	v_cvt_pk_fp8_f32 v108, v84, v85 op_sel:[0,0,1]
	v_cvt_pk_fp8_f32 v109, v114, v115 op_sel:[0,0,1]
	v_cvt_pk_bf16_f32 v82, v86, v87
	v_cvt_pk_bf16_f32 v83, v88, v89
	v_cvt_pk_bf16_f32 v84, v102, v103
	v_cvt_pk_bf16_f32 v85, v100, v101
	global_store_dwordx4 v[106:107], v[82:85], off
	global_store_dwordx2 v[110:111], v[108:109], off
	s_nop 0
	v_mul_f32_e32 v87, v87, v87
	v_mul_f32_e32 v89, v89, v89
	v_mul_f32_e32 v103, v103, v103
	v_fmac_f32_e32 v87, v86, v86
	v_fmac_f32_e32 v89, v88, v88
	v_mul_f32_e32 v101, v101, v101
	v_fmac_f32_e32 v103, v102, v102
	v_add_f32_e32 v86, v87, v89
	v_fmac_f32_e32 v101, v100, v100
	v_add_f32_e32 v86, v103, v86
	v_add_f32_e32 v100, v101, v86
	v_mov_b32_e32 v106, 0
	v_mov_b32_e32 v107, 0
	s_waitcnt vmcnt(21)
	s_nop 1
	v_mov_b32_e32 v82, v248
	v_mov_b32_e32 v83, v249
	v_mov_b32_e32 v84, v250
	v_mov_b32_e32 v85, v251
	global_load_dwordx4 v[248:251], v[252:253], off offset:256
	v_lshlrev_b32_e32 v86, 16, v82
	v_and_b32_e32 v87, 0xffff0000, v82
	v_lshlrev_b32_e32 v82, 16, v83
	v_and_b32_e32 v83, 0xffff0000, v83
	v_lshlrev_b32_e32 v88, 16, v84
	v_and_b32_e32 v89, 0xffff0000, v84
	v_lshlrev_b32_e32 v84, 16, v85
	v_and_b32_e32 v85, 0xffff0000, v85
	v_pk_add_f32 v[72:73], v[72:73], v[82:83]
	v_pk_add_f32 v[82:83], v[70:71], v[86:87]
	v_pk_add_f32 v[84:85], v[68:69], v[84:85]
	v_pk_add_f32 v[66:67], v[66:67], v[88:89]
	v_cvt_pk_bf16_f32 v68, v82, v83
	v_pk_mul_f32 v[86:87], v[78:79], v[82:83]
	v_mul_f32_e32 v71, v83, v83
	v_mul_f32_e32 v83, v73, v73
	v_cvt_pk_bf16_f32 v69, v72, v73
	v_cvt_pk_bf16_f32 v70, v66, v67
	v_pk_mul_f32 v[88:89], v[74:75], v[66:67]
	v_mul_f32_e32 v67, v67, v67
	v_fmac_f32_e32 v71, v82, v82
	v_fmac_f32_e32 v83, v72, v72
	v_mul_f32_e32 v101, v85, v85
	v_fmac_f32_e32 v67, v66, v66
	v_add_f32_e32 v66, v71, v83
	v_add_f32_e32 v66, v67, v66
	v_fmac_f32_e32 v101, v84, v84
	v_add_f32_e32 v66, v101, v66
	v_add_f32_e32 v71, v100, v66
	ds_bpermute_b32 v82, v138, v71
	v_cvt_pk_fp8_f32 v106, v86, v87
	v_cvt_pk_fp8_f32 v107, v88, v89
	v_pk_mul_f32 v[66:67], v[80:81], v[72:73]
	v_pk_mul_f32 v[72:73], v[76:77], v[84:85]
	v_cvt_pk_fp8_f32 v106, v66, v67 op_sel:[0,0,1]
	s_waitcnt lgkmcnt(0)
	v_add_f32_e32 v66, v71, v82
	ds_bpermute_b32 v67, v132, v66
	v_cvt_pk_fp8_f32 v107, v72, v73 op_sel:[0,0,1]
	v_cvt_pk_bf16_f32 v71, v84, v85
	global_store_dwordx4 v[112:113], v[68:71], off
	s_nop 1
	v_lshl_add_u64 v[68:69], s[62:63], 0, v[104:105]
	global_store_dwordx2 v[68:69], v[106:107], off
	s_and_saveexec_b64 s[46:47], s[0:1]
	s_cbranch_execz .LBB0_1969
	s_waitcnt lgkmcnt(0)
	v_add_f32_e32 v66, v66, v67
	v_mul_f32_e32 v66, 0x4b800000, v66
	v_trunc_f32_e32 v66, v66
	v_mul_f32_e32 v67, 0x2f800000, v66
	v_floor_f32_e32 v67, v67
	v_fmac_f32_e32 v66, 0xcf800000, v67
	v_cvt_u32_f32_e32 v66, v66
	v_cvt_u32_f32_e32 v67, v67
	v_lshl_add_u64 v[68:69], v[98:99], 3, s[20:21]
	global_atomic_add_x2 v[68:69], v[66:67], off
; __device__ __forceinline__ unsigned pk4_fp8(float a, float b, float c, float d) { int w = 0; w = __builtin_amdgcn_cvt_pk_fp8_f32(a, b, w, false); w = __builtin_amdgcn_cvt_pk_fp8_f32(c, d, w, true); return (unsigned)w; }
; __device__ __forceinline__ u32x4 pack8(f32x4 v0, f32x4 v1) { u32x4 w; w.x = cvt_pk_bf16(v0[0], v0[1]); w.y = cvt_pk_bf16(v0[2], v0[3]); w.z = cvt_pk_bf16(v1[0], v1[1]); w.w = cvt_pk_bf16(v1[2], v1[3]); return w; }
; template <class T> __device__ __forceinline__ void est(T* p, T v) { if constexpr (MK_EPI_NT != 0) __builtin_nontemporal_store(v, p); else *p = v; }
; __device__ __forceinline__ void unpack8(u32x4 w, f32x4& v0, f32x4& v1) { v0 = (f32x4){bf_lo(w.x), bf_hi(w.x), bf_lo(w.y), bf_hi(w.y)}; v1 = (f32x4){bf_lo(w.z), bf_hi(w.z), bf_lo(w.w), bf_hi(w.w)}; }
; __device__ __forceinline__ float sum8sq(f32x4 a, f32x4 b) { return (a[0] * a[0] + a[1] * a[1]) + (a[2] * a[2] + a[3] * a[3]) + (b[0] * b[0] + b[1] * b[1]) + (b[2] * b[2] + b[3] * b[3]); }
; __device__ __forceinline__ void row_atomic(ss_t* ss, int row, float sq, int fq) { sq += __shfl_xor(sq, 16); sq += __shfl_xor(sq, 32); if (fq == 0) atomicAdd(ss + row, ss_fix(sq)); }
;     __device__ __forceinline__ void operator()(AccT acc, const Unit& u, int wr, int wc, int fr, int fq) const {
;     ...
;             for (int m = 0; m < 4; ++m) { const int row = row0 + ai * 128 + m * 16; float sq = 0.f;
; #pragma unroll
;                 for (int bj = 0; bj < 2; ++bj) { const size_t o = (size_t)row * DM + col0 + bj * 128;
;                     f32x4 r0, r1; if constexpr (RIN16) unpack8(*(const u32x4*)((const bf16_t*)Xin + o), r0, r1); else { r0 = *(const f32x4*)((const float*)Xin + o); r1 = *(const f32x4*)((const float*)Xin + o + 4); }
;                     const f32x4 x0 = r0 + acc[ai][bj][m][0] * ascale, x1 = r1 + acc[ai][bj][m][1] * ascale;
;                     est((u32x4*)(Xout + o), (u32x4)pack8(x0, x1));
;                     const f32x4 y0 = x0 * gv[bj][0], y1 = x1 * gv[bj][1];
;                     if constexpr (F8OUT) est((u32x2*)((unsigned char*)XB + o), (u32x2)(u32x2){pk4_fp8(y0[0], y0[1], y0[2], y0[3]), pk4_fp8(y1[0], y1[1], y1[2], y1[3])});
;                     else est((u32x4*)((bf16_t*)XB + o), (u32x4)pack8(y0, y1));
;                     sq += sum8sq(x0, x1); }
;                 row_atomic(ss, row, sq, fq); }
.LBB0_1969:
	s_or_b64 exec, exec, s[46:47]
	v_add_u32_e32 v66, 0x80, v164
	s_waitcnt lgkmcnt(0)
	v_ashrrev_i32_e32 v67, 31, v66
	v_lshlrev_b64 v[68:69], 11, v[66:67]
	v_lshl_add_u64 v[72:73], v[68:69], 0, v[162:163]
	v_lshl_add_u64 v[82:83], v[72:73], 1, s[30:31]
	s_nop 0
	v_mov_b32_e32 v84, 0
	v_mov_b32_e32 v85, 0
	v_lshl_add_u64 v[86:87], s[62:63], 0, v[72:73]
	v_or_b32_e32 v72, 0x80, v72
	v_lshl_add_u64 v[88:89], v[72:73], 1, s[30:31]
	s_waitcnt vmcnt(23)
	s_nop 1
	v_mov_b32_e32 v68, v196
	v_mov_b32_e32 v69, v197
	v_mov_b32_e32 v70, v198
	v_mov_b32_e32 v71, v199
	v_lshlrev_b32_e32 v98, 16, v68
	v_and_b32_e32 v99, 0xffff0000, v68
	v_lshlrev_b32_e32 v68, 16, v69
	v_and_b32_e32 v69, 0xffff0000, v69
	v_lshlrev_b32_e32 v100, 16, v70
	v_and_b32_e32 v101, 0xffff0000, v70
	v_lshlrev_b32_e32 v70, 16, v71
	v_and_b32_e32 v71, 0xffff0000, v71
	v_pk_add_f32 v[64:65], v[64:65], v[68:69]
	v_pk_add_f32 v[62:63], v[62:63], v[98:99]
	v_pk_add_f32 v[68:69], v[60:61], v[70:71]
	v_pk_add_f32 v[70:71], v[58:59], v[100:101]
	v_pk_mul_f32 v[60:61], v[94:95], v[62:63]
	v_pk_mul_f32 v[98:99], v[90:91], v[70:71]
	v_cvt_pk_fp8_f32 v84, v60, v61
	v_cvt_pk_fp8_f32 v85, v98, v99
	v_pk_mul_f32 v[60:61], v[96:97], v[64:65]
	v_pk_mul_f32 v[98:99], v[92:93], v[68:69]
	v_cvt_pk_fp8_f32 v84, v60, v61 op_sel:[0,0,1]
	v_cvt_pk_fp8_f32 v85, v98, v99 op_sel:[0,0,1]
	v_cvt_pk_bf16_f32 v58, v62, v63
	v_cvt_pk_bf16_f32 v59, v64, v65
	v_cvt_pk_bf16_f32 v60, v70, v71
	v_cvt_pk_bf16_f32 v61, v68, v69
	global_store_dwordx4 v[82:83], v[58:61], off
	global_store_dwordx2 v[86:87], v[84:85], off
	s_nop 0
	v_mul_f32_e32 v63, v63, v63
	v_mul_f32_e32 v65, v65, v65
	v_mul_f32_e32 v71, v71, v71
	v_fmac_f32_e32 v63, v62, v62
	v_fmac_f32_e32 v65, v64, v64
	v_mul_f32_e32 v69, v69, v69
	v_fmac_f32_e32 v71, v70, v70
	v_add_f32_e32 v62, v63, v65
	v_fmac_f32_e32 v69, v68, v68
	v_add_f32_e32 v62, v71, v62
	v_add_f32_e32 v68, v69, v62
	v_mov_b32_e32 v82, 0
	v_mov_b32_e32 v83, 0
	s_waitcnt vmcnt(22)
	s_nop 1
	v_mov_b32_e32 v58, v200
	v_mov_b32_e32 v59, v201
	v_mov_b32_e32 v60, v202
	v_mov_b32_e32 v61, v203
	v_lshlrev_b32_e32 v62, 16, v58
	v_and_b32_e32 v63, 0xffff0000, v58
	v_lshlrev_b32_e32 v58, 16, v59
	v_and_b32_e32 v59, 0xffff0000, v59
	v_lshlrev_b32_e32 v64, 16, v60
	v_and_b32_e32 v65, 0xffff0000, v60
	v_lshlrev_b32_e32 v60, 16, v61
	v_and_b32_e32 v61, 0xffff0000, v61
	v_pk_add_f32 v[56:57], v[56:57], v[58:59]
	v_pk_add_f32 v[58:59], v[54:55], v[62:63]
	v_pk_add_f32 v[60:61], v[52:53], v[60:61]
	v_pk_add_f32 v[50:51], v[50:51], v[64:65]
	v_cvt_pk_bf16_f32 v52, v58, v59
	v_pk_mul_f32 v[62:63], v[78:79], v[58:59]
	v_mul_f32_e32 v55, v59, v59
	v_mul_f32_e32 v59, v57, v57
	v_cvt_pk_bf16_f32 v53, v56, v57
	v_cvt_pk_bf16_f32 v54, v50, v51
	v_pk_mul_f32 v[64:65], v[74:75], v[50:51]
	v_mul_f32_e32 v51, v51, v51
	v_fmac_f32_e32 v55, v58, v58
	v_fmac_f32_e32 v59, v56, v56
	v_mul_f32_e32 v69, v61, v61
	v_fmac_f32_e32 v51, v50, v50
	v_add_f32_e32 v50, v55, v59
	v_add_f32_e32 v50, v51, v50
	v_fmac_f32_e32 v69, v60, v60
	v_add_f32_e32 v50, v69, v50
	v_add_f32_e32 v55, v68, v50
	ds_bpermute_b32 v58, v138, v55
	v_cvt_pk_fp8_f32 v82, v62, v63
	v_cvt_pk_fp8_f32 v83, v64, v65
	v_pk_mul_f32 v[50:51], v[80:81], v[56:57]
	v_pk_mul_f32 v[56:57], v[76:77], v[60:61]
	v_cvt_pk_fp8_f32 v82, v50, v51 op_sel:[0,0,1]
	s_waitcnt lgkmcnt(0)
	v_add_f32_e32 v50, v55, v58
	ds_bpermute_b32 v51, v132, v50
	v_cvt_pk_fp8_f32 v83, v56, v57 op_sel:[0,0,1]
	v_cvt_pk_bf16_f32 v55, v60, v61
	global_store_dwordx4 v[88:89], v[52:55], off
	s_nop 1
	v_lshl_add_u64 v[52:53], s[62:63], 0, v[72:73]
	global_store_dwordx2 v[52:53], v[82:83], off
	s_and_saveexec_b64 s[46:47], s[0:1]
	s_cbranch_execz .LBB0_1971
	s_waitcnt lgkmcnt(0)
	v_add_f32_e32 v50, v50, v51
	v_mul_f32_e32 v50, 0x4b800000, v50
	v_trunc_f32_e32 v50, v50
	v_mul_f32_e32 v51, 0x2f800000, v50
	v_floor_f32_e32 v51, v51
	v_fmac_f32_e32 v50, 0xcf800000, v51
	v_cvt_u32_f32_e32 v50, v50
	v_cvt_u32_f32_e32 v51, v51
	v_lshl_add_u64 v[52:53], v[66:67], 3, s[20:21]
	global_atomic_add_x2 v[52:53], v[50:51], off
.LBB0_1971:
	s_or_b64 exec, exec, s[46:47]
	v_add_u32_e32 v50, 0x90, v164
	s_waitcnt lgkmcnt(0)
	v_ashrrev_i32_e32 v51, 31, v50
	v_lshlrev_b64 v[52:53], 11, v[50:51]
	v_lshl_add_u64 v[56:57], v[52:53], 0, v[162:163]
	v_lshl_add_u64 v[58:59], v[56:57], 1, s[30:31]
	s_nop 0
	v_mov_b32_e32 v60, 0
	v_mov_b32_e32 v61, 0
	v_lshl_add_u64 v[62:63], s[62:63], 0, v[56:57]
	v_or_b32_e32 v56, 0x80, v56
	v_lshl_add_u64 v[64:65], v[56:57], 1, s[30:31]
	s_waitcnt vmcnt(21)
	s_nop 1
	v_mov_b32_e32 v52, v204
	v_mov_b32_e32 v53, v205
	v_mov_b32_e32 v54, v206
	v_mov_b32_e32 v55, v207
	v_lshlrev_b32_e32 v66, 16, v52
	v_and_b32_e32 v67, 0xffff0000, v52
	v_lshlrev_b32_e32 v52, 16, v53
	v_and_b32_e32 v53, 0xffff0000, v53
	v_lshlrev_b32_e32 v68, 16, v54
	v_and_b32_e32 v69, 0xffff0000, v54
	v_lshlrev_b32_e32 v54, 16, v55
	v_and_b32_e32 v55, 0xffff0000, v55
	v_pk_add_f32 v[48:49], v[48:49], v[52:53]
	v_pk_add_f32 v[46:47], v[46:47], v[66:67]
	v_pk_add_f32 v[52:53], v[44:45], v[54:55]
	v_pk_add_f32 v[54:55], v[42:43], v[68:69]
	v_pk_mul_f32 v[44:45], v[94:95], v[46:47]
	v_pk_mul_f32 v[66:67], v[90:91], v[54:55]
	v_cvt_pk_fp8_f32 v60, v44, v45
	v_cvt_pk_fp8_f32 v61, v66, v67
	v_pk_mul_f32 v[44:45], v[96:97], v[48:49]
	v_pk_mul_f32 v[66:67], v[92:93], v[52:53]
	v_cvt_pk_fp8_f32 v60, v44, v45 op_sel:[0,0,1]
	v_cvt_pk_fp8_f32 v61, v66, v67 op_sel:[0,0,1]
	v_cvt_pk_bf16_f32 v42, v46, v47
	v_cvt_pk_bf16_f32 v43, v48, v49
	v_cvt_pk_bf16_f32 v44, v54, v55
	v_cvt_pk_bf16_f32 v45, v52, v53
	global_store_dwordx4 v[58:59], v[42:45], off
	global_store_dwordx2 v[62:63], v[60:61], off
	s_nop 0
	v_mul_f32_e32 v47, v47, v47
	v_mul_f32_e32 v49, v49, v49
	v_mul_f32_e32 v55, v55, v55
	v_fmac_f32_e32 v47, v46, v46
	v_fmac_f32_e32 v49, v48, v48
	v_mul_f32_e32 v53, v53, v53
	v_fmac_f32_e32 v55, v54, v54
	v_add_f32_e32 v46, v47, v49
	v_fmac_f32_e32 v53, v52, v52
	v_add_f32_e32 v46, v55, v46
	v_add_f32_e32 v52, v53, v46
	v_mov_b32_e32 v58, 0
	v_mov_b32_e32 v59, 0
	s_waitcnt vmcnt(20)
; __device__ __forceinline__ unsigned pk4_fp8(float a, float b, float c, float d) { int w = 0; w = __builtin_amdgcn_cvt_pk_fp8_f32(a, b, w, false); w = __builtin_amdgcn_cvt_pk_fp8_f32(c, d, w, true); return (unsigned)w; }
; __device__ __forceinline__ u32x4 pack8(f32x4 v0, f32x4 v1) { u32x4 w; w.x = cvt_pk_bf16(v0[0], v0[1]); w.y = cvt_pk_bf16(v0[2], v0[3]); w.z = cvt_pk_bf16(v1[0], v1[1]); w.w = cvt_pk_bf16(v1[2], v1[3]); return w; }
; template <class T> __device__ __forceinline__ void est(T* p, T v) { if constexpr (MK_EPI_NT != 0) __builtin_nontemporal_store(v, p); else *p = v; }
; __device__ __forceinline__ void unpack8(u32x4 w, f32x4& v0, f32x4& v1) { v0 = (f32x4){bf_lo(w.x), bf_hi(w.x), bf_lo(w.y), bf_hi(w.y)}; v1 = (f32x4){bf_lo(w.z), bf_hi(w.z), bf_lo(w.w), bf_hi(w.w)}; }
; __device__ __forceinline__ float sum8sq(f32x4 a, f32x4 b) { return (a[0] * a[0] + a[1] * a[1]) + (a[2] * a[2] + a[3] * a[3]) + (b[0] * b[0] + b[1] * b[1]) + (b[2] * b[2] + b[3] * b[3]); }
; __device__ __forceinline__ void row_atomic(ss_t* ss, int row, float sq, int fq) { sq += __shfl_xor(sq, 16); sq += __shfl_xor(sq, 32); if (fq == 0) atomicAdd(ss + row, ss_fix(sq)); }
;     __device__ __forceinline__ void operator()(AccT acc, const Unit& u, int wr, int wc, int fr, int fq) const {
;     ...
;             for (int m = 0; m < 4; ++m) { const int row = row0 + ai * 128 + m * 16; float sq = 0.f;
; #pragma unroll
;                 for (int bj = 0; bj < 2; ++bj) { const size_t o = (size_t)row * DM + col0 + bj * 128;
;                     f32x4 r0, r1; if constexpr (RIN16) unpack8(*(const u32x4*)((const bf16_t*)Xin + o), r0, r1); else { r0 = *(const f32x4*)((const float*)Xin + o); r1 = *(const f32x4*)((const float*)Xin + o + 4); }
;                     const f32x4 x0 = r0 + acc[ai][bj][m][0] * ascale, x1 = r1 + acc[ai][bj][m][1] * ascale;
;                     est((u32x4*)(Xout + o), (u32x4)pack8(x0, x1));
;                     const f32x4 y0 = x0 * gv[bj][0], y1 = x1 * gv[bj][1];
;                     if constexpr (F8OUT) est((u32x2*)((unsigned char*)XB + o), (u32x2)(u32x2){pk4_fp8(y0[0], y0[1], y0[2], y0[3]), pk4_fp8(y1[0], y1[1], y1[2], y1[3])});
;                     else est((u32x4*)((bf16_t*)XB + o), (u32x4)pack8(y0, y1));
;                     sq += sum8sq(x0, x1); }
;                 row_atomic(ss, row, sq, fq); }
	s_nop 1
	v_mov_b32_e32 v42, v208
	v_mov_b32_e32 v43, v209
	v_mov_b32_e32 v44, v210
	v_mov_b32_e32 v45, v211
	v_lshlrev_b32_e32 v46, 16, v42
	v_and_b32_e32 v47, 0xffff0000, v42
	v_lshlrev_b32_e32 v42, 16, v43
	v_and_b32_e32 v43, 0xffff0000, v43
	v_lshlrev_b32_e32 v48, 16, v44
	v_and_b32_e32 v49, 0xffff0000, v44
	v_lshlrev_b32_e32 v44, 16, v45
	v_and_b32_e32 v45, 0xffff0000, v45
	v_pk_add_f32 v[40:41], v[40:41], v[42:43]
	v_pk_add_f32 v[42:43], v[38:39], v[46:47]
	v_pk_add_f32 v[44:45], v[36:37], v[44:45]
	v_pk_add_f32 v[34:35], v[34:35], v[48:49]
	v_cvt_pk_bf16_f32 v36, v42, v43
	v_pk_mul_f32 v[46:47], v[78:79], v[42:43]
	v_mul_f32_e32 v39, v43, v43
	v_mul_f32_e32 v43, v41, v41
	v_cvt_pk_bf16_f32 v37, v40, v41
	v_cvt_pk_bf16_f32 v38, v34, v35
	v_pk_mul_f32 v[48:49], v[74:75], v[34:35]
	v_mul_f32_e32 v35, v35, v35
	v_fmac_f32_e32 v39, v42, v42
	v_fmac_f32_e32 v43, v40, v40
	v_mul_f32_e32 v53, v45, v45
	v_fmac_f32_e32 v35, v34, v34
	v_add_f32_e32 v34, v39, v43
	v_add_f32_e32 v34, v35, v34
	v_fmac_f32_e32 v53, v44, v44
	v_add_f32_e32 v34, v53, v34
	v_add_f32_e32 v39, v52, v34
	ds_bpermute_b32 v42, v138, v39
	v_cvt_pk_fp8_f32 v58, v46, v47
	v_cvt_pk_fp8_f32 v59, v48, v49
	v_pk_mul_f32 v[34:35], v[80:81], v[40:41]
	v_pk_mul_f32 v[40:41], v[76:77], v[44:45]
	v_cvt_pk_fp8_f32 v58, v34, v35 op_sel:[0,0,1]
	s_waitcnt lgkmcnt(0)
	v_add_f32_e32 v34, v39, v42
	ds_bpermute_b32 v35, v132, v34
	v_cvt_pk_fp8_f32 v59, v40, v41 op_sel:[0,0,1]
	v_cvt_pk_bf16_f32 v39, v44, v45
	global_store_dwordx4 v[64:65], v[36:39], off
	s_nop 1
	v_lshl_add_u64 v[36:37], s[62:63], 0, v[56:57]
	global_store_dwordx2 v[36:37], v[58:59], off
	s_and_saveexec_b64 s[46:47], s[0:1]
	s_cbranch_execz .LBB0_1973
	s_waitcnt lgkmcnt(0)
	v_add_f32_e32 v34, v34, v35
	v_mul_f32_e32 v34, 0x4b800000, v34
	v_trunc_f32_e32 v34, v34
	v_mul_f32_e32 v35, 0x2f800000, v34
	v_floor_f32_e32 v35, v35
	v_fmac_f32_e32 v34, 0xcf800000, v35
	v_cvt_u32_f32_e32 v34, v34
	v_cvt_u32_f32_e32 v35, v35
	v_lshl_add_u64 v[36:37], v[50:51], 3, s[20:21]
	global_atomic_add_x2 v[36:37], v[34:35], off
.LBB0_1973:
	s_or_b64 exec, exec, s[46:47]
	v_add_u32_e32 v34, 0xa0, v164
	s_waitcnt lgkmcnt(0)
	v_ashrrev_i32_e32 v35, 31, v34
	v_lshlrev_b64 v[36:37], 11, v[34:35]
	v_lshl_add_u64 v[40:41], v[36:37], 0, v[162:163]
	v_lshl_add_u64 v[42:43], v[40:41], 1, s[30:31]
	s_nop 0
	v_mov_b32_e32 v44, 0
	v_mov_b32_e32 v45, 0
	v_lshl_add_u64 v[46:47], s[62:63], 0, v[40:41]
	v_or_b32_e32 v40, 0x80, v40
	v_lshl_add_u64 v[48:49], v[40:41], 1, s[30:31]
	s_waitcnt vmcnt(19)
	s_nop 1
	v_mov_b32_e32 v36, v212
	v_mov_b32_e32 v37, v213
	v_mov_b32_e32 v38, v214
	v_mov_b32_e32 v39, v215
	v_lshlrev_b32_e32 v50, 16, v36
	v_and_b32_e32 v51, 0xffff0000, v36
	v_lshlrev_b32_e32 v36, 16, v37
	v_and_b32_e32 v37, 0xffff0000, v37
	v_lshlrev_b32_e32 v52, 16, v38
	v_and_b32_e32 v53, 0xffff0000, v38
	v_lshlrev_b32_e32 v38, 16, v39
	v_and_b32_e32 v39, 0xffff0000, v39
	v_pk_add_f32 v[32:33], v[32:33], v[36:37]
	v_pk_add_f32 v[30:31], v[30:31], v[50:51]
	v_pk_add_f32 v[36:37], v[28:29], v[38:39]
	v_pk_add_f32 v[38:39], v[26:27], v[52:53]
	v_pk_mul_f32 v[28:29], v[94:95], v[30:31]
	v_pk_mul_f32 v[50:51], v[90:91], v[38:39]
	v_cvt_pk_fp8_f32 v44, v28, v29
	v_cvt_pk_fp8_f32 v45, v50, v51
	v_pk_mul_f32 v[28:29], v[96:97], v[32:33]
	v_pk_mul_f32 v[50:51], v[92:93], v[36:37]
	v_cvt_pk_fp8_f32 v44, v28, v29 op_sel:[0,0,1]
	v_cvt_pk_fp8_f32 v45, v50, v51 op_sel:[0,0,1]
	v_cvt_pk_bf16_f32 v26, v30, v31
	v_cvt_pk_bf16_f32 v27, v32, v33
	v_cvt_pk_bf16_f32 v28, v38, v39
	v_cvt_pk_bf16_f32 v29, v36, v37
	global_store_dwordx4 v[42:43], v[26:29], off
	global_store_dwordx2 v[46:47], v[44:45], off
	s_nop 0
	v_mul_f32_e32 v31, v31, v31
	v_mul_f32_e32 v33, v33, v33
	v_mul_f32_e32 v39, v39, v39
	v_fmac_f32_e32 v31, v30, v30
	v_fmac_f32_e32 v33, v32, v32
	v_mul_f32_e32 v37, v37, v37
	v_fmac_f32_e32 v39, v38, v38
	v_add_f32_e32 v30, v31, v33
	v_fmac_f32_e32 v37, v36, v36
	v_add_f32_e32 v30, v39, v30
	v_add_f32_e32 v36, v37, v30
	v_mov_b32_e32 v42, 0
	v_mov_b32_e32 v43, 0
	s_waitcnt vmcnt(18)
	s_nop 1
	v_mov_b32_e32 v26, v216
	v_mov_b32_e32 v27, v217
	v_mov_b32_e32 v28, v218
	v_mov_b32_e32 v29, v219
	v_lshlrev_b32_e32 v30, 16, v26
	v_and_b32_e32 v31, 0xffff0000, v26
	v_lshlrev_b32_e32 v26, 16, v27
	v_and_b32_e32 v27, 0xffff0000, v27
	v_lshlrev_b32_e32 v32, 16, v28
	v_and_b32_e32 v33, 0xffff0000, v28
	v_lshlrev_b32_e32 v28, 16, v29
	v_and_b32_e32 v29, 0xffff0000, v29
	v_pk_add_f32 v[24:25], v[24:25], v[26:27]
	v_pk_add_f32 v[26:27], v[22:23], v[30:31]
	v_pk_add_f32 v[28:29], v[20:21], v[28:29]
	v_pk_add_f32 v[18:19], v[18:19], v[32:33]
	v_cvt_pk_bf16_f32 v20, v26, v27
	v_pk_mul_f32 v[30:31], v[78:79], v[26:27]
	v_mul_f32_e32 v23, v27, v27
	v_mul_f32_e32 v27, v25, v25
	v_cvt_pk_bf16_f32 v21, v24, v25
	v_cvt_pk_bf16_f32 v22, v18, v19
	v_pk_mul_f32 v[32:33], v[74:75], v[18:19]
	v_mul_f32_e32 v19, v19, v19
	v_fmac_f32_e32 v23, v26, v26
	v_fmac_f32_e32 v27, v24, v24
	v_mul_f32_e32 v37, v29, v29
	v_fmac_f32_e32 v19, v18, v18
	v_add_f32_e32 v18, v23, v27
	v_add_f32_e32 v18, v19, v18
	v_fmac_f32_e32 v37, v28, v28
	v_add_f32_e32 v18, v37, v18
	v_add_f32_e32 v23, v36, v18
	ds_bpermute_b32 v26, v138, v23
	v_cvt_pk_fp8_f32 v42, v30, v31
	v_cvt_pk_fp8_f32 v43, v32, v33
	v_pk_mul_f32 v[18:19], v[80:81], v[24:25]
	v_pk_mul_f32 v[24:25], v[76:77], v[28:29]
	v_cvt_pk_fp8_f32 v42, v18, v19 op_sel:[0,0,1]
	s_waitcnt lgkmcnt(0)
	v_add_f32_e32 v18, v23, v26
	ds_bpermute_b32 v19, v132, v18
	v_cvt_pk_fp8_f32 v43, v24, v25 op_sel:[0,0,1]
	v_cvt_pk_bf16_f32 v23, v28, v29
	global_store_dwordx4 v[48:49], v[20:23], off
	s_nop 1
	v_lshl_add_u64 v[20:21], s[62:63], 0, v[40:41]
	global_store_dwordx2 v[20:21], v[42:43], off
	s_and_saveexec_b64 s[46:47], s[0:1]
	s_cbranch_execz .LBB0_1975
	s_waitcnt lgkmcnt(0)
	v_add_f32_e32 v18, v18, v19
	v_mul_f32_e32 v18, 0x4b800000, v18
	v_trunc_f32_e32 v18, v18
	v_mul_f32_e32 v19, 0x2f800000, v18
	v_floor_f32_e32 v19, v19
	v_fmac_f32_e32 v18, 0xcf800000, v19
	v_cvt_u32_f32_e32 v18, v18
	v_cvt_u32_f32_e32 v19, v19
	v_lshl_add_u64 v[20:21], v[34:35], 3, s[20:21]
	global_atomic_add_x2 v[20:21], v[18:19], off
; __device__ __forceinline__ unsigned pk4_fp8(float a, float b, float c, float d) { int w = 0; w = __builtin_amdgcn_cvt_pk_fp8_f32(a, b, w, false); w = __builtin_amdgcn_cvt_pk_fp8_f32(c, d, w, true); return (unsigned)w; }
; __device__ __forceinline__ u32x4 pack8(f32x4 v0, f32x4 v1) { u32x4 w; w.x = cvt_pk_bf16(v0[0], v0[1]); w.y = cvt_pk_bf16(v0[2], v0[3]); w.z = cvt_pk_bf16(v1[0], v1[1]); w.w = cvt_pk_bf16(v1[2], v1[3]); return w; }
; template <class T> __device__ __forceinline__ void est(T* p, T v) { if constexpr (MK_EPI_NT != 0) __builtin_nontemporal_store(v, p); else *p = v; }
; __device__ __forceinline__ void unpack8(u32x4 w, f32x4& v0, f32x4& v1) { v0 = (f32x4){bf_lo(w.x), bf_hi(w.x), bf_lo(w.y), bf_hi(w.y)}; v1 = (f32x4){bf_lo(w.z), bf_hi(w.z), bf_lo(w.w), bf_hi(w.w)}; }
; __device__ __forceinline__ float sum8sq(f32x4 a, f32x4 b) { return (a[0] * a[0] + a[1] * a[1]) + (a[2] * a[2] + a[3] * a[3]) + (b[0] * b[0] + b[1] * b[1]) + (b[2] * b[2] + b[3] * b[3]); }
; __device__ __forceinline__ void row_atomic(ss_t* ss, int row, float sq, int fq) { sq += __shfl_xor(sq, 16); sq += __shfl_xor(sq, 32); if (fq == 0) atomicAdd(ss + row, ss_fix(sq)); }
;     __device__ __forceinline__ void operator()(AccT acc, const Unit& u, int wr, int wc, int fr, int fq) const {
;     ...
;             for (int m = 0; m < 4; ++m) { const int row = row0 + ai * 128 + m * 16; float sq = 0.f;
; #pragma unroll
;                 for (int bj = 0; bj < 2; ++bj) { const size_t o = (size_t)row * DM + col0 + bj * 128;
;                     f32x4 r0, r1; if constexpr (RIN16) unpack8(*(const u32x4*)((const bf16_t*)Xin + o), r0, r1); else { r0 = *(const f32x4*)((const float*)Xin + o); r1 = *(const f32x4*)((const float*)Xin + o + 4); }
;                     const f32x4 x0 = r0 + acc[ai][bj][m][0] * ascale, x1 = r1 + acc[ai][bj][m][1] * ascale;
;                     est((u32x4*)(Xout + o), (u32x4)pack8(x0, x1));
;                     const f32x4 y0 = x0 * gv[bj][0], y1 = x1 * gv[bj][1];
;                     if constexpr (F8OUT) est((u32x2*)((unsigned char*)XB + o), (u32x2)(u32x2){pk4_fp8(y0[0], y0[1], y0[2], y0[3]), pk4_fp8(y1[0], y1[1], y1[2], y1[3])});
;                     else est((u32x4*)((bf16_t*)XB + o), (u32x4)pack8(y0, y1));
;                     sq += sum8sq(x0, x1); }
;                 row_atomic(ss, row, sq, fq); }
.LBB0_1975:
	s_or_b64 exec, exec, s[46:47]
	v_add_u32_e32 v18, 0xb0, v164
	s_waitcnt lgkmcnt(0)
	v_ashrrev_i32_e32 v19, 31, v18
	v_lshlrev_b64 v[20:21], 11, v[18:19]
	v_lshl_add_u64 v[24:25], v[20:21], 0, v[162:163]
	v_lshl_add_u64 v[26:27], v[24:25], 1, s[30:31]
	s_nop 0
	v_mov_b32_e32 v28, 0
	v_mov_b32_e32 v29, 0
	v_lshl_add_u64 v[30:31], s[62:63], 0, v[24:25]
	v_or_b32_e32 v24, 0x80, v24
	v_lshl_add_u64 v[32:33], v[24:25], 1, s[30:31]
	s_waitcnt vmcnt(17)
	s_nop 1
	v_mov_b32_e32 v20, v220
	v_mov_b32_e32 v21, v221
	v_mov_b32_e32 v22, v222
	v_mov_b32_e32 v23, v223
	v_lshlrev_b32_e32 v34, 16, v20
	v_and_b32_e32 v35, 0xffff0000, v20
	v_lshlrev_b32_e32 v20, 16, v21
	v_and_b32_e32 v21, 0xffff0000, v21
	v_lshlrev_b32_e32 v36, 16, v22
	v_and_b32_e32 v37, 0xffff0000, v22
	v_lshlrev_b32_e32 v22, 16, v23
	v_and_b32_e32 v23, 0xffff0000, v23
	v_pk_add_f32 v[16:17], v[16:17], v[20:21]
	v_pk_add_f32 v[14:15], v[14:15], v[34:35]
	v_pk_add_f32 v[20:21], v[12:13], v[22:23]
	v_pk_add_f32 v[22:23], v[10:11], v[36:37]
	v_pk_mul_f32 v[12:13], v[94:95], v[14:15]
	v_pk_mul_f32 v[34:35], v[90:91], v[22:23]
	v_cvt_pk_fp8_f32 v28, v12, v13
	v_cvt_pk_fp8_f32 v29, v34, v35
	v_pk_mul_f32 v[12:13], v[96:97], v[16:17]
	v_pk_mul_f32 v[34:35], v[92:93], v[20:21]
	v_cvt_pk_fp8_f32 v28, v12, v13 op_sel:[0,0,1]
	v_cvt_pk_fp8_f32 v29, v34, v35 op_sel:[0,0,1]
	v_cvt_pk_bf16_f32 v10, v14, v15
	v_cvt_pk_bf16_f32 v11, v16, v17
	v_cvt_pk_bf16_f32 v12, v22, v23
	v_cvt_pk_bf16_f32 v13, v20, v21
	global_store_dwordx4 v[26:27], v[10:13], off
	global_store_dwordx2 v[30:31], v[28:29], off
	s_nop 0
	v_mul_f32_e32 v15, v15, v15
	v_mul_f32_e32 v17, v17, v17
	v_mul_f32_e32 v23, v23, v23
	v_fmac_f32_e32 v15, v14, v14
	v_fmac_f32_e32 v17, v16, v16
	v_mul_f32_e32 v21, v21, v21
	v_fmac_f32_e32 v23, v22, v22
	v_add_f32_e32 v14, v15, v17
	v_fmac_f32_e32 v21, v20, v20
	v_add_f32_e32 v14, v23, v14
	v_add_f32_e32 v20, v21, v14
	v_mov_b32_e32 v26, 0
	v_mov_b32_e32 v27, 0
	s_waitcnt vmcnt(16)
	s_nop 1
	v_mov_b32_e32 v10, v248
	v_mov_b32_e32 v11, v249
	v_mov_b32_e32 v12, v250
	v_mov_b32_e32 v13, v251
	v_lshlrev_b32_e32 v14, 16, v10
	v_and_b32_e32 v15, 0xffff0000, v10
	v_lshlrev_b32_e32 v10, 16, v11
	v_and_b32_e32 v11, 0xffff0000, v11
	v_lshlrev_b32_e32 v16, 16, v12
	v_and_b32_e32 v17, 0xffff0000, v12
	v_lshlrev_b32_e32 v12, 16, v13
	v_and_b32_e32 v13, 0xffff0000, v13
	v_pk_add_f32 v[8:9], v[8:9], v[10:11]
	v_pk_add_f32 v[10:11], v[6:7], v[14:15]
	v_pk_add_f32 v[12:13], v[4:5], v[12:13]
	v_pk_add_f32 v[2:3], v[2:3], v[16:17]
	v_cvt_pk_bf16_f32 v4, v10, v11
	v_pk_mul_f32 v[14:15], v[78:79], v[10:11]
	v_mul_f32_e32 v7, v11, v11
	v_mul_f32_e32 v11, v9, v9
	v_cvt_pk_bf16_f32 v5, v8, v9
	v_cvt_pk_bf16_f32 v6, v2, v3
	v_pk_mul_f32 v[16:17], v[74:75], v[2:3]
	v_mul_f32_e32 v3, v3, v3
	v_fmac_f32_e32 v7, v10, v10
	v_fmac_f32_e32 v11, v8, v8
	v_mul_f32_e32 v21, v13, v13
	v_fmac_f32_e32 v3, v2, v2
	v_add_f32_e32 v2, v7, v11
	v_add_f32_e32 v2, v3, v2
	v_fmac_f32_e32 v21, v12, v12
	v_add_f32_e32 v2, v21, v2
	v_add_f32_e32 v7, v20, v2
	ds_bpermute_b32 v10, v138, v7
	v_cvt_pk_fp8_f32 v26, v14, v15
	v_cvt_pk_fp8_f32 v27, v16, v17
	v_pk_mul_f32 v[2:3], v[80:81], v[8:9]
	v_pk_mul_f32 v[8:9], v[76:77], v[12:13]
	v_cvt_pk_fp8_f32 v26, v2, v3 op_sel:[0,0,1]
	s_waitcnt lgkmcnt(0)
	v_add_f32_e32 v2, v7, v10
	ds_bpermute_b32 v3, v132, v2
	v_cvt_pk_fp8_f32 v27, v8, v9 op_sel:[0,0,1]
	v_cvt_pk_bf16_f32 v7, v12, v13
	global_store_dwordx4 v[32:33], v[4:7], off
	s_nop 1
	v_lshl_add_u64 v[4:5], s[62:63], 0, v[24:25]
	global_store_dwordx2 v[4:5], v[26:27], off
	s_and_saveexec_b64 s[46:47], s[0:1]
	s_cbranch_execz .LBB0_1977
	s_waitcnt lgkmcnt(0)
	v_add_f32_e32 v2, v2, v3
	v_mul_f32_e32 v2, 0x4b800000, v2
	v_trunc_f32_e32 v2, v2
	v_mul_f32_e32 v3, 0x2f800000, v2
	v_floor_f32_e32 v3, v3
	v_fmac_f32_e32 v2, 0xcf800000, v3
	v_cvt_u32_f32_e32 v2, v2
	v_cvt_u32_f32_e32 v3, v3
	v_lshl_add_u64 v[4:5], v[18:19], 3, s[20:21]
	global_atomic_add_x2 v[4:5], v[2:3], off
